# LDS-DMA loads of all 7 GEMM K-loops use the SADDR form (SGPR base + 32-bit lane offset): 16 v_lshl_add_u64 per loop body removed from the load slots (P15: 7 of 14)
# baseline (speedup 1.0000x reference)
.LBB0_710:
	s_add_u32 s46, s46, 0x20080
	s_addc_u32 s47, s47, 0
	s_add_u32 s37, s52, 0x100
	s_addc_u32 s39, s53, 0
	s_mov_b32 s79, -2
	ds_read_b128 v[18:21], v192
	ds_read_b128 v[22:25], v192 offset:1024
	ds_read_b128 v[26:29], v192 offset:2048
	ds_read_b128 v[30:33], v192 offset:3072
	ds_read_b128 v[2:5], v193
	ds_read_b128 v[6:9], v193 offset:1024
	ds_read_b128 v[10:13], v193 offset:2048
	ds_read_b128 v[14:17], v193 offset:3072
	s_add_u32 s52, s46, 0xfffe0080
	s_addc_u32 s53, s47, -1
	s_cmp_eq_u32 s79, 4
	s_cselect_b32 s55, s41, s53
	s_cselect_b32 s54, s40, s52
	s_cselect_b32 s53, s43, s39
	s_cselect_b32 s52, s42, s37
	s_add_i32 m0, s35, 0xc000
	ds_read_b128 v[182:185], v194
	ds_read_b128 v[186:189], v194 offset:1024
	ds_read_b128 v[196:199], v194 offset:2048
	ds_read_b128 v[200:203], v194 offset:3072
	ds_read_b128 v[204:207], v194 offset:4096
	ds_read_b128 v[208:211], v194 offset:5120
	ds_read_b128 v[212:215], v194 offset:6144
	ds_read_b128 v[216:219], v194 offset:7168
	global_load_lds_dwordx4 v174, s[46:47]
	s_add_i32 m0, s35, 0xe000
	s_nop 0
	global_load_lds_dwordx4 v176, s[46:47]
	s_waitcnt vmcnt(8)
	s_waitcnt lgkmcnt(0)
	s_barrier
	s_setprio 1
	s_waitcnt lgkmcnt(0)
	v_mfma_f32_16x16x128_f8f6f4 v[158:161], v[18:25], v[182:189], 0
	v_mfma_f32_16x16x128_f8f6f4 v[150:153], v[26:33], v[182:189], 0
	v_mfma_f32_16x16x128_f8f6f4 v[142:145], v[18:25], v[196:203], 0
	v_mfma_f32_16x16x128_f8f6f4 v[134:137], v[26:33], v[196:203], 0
	v_mfma_f32_16x16x128_f8f6f4 v[126:129], v[18:25], v[204:211], 0
	v_mfma_f32_16x16x128_f8f6f4 v[118:121], v[26:33], v[204:211], 0
	v_mfma_f32_16x16x128_f8f6f4 v[110:113], v[18:25], v[212:219], 0
	v_mfma_f32_16x16x128_f8f6f4 v[102:105], v[26:33], v[212:219], 0
	s_setprio 0
	s_setprio 1
	v_mfma_f32_16x16x128_f8f6f4 v[154:157], v[2:9], v[182:189], 0
	v_mfma_f32_16x16x128_f8f6f4 v[146:149], v[10:17], v[182:189], 0
	v_mfma_f32_16x16x128_f8f6f4 v[138:141], v[2:9], v[196:203], 0
	v_mfma_f32_16x16x128_f8f6f4 v[130:133], v[10:17], v[196:203], 0
	v_mfma_f32_16x16x128_f8f6f4 v[122:125], v[2:9], v[204:211], 0
	v_mfma_f32_16x16x128_f8f6f4 v[114:117], v[10:17], v[204:211], 0
	v_mfma_f32_16x16x128_f8f6f4 v[106:109], v[2:9], v[212:219], 0
	v_mfma_f32_16x16x128_f8f6f4 v[98:101], v[10:17], v[212:219], 0
	s_setprio 0
	s_barrier
	s_add_i32 s76, s66, s31
	s_mov_b64 s[98:99], s[52:53]
	s_mov_b32 m0, s76
	ds_read_b128 v[196:199], v194 offset:16384
	ds_read_b128 v[200:203], v194 offset:17408
	ds_read_b128 v[204:207], v194 offset:18432
	ds_read_b128 v[208:211], v194 offset:19456
	ds_read_b128 v[212:215], v194 offset:20480
	ds_read_b128 v[216:219], v194 offset:21504
	ds_read_b128 v[220:223], v194 offset:22528
	ds_read_b128 v[224:227], v194 offset:23552
	global_load_lds_dwordx4 v168, s[98:99]
	s_add_i32 m0, s76, 0x2000
	s_add_u32 s80, s52, 0x20000
	s_addc_u32 s81, s53, 0
	s_add_i32 s76, s67, s31
	global_load_lds_dwordx4 v164, s[98:99]
	s_mov_b32 m0, s76
	s_mov_b64 s[100:101], s[54:55]
	global_load_lds_dwordx4 v168, s[80:81]
	s_add_i32 m0, s76, 0x2000
	s_nop 0
	global_load_lds_dwordx4 v164, s[80:81]
	s_mov_b32 m0, s35
	s_nop 0
	global_load_lds_dwordx4 v172, s[100:101]
	s_mov_b32 m0, s45
	s_nop 0
	global_load_lds_dwordx4 v166, s[100:101]
	s_waitcnt vmcnt(8)
	s_waitcnt lgkmcnt(0)
	s_barrier
	s_setprio 1
	s_waitcnt lgkmcnt(0)
	v_mfma_f32_16x16x128_f8f6f4 v[94:97], v[18:25], v[196:203], 0
	v_mfma_f32_16x16x128_f8f6f4 v[86:89], v[26:33], v[196:203], 0
	v_mfma_f32_16x16x128_f8f6f4 v[78:81], v[18:25], v[204:211], 0
	v_mfma_f32_16x16x128_f8f6f4 v[70:73], v[26:33], v[204:211], 0
	v_mfma_f32_16x16x128_f8f6f4 v[62:65], v[18:25], v[212:219], 0
	v_mfma_f32_16x16x128_f8f6f4 v[54:57], v[26:33], v[212:219], 0
	v_mfma_f32_16x16x128_f8f6f4 v[46:49], v[18:25], v[220:227], 0
	v_mfma_f32_16x16x128_f8f6f4 v[38:41], v[26:33], v[220:227], 0
	s_setprio 0
	s_setprio 1
	v_mfma_f32_16x16x128_f8f6f4 v[90:93], v[2:9], v[196:203], 0
	v_mfma_f32_16x16x128_f8f6f4 v[82:85], v[10:17], v[196:203], 0
	v_mfma_f32_16x16x128_f8f6f4 v[74:77], v[2:9], v[204:211], 0
	v_mfma_f32_16x16x128_f8f6f4 v[66:69], v[10:17], v[204:211], 0
	v_mfma_f32_16x16x128_f8f6f4 v[58:61], v[2:9], v[212:219], 0
	v_mfma_f32_16x16x128_f8f6f4 v[50:53], v[10:17], v[212:219], 0
	v_mfma_f32_16x16x128_f8f6f4 v[42:45], v[2:9], v[220:227], 0
	v_mfma_f32_16x16x128_f8f6f4 v[34:37], v[10:17], v[220:227], 0
	s_setprio 0
	s_barrier
	s_add_i32 s76, 0, 0x18000
	s_add_i32 s80, 0, 0x1c000
	v_add_u32_e32 v14, s76, v171
	v_add_u32_e32 v30, s80, v171
	ds_read_b128 v[2:5], v14
	ds_read_b128 v[6:9], v14 offset:1024
	ds_read_b128 v[10:13], v14 offset:2048
	ds_read_b128 v[14:17], v14 offset:3072
	ds_read_b128 v[18:21], v30
	ds_read_b128 v[22:25], v30 offset:1024
	ds_read_b128 v[26:29], v30 offset:2048
	ds_read_b128 v[30:33], v30 offset:3072
	s_add_u32 s54, s54, 0x20000
	s_addc_u32 s55, s55, 0
	s_mov_b32 m0, s56
	ds_read_b128 v[196:199], v194 offset:32768
	ds_read_b128 v[200:203], v194 offset:33792
	ds_read_b128 v[204:207], v194 offset:34816
	ds_read_b128 v[208:211], v194 offset:35840
	ds_read_b128 v[212:215], v194 offset:36864
	ds_read_b128 v[216:219], v194 offset:37888
	ds_read_b128 v[220:223], v194 offset:38912
	ds_read_b128 v[224:227], v194 offset:39936
	global_load_lds_dwordx4 v172, s[54:55]
	s_mov_b32 m0, s57
	s_nop 0
	global_load_lds_dwordx4 v166, s[54:55]
	s_waitcnt vmcnt(8)
	s_waitcnt lgkmcnt(0)
	s_barrier
	s_setprio 1
	s_waitcnt lgkmcnt(0)
	v_mfma_f32_16x16x128_f8f6f4 v[158:161], v[2:9], v[196:203], v[158:161]
	v_mfma_f32_16x16x128_f8f6f4 v[150:153], v[10:17], v[196:203], v[150:153]
	v_mfma_f32_16x16x128_f8f6f4 v[142:145], v[2:9], v[204:211], v[142:145]
	v_mfma_f32_16x16x128_f8f6f4 v[134:137], v[10:17], v[204:211], v[134:137]
	v_mfma_f32_16x16x128_f8f6f4 v[126:129], v[2:9], v[212:219], v[126:129]
	v_mfma_f32_16x16x128_f8f6f4 v[118:121], v[10:17], v[212:219], v[118:121]
	v_mfma_f32_16x16x128_f8f6f4 v[110:113], v[2:9], v[220:227], v[110:113]
	v_mfma_f32_16x16x128_f8f6f4 v[102:105], v[10:17], v[220:227], v[102:105]
	s_setprio 0
	s_setprio 1
	v_mfma_f32_16x16x128_f8f6f4 v[154:157], v[18:25], v[196:203], v[154:157]
	v_mfma_f32_16x16x128_f8f6f4 v[146:149], v[26:33], v[196:203], v[146:149]
	v_mfma_f32_16x16x128_f8f6f4 v[138:141], v[18:25], v[204:211], v[138:141]
	v_mfma_f32_16x16x128_f8f6f4 v[130:133], v[26:33], v[204:211], v[130:133]
	v_mfma_f32_16x16x128_f8f6f4 v[122:125], v[18:25], v[212:219], v[122:125]
	v_mfma_f32_16x16x128_f8f6f4 v[114:117], v[26:33], v[212:219], v[114:117]
	v_mfma_f32_16x16x128_f8f6f4 v[106:109], v[18:25], v[220:227], v[106:109]
	v_mfma_f32_16x16x128_f8f6f4 v[98:101], v[26:33], v[220:227], v[98:101]
	s_setprio 0
	s_barrier
	s_add_i32 s54, s76, s31
	s_mov_b32 m0, s54
	ds_read_b128 v[196:199], v194 offset:49152
	ds_read_b128 v[200:203], v194 offset:50176
	ds_read_b128 v[204:207], v194 offset:51200
	ds_read_b128 v[208:211], v194 offset:52224
	ds_read_b128 v[212:215], v194 offset:53248
	ds_read_b128 v[216:219], v194 offset:54272
	ds_read_b128 v[220:223], v194 offset:55296
	ds_read_b128 v[224:227], v194 offset:56320
	s_add_u32 s98, s98, 0x80
	s_addc_u32 s99, s99, 0
	global_load_lds_dwordx4 v168, s[98:99]
	s_add_i32 m0, s54, 0x2000
	s_add_u32 s52, s52, 0x20080
	s_addc_u32 s53, s53, 0
	s_add_i32 s54, s80, s31
	global_load_lds_dwordx4 v164, s[98:99]
	s_mov_b32 m0, s54
	s_nop 0
	global_load_lds_dwordx4 v168, s[52:53]
	s_add_i32 m0, s54, 0x2000
	s_nop 0
	global_load_lds_dwordx4 v164, s[52:53]
	s_mov_b32 m0, s59
	s_nop 0
	s_add_u32 s100, s100, 0x80
	s_addc_u32 s101, s101, 0
	global_load_lds_dwordx4 v172, s[100:101]
	s_mov_b32 m0, s60
	s_nop 0
	global_load_lds_dwordx4 v166, s[100:101]
	s_waitcnt vmcnt(8)
	s_waitcnt lgkmcnt(0)
	s_barrier
	s_setprio 1
	s_waitcnt lgkmcnt(0)
	v_mfma_f32_16x16x128_f8f6f4 v[94:97], v[2:9], v[196:203], v[94:97]
	v_mfma_f32_16x16x128_f8f6f4 v[86:89], v[10:17], v[196:203], v[86:89]
	v_mfma_f32_16x16x128_f8f6f4 v[78:81], v[2:9], v[204:211], v[78:81]
	v_mfma_f32_16x16x128_f8f6f4 v[70:73], v[10:17], v[204:211], v[70:73]
	v_mfma_f32_16x16x128_f8f6f4 v[62:65], v[2:9], v[212:219], v[62:65]
	v_mfma_f32_16x16x128_f8f6f4 v[54:57], v[10:17], v[212:219], v[54:57]
	v_mfma_f32_16x16x128_f8f6f4 v[46:49], v[2:9], v[220:227], v[46:49]
	v_mfma_f32_16x16x128_f8f6f4 v[38:41], v[10:17], v[220:227], v[38:41]
	s_setprio 0
	s_setprio 1
	v_mfma_f32_16x16x128_f8f6f4 v[90:93], v[18:25], v[196:203], v[90:93]
	v_mfma_f32_16x16x128_f8f6f4 v[82:85], v[26:33], v[196:203], v[82:85]
	v_mfma_f32_16x16x128_f8f6f4 v[74:77], v[18:25], v[204:211], v[74:77]
	v_mfma_f32_16x16x128_f8f6f4 v[66:69], v[26:33], v[204:211], v[66:69]
	v_mfma_f32_16x16x128_f8f6f4 v[58:61], v[18:25], v[212:219], v[58:61]
	v_mfma_f32_16x16x128_f8f6f4 v[50:53], v[26:33], v[212:219], v[50:53]
	v_mfma_f32_16x16x128_f8f6f4 v[42:45], v[18:25], v[220:227], v[42:45]
	v_mfma_f32_16x16x128_f8f6f4 v[34:37], v[26:33], v[220:227], v[34:37]
	s_setprio 0
	s_barrier
	s_add_i32 s79, s79, 2
	s_add_u32 s46, s46, 0x100
	s_addc_u32 s47, s47, 0
	s_add_u32 s37, s37, 0x100
	s_addc_u32 s39, s39, 0
	s_cmp_gt_u32 s79, 5
.LBB0_711:
	ds_read_b128 v[18:21], v192
	ds_read_b128 v[22:25], v192 offset:1024
	ds_read_b128 v[26:29], v192 offset:2048
	ds_read_b128 v[30:33], v192 offset:3072
	ds_read_b128 v[2:5], v193
	ds_read_b128 v[6:9], v193 offset:1024
	ds_read_b128 v[10:13], v193 offset:2048
	ds_read_b128 v[14:17], v193 offset:3072
	s_add_u32 s52, s46, 0xfffe0080
	s_addc_u32 s53, s47, -1
	s_cmp_eq_u32 s79, 4
	s_cselect_b32 s55, s41, s53
	s_cselect_b32 s54, s40, s52
	s_cselect_b32 s53, s43, s39
	s_cselect_b32 s52, s42, s37
	s_add_i32 m0, s35, 0xc000
	ds_read_b128 v[182:185], v194
	ds_read_b128 v[186:189], v194 offset:1024
	ds_read_b128 v[196:199], v194 offset:2048
	ds_read_b128 v[200:203], v194 offset:3072
	ds_read_b128 v[204:207], v194 offset:4096
	ds_read_b128 v[208:211], v194 offset:5120
	ds_read_b128 v[212:215], v194 offset:6144
	ds_read_b128 v[216:219], v194 offset:7168
	global_load_lds_dwordx4 v174, s[46:47]
	s_add_i32 m0, s35, 0xe000
	s_nop 0
	global_load_lds_dwordx4 v176, s[46:47]
	s_waitcnt vmcnt(8)
	s_waitcnt lgkmcnt(0)
	s_barrier
	s_setprio 1
	s_waitcnt lgkmcnt(0)
	v_mfma_f32_16x16x128_f8f6f4 v[158:161], v[18:25], v[182:189], v[158:161]
	v_mfma_f32_16x16x128_f8f6f4 v[150:153], v[26:33], v[182:189], v[150:153]
	v_mfma_f32_16x16x128_f8f6f4 v[142:145], v[18:25], v[196:203], v[142:145]
	v_mfma_f32_16x16x128_f8f6f4 v[134:137], v[26:33], v[196:203], v[134:137]
	v_mfma_f32_16x16x128_f8f6f4 v[126:129], v[18:25], v[204:211], v[126:129]
	v_mfma_f32_16x16x128_f8f6f4 v[118:121], v[26:33], v[204:211], v[118:121]
	v_mfma_f32_16x16x128_f8f6f4 v[110:113], v[18:25], v[212:219], v[110:113]
	v_mfma_f32_16x16x128_f8f6f4 v[102:105], v[26:33], v[212:219], v[102:105]
	s_setprio 0
	s_setprio 1
	v_mfma_f32_16x16x128_f8f6f4 v[154:157], v[2:9], v[182:189], v[154:157]
	v_mfma_f32_16x16x128_f8f6f4 v[146:149], v[10:17], v[182:189], v[146:149]
	v_mfma_f32_16x16x128_f8f6f4 v[138:141], v[2:9], v[196:203], v[138:141]
	v_mfma_f32_16x16x128_f8f6f4 v[130:133], v[10:17], v[196:203], v[130:133]
	v_mfma_f32_16x16x128_f8f6f4 v[122:125], v[2:9], v[204:211], v[122:125]
	v_mfma_f32_16x16x128_f8f6f4 v[114:117], v[10:17], v[204:211], v[114:117]
	v_mfma_f32_16x16x128_f8f6f4 v[106:109], v[2:9], v[212:219], v[106:109]
	v_mfma_f32_16x16x128_f8f6f4 v[98:101], v[10:17], v[212:219], v[98:101]
	s_setprio 0
	s_barrier
	s_add_i32 s76, s66, s31
	s_mov_b64 s[98:99], s[52:53]
	s_mov_b32 m0, s76
	ds_read_b128 v[196:199], v194 offset:16384
	ds_read_b128 v[200:203], v194 offset:17408
	ds_read_b128 v[204:207], v194 offset:18432
	ds_read_b128 v[208:211], v194 offset:19456
	ds_read_b128 v[212:215], v194 offset:20480
	ds_read_b128 v[216:219], v194 offset:21504
	ds_read_b128 v[220:223], v194 offset:22528
	ds_read_b128 v[224:227], v194 offset:23552
	global_load_lds_dwordx4 v168, s[98:99]
	s_add_i32 m0, s76, 0x2000
	s_add_u32 s80, s52, 0x20000
	s_addc_u32 s81, s53, 0
	s_add_i32 s76, s67, s31
	global_load_lds_dwordx4 v164, s[98:99]
	s_mov_b32 m0, s76
	s_mov_b64 s[100:101], s[54:55]
	global_load_lds_dwordx4 v168, s[80:81]
	s_add_i32 m0, s76, 0x2000
	s_nop 0
	global_load_lds_dwordx4 v164, s[80:81]
	s_mov_b32 m0, s35
	s_nop 0
	global_load_lds_dwordx4 v172, s[100:101]
	s_mov_b32 m0, s45
	s_nop 0
	global_load_lds_dwordx4 v166, s[100:101]
	s_waitcnt vmcnt(8)
	s_waitcnt lgkmcnt(0)
	s_barrier
	s_setprio 1
	s_waitcnt lgkmcnt(0)
	v_mfma_f32_16x16x128_f8f6f4 v[94:97], v[18:25], v[196:203], v[94:97]
	v_mfma_f32_16x16x128_f8f6f4 v[86:89], v[26:33], v[196:203], v[86:89]
	v_mfma_f32_16x16x128_f8f6f4 v[78:81], v[18:25], v[204:211], v[78:81]
	v_mfma_f32_16x16x128_f8f6f4 v[70:73], v[26:33], v[204:211], v[70:73]
	v_mfma_f32_16x16x128_f8f6f4 v[62:65], v[18:25], v[212:219], v[62:65]
	v_mfma_f32_16x16x128_f8f6f4 v[54:57], v[26:33], v[212:219], v[54:57]
	v_mfma_f32_16x16x128_f8f6f4 v[46:49], v[18:25], v[220:227], v[46:49]
	v_mfma_f32_16x16x128_f8f6f4 v[38:41], v[26:33], v[220:227], v[38:41]
	s_setprio 0
	s_setprio 1
	v_mfma_f32_16x16x128_f8f6f4 v[90:93], v[2:9], v[196:203], v[90:93]
	v_mfma_f32_16x16x128_f8f6f4 v[82:85], v[10:17], v[196:203], v[82:85]
	v_mfma_f32_16x16x128_f8f6f4 v[74:77], v[2:9], v[204:211], v[74:77]
	v_mfma_f32_16x16x128_f8f6f4 v[66:69], v[10:17], v[204:211], v[66:69]
	v_mfma_f32_16x16x128_f8f6f4 v[58:61], v[2:9], v[212:219], v[58:61]
	v_mfma_f32_16x16x128_f8f6f4 v[50:53], v[10:17], v[212:219], v[50:53]
	v_mfma_f32_16x16x128_f8f6f4 v[42:45], v[2:9], v[220:227], v[42:45]
	v_mfma_f32_16x16x128_f8f6f4 v[34:37], v[10:17], v[220:227], v[34:37]
	s_setprio 0
	s_barrier
	s_add_i32 s76, 0, 0x18000
	s_add_i32 s80, 0, 0x1c000
	v_add_u32_e32 v14, s76, v171
	v_add_u32_e32 v30, s80, v171
	ds_read_b128 v[2:5], v14
	ds_read_b128 v[6:9], v14 offset:1024
	ds_read_b128 v[10:13], v14 offset:2048
	ds_read_b128 v[14:17], v14 offset:3072
	ds_read_b128 v[18:21], v30
	ds_read_b128 v[22:25], v30 offset:1024
	ds_read_b128 v[26:29], v30 offset:2048
	ds_read_b128 v[30:33], v30 offset:3072
	s_add_u32 s54, s54, 0x20000
	s_addc_u32 s55, s55, 0
	s_mov_b32 m0, s56
	ds_read_b128 v[196:199], v194 offset:32768
	ds_read_b128 v[200:203], v194 offset:33792
	ds_read_b128 v[204:207], v194 offset:34816
	ds_read_b128 v[208:211], v194 offset:35840
	ds_read_b128 v[212:215], v194 offset:36864
	ds_read_b128 v[216:219], v194 offset:37888
	ds_read_b128 v[220:223], v194 offset:38912
	ds_read_b128 v[224:227], v194 offset:39936
	global_load_lds_dwordx4 v172, s[54:55]
	s_mov_b32 m0, s57
	s_nop 0
	global_load_lds_dwordx4 v166, s[54:55]
	s_waitcnt vmcnt(8)
	s_waitcnt lgkmcnt(0)
	s_barrier
	s_setprio 1
	s_waitcnt lgkmcnt(0)
	v_mfma_f32_16x16x128_f8f6f4 v[158:161], v[2:9], v[196:203], v[158:161]
	v_mfma_f32_16x16x128_f8f6f4 v[150:153], v[10:17], v[196:203], v[150:153]
	v_mfma_f32_16x16x128_f8f6f4 v[142:145], v[2:9], v[204:211], v[142:145]
	v_mfma_f32_16x16x128_f8f6f4 v[134:137], v[10:17], v[204:211], v[134:137]
	v_mfma_f32_16x16x128_f8f6f4 v[126:129], v[2:9], v[212:219], v[126:129]
	v_mfma_f32_16x16x128_f8f6f4 v[118:121], v[10:17], v[212:219], v[118:121]
	v_mfma_f32_16x16x128_f8f6f4 v[110:113], v[2:9], v[220:227], v[110:113]
	v_mfma_f32_16x16x128_f8f6f4 v[102:105], v[10:17], v[220:227], v[102:105]
	s_setprio 0
	s_setprio 1
	v_mfma_f32_16x16x128_f8f6f4 v[154:157], v[18:25], v[196:203], v[154:157]
	v_mfma_f32_16x16x128_f8f6f4 v[146:149], v[26:33], v[196:203], v[146:149]
	v_mfma_f32_16x16x128_f8f6f4 v[138:141], v[18:25], v[204:211], v[138:141]
	v_mfma_f32_16x16x128_f8f6f4 v[130:133], v[26:33], v[204:211], v[130:133]
	v_mfma_f32_16x16x128_f8f6f4 v[122:125], v[18:25], v[212:219], v[122:125]
	v_mfma_f32_16x16x128_f8f6f4 v[114:117], v[26:33], v[212:219], v[114:117]
	v_mfma_f32_16x16x128_f8f6f4 v[106:109], v[18:25], v[220:227], v[106:109]
	v_mfma_f32_16x16x128_f8f6f4 v[98:101], v[26:33], v[220:227], v[98:101]
	s_setprio 0
	s_barrier
	s_add_i32 s54, s76, s31
	s_mov_b32 m0, s54
	ds_read_b128 v[196:199], v194 offset:49152
	ds_read_b128 v[200:203], v194 offset:50176
	ds_read_b128 v[204:207], v194 offset:51200
	ds_read_b128 v[208:211], v194 offset:52224
	ds_read_b128 v[212:215], v194 offset:53248
	ds_read_b128 v[216:219], v194 offset:54272
	ds_read_b128 v[220:223], v194 offset:55296
	ds_read_b128 v[224:227], v194 offset:56320
	s_add_u32 s98, s98, 0x80
	s_addc_u32 s99, s99, 0
	global_load_lds_dwordx4 v168, s[98:99]
	s_add_i32 m0, s54, 0x2000
	s_add_u32 s52, s52, 0x20080
	s_addc_u32 s53, s53, 0
	s_add_i32 s54, s80, s31
	global_load_lds_dwordx4 v164, s[98:99]
	s_mov_b32 m0, s54
	s_nop 0
	global_load_lds_dwordx4 v168, s[52:53]
	s_add_i32 m0, s54, 0x2000
	s_nop 0
	global_load_lds_dwordx4 v164, s[52:53]
	s_mov_b32 m0, s59
	s_nop 0
	s_add_u32 s100, s100, 0x80
	s_addc_u32 s101, s101, 0
	global_load_lds_dwordx4 v172, s[100:101]
	s_mov_b32 m0, s60
	s_nop 0
	global_load_lds_dwordx4 v166, s[100:101]
	s_waitcnt vmcnt(8)
	s_waitcnt lgkmcnt(0)
	s_barrier
	s_setprio 1
	s_waitcnt lgkmcnt(0)
	v_mfma_f32_16x16x128_f8f6f4 v[94:97], v[2:9], v[196:203], v[94:97]
	v_mfma_f32_16x16x128_f8f6f4 v[86:89], v[10:17], v[196:203], v[86:89]
	v_mfma_f32_16x16x128_f8f6f4 v[78:81], v[2:9], v[204:211], v[78:81]
	v_mfma_f32_16x16x128_f8f6f4 v[70:73], v[10:17], v[204:211], v[70:73]
	v_mfma_f32_16x16x128_f8f6f4 v[62:65], v[2:9], v[212:219], v[62:65]
	v_mfma_f32_16x16x128_f8f6f4 v[54:57], v[10:17], v[212:219], v[54:57]
	v_mfma_f32_16x16x128_f8f6f4 v[46:49], v[2:9], v[220:227], v[46:49]
	v_mfma_f32_16x16x128_f8f6f4 v[38:41], v[10:17], v[220:227], v[38:41]
	s_setprio 0
	s_setprio 1
	v_mfma_f32_16x16x128_f8f6f4 v[90:93], v[18:25], v[196:203], v[90:93]
	v_mfma_f32_16x16x128_f8f6f4 v[82:85], v[26:33], v[196:203], v[82:85]
	v_mfma_f32_16x16x128_f8f6f4 v[74:77], v[18:25], v[204:211], v[74:77]
	v_mfma_f32_16x16x128_f8f6f4 v[66:69], v[26:33], v[204:211], v[66:69]
	v_mfma_f32_16x16x128_f8f6f4 v[58:61], v[18:25], v[212:219], v[58:61]
	v_mfma_f32_16x16x128_f8f6f4 v[50:53], v[26:33], v[212:219], v[50:53]
	v_mfma_f32_16x16x128_f8f6f4 v[42:45], v[18:25], v[220:227], v[42:45]
	v_mfma_f32_16x16x128_f8f6f4 v[34:37], v[26:33], v[220:227], v[34:37]
	s_setprio 0
	s_barrier
	s_add_i32 s79, s79, 2
	s_add_u32 s46, s46, 0x100
	s_addc_u32 s47, s47, 0
	s_add_u32 s37, s37, 0x100
	s_addc_u32 s39, s39, 0
	s_cmp_gt_u32 s79, 5
	s_cbranch_scc0 .LBB0_711
	s_and_b64 vcc, exec, s[18:19]
	s_cbranch_vccz .LBB0_714
	s_barrier

.LBB0_872:
	s_add_u32 s40, s40, 0x58080
	s_addc_u32 s41, s41, 0
	s_add_u32 s79, s42, 0x100
	s_addc_u32 s80, s43, 0
	s_mov_b32 s81, -2
	s_waitcnt vmcnt(0)
	ds_read_b128 v[18:21], v192
	ds_read_b128 v[22:25], v192 offset:1024
	ds_read_b128 v[26:29], v192 offset:2048
	ds_read_b128 v[30:33], v192 offset:3072
	ds_read_b128 v[2:5], v193
	ds_read_b128 v[6:9], v193 offset:1024
	ds_read_b128 v[10:13], v193 offset:2048
	ds_read_b128 v[14:17], v193 offset:3072
	s_add_u32 s42, s40, 0xfffa8080
	s_addc_u32 s43, s41, -1
	s_cmp_eq_u32 s81, 18
	s_cselect_b32 s45, s37, s43
	s_cselect_b32 s44, s36, s42
	s_cselect_b32 s43, s39, s80
	s_cselect_b32 s42, s38, s79
	s_add_i32 m0, s46, 0xc000
	ds_read_b128 v[182:185], v194
	ds_read_b128 v[186:189], v194 offset:1024
	ds_read_b128 v[196:199], v194 offset:2048
	ds_read_b128 v[200:203], v194 offset:3072
	ds_read_b128 v[204:207], v194 offset:4096
	ds_read_b128 v[208:211], v194 offset:5120
	ds_read_b128 v[212:215], v194 offset:6144
	ds_read_b128 v[216:219], v194 offset:7168
	global_load_lds_dwordx4 v174, s[40:41]
	s_add_i32 m0, s46, 0xe000
	s_nop 0
	global_load_lds_dwordx4 v176, s[40:41]
	s_waitcnt vmcnt(8)
	s_waitcnt lgkmcnt(0)
	s_barrier
	s_setprio 1
	s_waitcnt lgkmcnt(0)
	v_mfma_f32_16x16x128_f8f6f4 v[158:161], v[18:25], v[182:189], 0
	v_mfma_f32_16x16x128_f8f6f4 v[154:157], v[26:33], v[182:189], 0
	v_mfma_f32_16x16x128_f8f6f4 v[146:149], v[18:25], v[196:203], 0
	v_mfma_f32_16x16x128_f8f6f4 v[138:141], v[26:33], v[196:203], 0
	v_mfma_f32_16x16x128_f8f6f4 v[130:133], v[18:25], v[204:211], 0
	v_mfma_f32_16x16x128_f8f6f4 v[122:125], v[26:33], v[204:211], 0
	v_mfma_f32_16x16x128_f8f6f4 v[114:117], v[18:25], v[212:219], 0
	v_mfma_f32_16x16x128_f8f6f4 v[106:109], v[26:33], v[212:219], 0
	s_setprio 0
	s_setprio 1
	v_mfma_f32_16x16x128_f8f6f4 v[150:153], v[2:9], v[182:189], 0
	v_mfma_f32_16x16x128_f8f6f4 v[142:145], v[10:17], v[182:189], 0
	v_mfma_f32_16x16x128_f8f6f4 v[134:137], v[2:9], v[196:203], 0
	v_mfma_f32_16x16x128_f8f6f4 v[126:129], v[10:17], v[196:203], 0
	v_mfma_f32_16x16x128_f8f6f4 v[118:121], v[2:9], v[204:211], 0
	v_mfma_f32_16x16x128_f8f6f4 v[110:113], v[10:17], v[204:211], 0
	v_mfma_f32_16x16x128_f8f6f4 v[102:105], v[2:9], v[212:219], 0
	v_mfma_f32_16x16x128_f8f6f4 v[98:101], v[10:17], v[212:219], 0
	s_setprio 0
	s_barrier
	s_add_i32 s76, s60, s3
	s_mov_b64 s[98:99], s[42:43]
	s_mov_b32 m0, s76
	ds_read_b128 v[196:199], v194 offset:16384
	ds_read_b128 v[200:203], v194 offset:17408
	ds_read_b128 v[204:207], v194 offset:18432
	ds_read_b128 v[208:211], v194 offset:19456
	ds_read_b128 v[212:215], v194 offset:20480
	ds_read_b128 v[216:219], v194 offset:21504
	ds_read_b128 v[220:223], v194 offset:22528
	ds_read_b128 v[224:227], v194 offset:23552
	global_load_lds_dwordx4 v168, s[98:99]
	s_add_i32 m0, s76, 0x2000
	s_add_u32 s82, s42, 0x58000
	s_addc_u32 s83, s43, 0
	s_add_i32 s76, s61, s3
	global_load_lds_dwordx4 v164, s[98:99]
	s_mov_b32 m0, s76
	s_mov_b64 s[100:101], s[44:45]
	global_load_lds_dwordx4 v168, s[82:83]
	s_add_i32 m0, s76, 0x2000
	s_nop 0
	global_load_lds_dwordx4 v164, s[82:83]
	s_mov_b32 m0, s46
	s_nop 0
	global_load_lds_dwordx4 v172, s[100:101]
	s_mov_b32 m0, s47
	s_nop 0
	global_load_lds_dwordx4 v166, s[100:101]
	s_waitcnt vmcnt(8)
	s_waitcnt lgkmcnt(0)
	s_barrier
	s_setprio 1
	s_waitcnt lgkmcnt(0)
	v_mfma_f32_16x16x128_f8f6f4 v[94:97], v[18:25], v[196:203], 0
	v_mfma_f32_16x16x128_f8f6f4 v[90:93], v[26:33], v[196:203], 0
	v_mfma_f32_16x16x128_f8f6f4 v[82:85], v[18:25], v[204:211], 0
	v_mfma_f32_16x16x128_f8f6f4 v[74:77], v[26:33], v[204:211], 0
	v_mfma_f32_16x16x128_f8f6f4 v[66:69], v[18:25], v[212:219], 0
	v_mfma_f32_16x16x128_f8f6f4 v[58:61], v[26:33], v[212:219], 0
	v_mfma_f32_16x16x128_f8f6f4 v[50:53], v[18:25], v[220:227], 0
	v_mfma_f32_16x16x128_f8f6f4 v[42:45], v[26:33], v[220:227], 0
	s_setprio 0
	s_setprio 1
	v_mfma_f32_16x16x128_f8f6f4 v[86:89], v[2:9], v[196:203], 0
	v_mfma_f32_16x16x128_f8f6f4 v[78:81], v[10:17], v[196:203], 0
	v_mfma_f32_16x16x128_f8f6f4 v[70:73], v[2:9], v[204:211], 0
	v_mfma_f32_16x16x128_f8f6f4 v[62:65], v[10:17], v[204:211], 0
	v_mfma_f32_16x16x128_f8f6f4 v[54:57], v[2:9], v[212:219], 0
	v_mfma_f32_16x16x128_f8f6f4 v[46:49], v[10:17], v[212:219], 0
	v_mfma_f32_16x16x128_f8f6f4 v[38:41], v[2:9], v[220:227], 0
	v_mfma_f32_16x16x128_f8f6f4 v[34:37], v[10:17], v[220:227], 0
	s_setprio 0
	s_barrier
	s_add_i32 s76, 0, 0x18000
	s_add_i32 s82, 0, 0x1c000
	v_add_u32_e32 v14, s76, v190
	v_add_u32_e32 v30, s82, v190
	ds_read_b128 v[2:5], v14
	ds_read_b128 v[6:9], v14 offset:1024
	ds_read_b128 v[10:13], v14 offset:2048
	ds_read_b128 v[14:17], v14 offset:3072
	ds_read_b128 v[18:21], v30
	ds_read_b128 v[22:25], v30 offset:1024
	ds_read_b128 v[26:29], v30 offset:2048
	ds_read_b128 v[30:33], v30 offset:3072
	s_add_u32 s44, s44, 0x58000
	s_addc_u32 s45, s45, 0
	s_mov_b32 m0, s52
	ds_read_b128 v[196:199], v194 offset:32768
	ds_read_b128 v[200:203], v194 offset:33792
	ds_read_b128 v[204:207], v194 offset:34816
	ds_read_b128 v[208:211], v194 offset:35840
	ds_read_b128 v[212:215], v194 offset:36864
	ds_read_b128 v[216:219], v194 offset:37888
	ds_read_b128 v[220:223], v194 offset:38912
	ds_read_b128 v[224:227], v194 offset:39936
	global_load_lds_dwordx4 v172, s[44:45]
	s_mov_b32 m0, s53
	s_nop 0
	global_load_lds_dwordx4 v166, s[44:45]
	s_waitcnt vmcnt(8)
	s_waitcnt lgkmcnt(0)
	s_barrier
	s_setprio 1
	s_waitcnt lgkmcnt(0)
	v_mfma_f32_16x16x128_f8f6f4 v[158:161], v[2:9], v[196:203], v[158:161]
	v_mfma_f32_16x16x128_f8f6f4 v[154:157], v[10:17], v[196:203], v[154:157]
	v_mfma_f32_16x16x128_f8f6f4 v[146:149], v[2:9], v[204:211], v[146:149]
	v_mfma_f32_16x16x128_f8f6f4 v[138:141], v[10:17], v[204:211], v[138:141]
	v_mfma_f32_16x16x128_f8f6f4 v[130:133], v[2:9], v[212:219], v[130:133]
	v_mfma_f32_16x16x128_f8f6f4 v[122:125], v[10:17], v[212:219], v[122:125]
	v_mfma_f32_16x16x128_f8f6f4 v[114:117], v[2:9], v[220:227], v[114:117]
	v_mfma_f32_16x16x128_f8f6f4 v[106:109], v[10:17], v[220:227], v[106:109]
	s_setprio 0
	s_setprio 1
	v_mfma_f32_16x16x128_f8f6f4 v[150:153], v[18:25], v[196:203], v[150:153]
	v_mfma_f32_16x16x128_f8f6f4 v[142:145], v[26:33], v[196:203], v[142:145]
	v_mfma_f32_16x16x128_f8f6f4 v[134:137], v[18:25], v[204:211], v[134:137]
	v_mfma_f32_16x16x128_f8f6f4 v[126:129], v[26:33], v[204:211], v[126:129]
	v_mfma_f32_16x16x128_f8f6f4 v[118:121], v[18:25], v[212:219], v[118:121]
	v_mfma_f32_16x16x128_f8f6f4 v[110:113], v[26:33], v[212:219], v[110:113]
	v_mfma_f32_16x16x128_f8f6f4 v[102:105], v[18:25], v[220:227], v[102:105]
	v_mfma_f32_16x16x128_f8f6f4 v[98:101], v[26:33], v[220:227], v[98:101]
	s_setprio 0
	s_barrier
	s_add_i32 s44, s76, s3
	s_mov_b32 m0, s44
	ds_read_b128 v[196:199], v194 offset:49152
	ds_read_b128 v[200:203], v194 offset:50176
	ds_read_b128 v[204:207], v194 offset:51200
	ds_read_b128 v[208:211], v194 offset:52224
	ds_read_b128 v[212:215], v194 offset:53248
	ds_read_b128 v[216:219], v194 offset:54272
	ds_read_b128 v[220:223], v194 offset:55296
	ds_read_b128 v[224:227], v194 offset:56320
	s_add_u32 s98, s98, 0x80
	s_addc_u32 s99, s99, 0
	global_load_lds_dwordx4 v168, s[98:99]
	s_add_i32 m0, s44, 0x2000
	s_add_u32 s42, s42, 0x58080
	s_addc_u32 s43, s43, 0
	s_add_i32 s44, s82, s3
	global_load_lds_dwordx4 v164, s[98:99]
	s_mov_b32 m0, s44
	s_nop 0
	global_load_lds_dwordx4 v168, s[42:43]
	s_add_i32 m0, s44, 0x2000
	s_nop 0
	global_load_lds_dwordx4 v164, s[42:43]
	s_mov_b32 m0, s57
	s_nop 0
	s_add_u32 s100, s100, 0x80
	s_addc_u32 s101, s101, 0
	global_load_lds_dwordx4 v172, s[100:101]
	s_mov_b32 m0, s58
	s_nop 0
	global_load_lds_dwordx4 v166, s[100:101]
	s_waitcnt vmcnt(8)
	s_waitcnt lgkmcnt(0)
	s_barrier
	s_setprio 1
	s_waitcnt lgkmcnt(0)
	v_mfma_f32_16x16x128_f8f6f4 v[94:97], v[2:9], v[196:203], v[94:97]
	v_mfma_f32_16x16x128_f8f6f4 v[90:93], v[10:17], v[196:203], v[90:93]
	v_mfma_f32_16x16x128_f8f6f4 v[82:85], v[2:9], v[204:211], v[82:85]
	v_mfma_f32_16x16x128_f8f6f4 v[74:77], v[10:17], v[204:211], v[74:77]
	v_mfma_f32_16x16x128_f8f6f4 v[66:69], v[2:9], v[212:219], v[66:69]
	v_mfma_f32_16x16x128_f8f6f4 v[58:61], v[10:17], v[212:219], v[58:61]
	v_mfma_f32_16x16x128_f8f6f4 v[50:53], v[2:9], v[220:227], v[50:53]
	v_mfma_f32_16x16x128_f8f6f4 v[42:45], v[10:17], v[220:227], v[42:45]
	s_setprio 0
	s_setprio 1
	v_mfma_f32_16x16x128_f8f6f4 v[86:89], v[18:25], v[196:203], v[86:89]
	v_mfma_f32_16x16x128_f8f6f4 v[78:81], v[26:33], v[196:203], v[78:81]
	v_mfma_f32_16x16x128_f8f6f4 v[70:73], v[18:25], v[204:211], v[70:73]
	v_mfma_f32_16x16x128_f8f6f4 v[62:65], v[26:33], v[204:211], v[62:65]
	v_mfma_f32_16x16x128_f8f6f4 v[54:57], v[18:25], v[212:219], v[54:57]
	v_mfma_f32_16x16x128_f8f6f4 v[46:49], v[26:33], v[212:219], v[46:49]
	v_mfma_f32_16x16x128_f8f6f4 v[38:41], v[18:25], v[220:227], v[38:41]
	v_mfma_f32_16x16x128_f8f6f4 v[34:37], v[26:33], v[220:227], v[34:37]
	s_setprio 0
	s_barrier
	s_add_i32 s81, s81, 2
	s_add_u32 s40, s40, 0x100
	s_addc_u32 s41, s41, 0
	s_add_u32 s79, s79, 0x100
	s_addc_u32 s80, s80, 0
	s_cmp_gt_u32 s81, 19
.LBB0_873:
	ds_read_b128 v[18:21], v192
	ds_read_b128 v[22:25], v192 offset:1024
	ds_read_b128 v[26:29], v192 offset:2048
	ds_read_b128 v[30:33], v192 offset:3072
	ds_read_b128 v[2:5], v193
	ds_read_b128 v[6:9], v193 offset:1024
	ds_read_b128 v[10:13], v193 offset:2048
	ds_read_b128 v[14:17], v193 offset:3072
	s_add_u32 s42, s40, 0xfffa8080
	s_addc_u32 s43, s41, -1
	s_cmp_eq_u32 s81, 18
	s_cselect_b32 s45, s37, s43
	s_cselect_b32 s44, s36, s42
	s_cselect_b32 s43, s39, s80
	s_cselect_b32 s42, s38, s79
	s_add_i32 m0, s46, 0xc000
	ds_read_b128 v[182:185], v194
	ds_read_b128 v[186:189], v194 offset:1024
	ds_read_b128 v[196:199], v194 offset:2048
	ds_read_b128 v[200:203], v194 offset:3072
	ds_read_b128 v[204:207], v194 offset:4096
	ds_read_b128 v[208:211], v194 offset:5120
	ds_read_b128 v[212:215], v194 offset:6144
	ds_read_b128 v[216:219], v194 offset:7168
	global_load_lds_dwordx4 v174, s[40:41]
	s_add_i32 m0, s46, 0xe000
	s_nop 0
	global_load_lds_dwordx4 v176, s[40:41]
	s_waitcnt vmcnt(8)
	s_waitcnt lgkmcnt(0)
	s_barrier
	s_setprio 1
	s_waitcnt lgkmcnt(0)
	v_mfma_f32_16x16x128_f8f6f4 v[158:161], v[18:25], v[182:189], v[158:161]
	v_mfma_f32_16x16x128_f8f6f4 v[154:157], v[26:33], v[182:189], v[154:157]
	v_mfma_f32_16x16x128_f8f6f4 v[146:149], v[18:25], v[196:203], v[146:149]
	v_mfma_f32_16x16x128_f8f6f4 v[138:141], v[26:33], v[196:203], v[138:141]
	v_mfma_f32_16x16x128_f8f6f4 v[130:133], v[18:25], v[204:211], v[130:133]
	v_mfma_f32_16x16x128_f8f6f4 v[122:125], v[26:33], v[204:211], v[122:125]
	v_mfma_f32_16x16x128_f8f6f4 v[114:117], v[18:25], v[212:219], v[114:117]
	v_mfma_f32_16x16x128_f8f6f4 v[106:109], v[26:33], v[212:219], v[106:109]
	s_setprio 0
	s_setprio 1
	v_mfma_f32_16x16x128_f8f6f4 v[150:153], v[2:9], v[182:189], v[150:153]
	v_mfma_f32_16x16x128_f8f6f4 v[142:145], v[10:17], v[182:189], v[142:145]
	v_mfma_f32_16x16x128_f8f6f4 v[134:137], v[2:9], v[196:203], v[134:137]
	v_mfma_f32_16x16x128_f8f6f4 v[126:129], v[10:17], v[196:203], v[126:129]
	v_mfma_f32_16x16x128_f8f6f4 v[118:121], v[2:9], v[204:211], v[118:121]
	v_mfma_f32_16x16x128_f8f6f4 v[110:113], v[10:17], v[204:211], v[110:113]
	v_mfma_f32_16x16x128_f8f6f4 v[102:105], v[2:9], v[212:219], v[102:105]
	v_mfma_f32_16x16x128_f8f6f4 v[98:101], v[10:17], v[212:219], v[98:101]
	s_setprio 0
	s_barrier
	s_add_i32 s76, s60, s3
	s_mov_b64 s[98:99], s[42:43]
	s_mov_b32 m0, s76
	ds_read_b128 v[196:199], v194 offset:16384
	ds_read_b128 v[200:203], v194 offset:17408
	ds_read_b128 v[204:207], v194 offset:18432
	ds_read_b128 v[208:211], v194 offset:19456
	ds_read_b128 v[212:215], v194 offset:20480
	ds_read_b128 v[216:219], v194 offset:21504
	ds_read_b128 v[220:223], v194 offset:22528
	ds_read_b128 v[224:227], v194 offset:23552
	global_load_lds_dwordx4 v168, s[98:99]
	s_add_i32 m0, s76, 0x2000
	s_add_u32 s82, s42, 0x58000
	s_addc_u32 s83, s43, 0
	s_add_i32 s76, s61, s3
	global_load_lds_dwordx4 v164, s[98:99]
	s_mov_b32 m0, s76
	s_mov_b64 s[100:101], s[44:45]
	global_load_lds_dwordx4 v168, s[82:83]
	s_add_i32 m0, s76, 0x2000
	s_nop 0
	global_load_lds_dwordx4 v164, s[82:83]
	s_mov_b32 m0, s46
	s_nop 0
	global_load_lds_dwordx4 v172, s[100:101]
	s_mov_b32 m0, s47
	s_nop 0
	global_load_lds_dwordx4 v166, s[100:101]
	s_waitcnt vmcnt(8)
	s_waitcnt lgkmcnt(0)
	s_barrier
	s_setprio 1
	s_waitcnt lgkmcnt(0)
	v_mfma_f32_16x16x128_f8f6f4 v[94:97], v[18:25], v[196:203], v[94:97]
	v_mfma_f32_16x16x128_f8f6f4 v[90:93], v[26:33], v[196:203], v[90:93]
	v_mfma_f32_16x16x128_f8f6f4 v[82:85], v[18:25], v[204:211], v[82:85]
	v_mfma_f32_16x16x128_f8f6f4 v[74:77], v[26:33], v[204:211], v[74:77]
	v_mfma_f32_16x16x128_f8f6f4 v[66:69], v[18:25], v[212:219], v[66:69]
	v_mfma_f32_16x16x128_f8f6f4 v[58:61], v[26:33], v[212:219], v[58:61]
	v_mfma_f32_16x16x128_f8f6f4 v[50:53], v[18:25], v[220:227], v[50:53]
	v_mfma_f32_16x16x128_f8f6f4 v[42:45], v[26:33], v[220:227], v[42:45]
	s_setprio 0
	s_setprio 1
	v_mfma_f32_16x16x128_f8f6f4 v[86:89], v[2:9], v[196:203], v[86:89]
	v_mfma_f32_16x16x128_f8f6f4 v[78:81], v[10:17], v[196:203], v[78:81]
	v_mfma_f32_16x16x128_f8f6f4 v[70:73], v[2:9], v[204:211], v[70:73]
	v_mfma_f32_16x16x128_f8f6f4 v[62:65], v[10:17], v[204:211], v[62:65]
	v_mfma_f32_16x16x128_f8f6f4 v[54:57], v[2:9], v[212:219], v[54:57]
	v_mfma_f32_16x16x128_f8f6f4 v[46:49], v[10:17], v[212:219], v[46:49]
	v_mfma_f32_16x16x128_f8f6f4 v[38:41], v[2:9], v[220:227], v[38:41]
	v_mfma_f32_16x16x128_f8f6f4 v[34:37], v[10:17], v[220:227], v[34:37]
	s_setprio 0
	s_barrier
	s_add_i32 s76, 0, 0x18000
	s_add_i32 s82, 0, 0x1c000
	v_add_u32_e32 v14, s76, v190
	v_add_u32_e32 v30, s82, v190
	ds_read_b128 v[2:5], v14
	ds_read_b128 v[6:9], v14 offset:1024
	ds_read_b128 v[10:13], v14 offset:2048
	ds_read_b128 v[14:17], v14 offset:3072
	ds_read_b128 v[18:21], v30
	ds_read_b128 v[22:25], v30 offset:1024
	ds_read_b128 v[26:29], v30 offset:2048
	ds_read_b128 v[30:33], v30 offset:3072
	s_add_u32 s44, s44, 0x58000
	s_addc_u32 s45, s45, 0
	s_mov_b32 m0, s52
	ds_read_b128 v[196:199], v194 offset:32768
	ds_read_b128 v[200:203], v194 offset:33792
	ds_read_b128 v[204:207], v194 offset:34816
	ds_read_b128 v[208:211], v194 offset:35840
	ds_read_b128 v[212:215], v194 offset:36864
	ds_read_b128 v[216:219], v194 offset:37888
	ds_read_b128 v[220:223], v194 offset:38912
	ds_read_b128 v[224:227], v194 offset:39936
	global_load_lds_dwordx4 v172, s[44:45]
	s_mov_b32 m0, s53
	s_nop 0
	global_load_lds_dwordx4 v166, s[44:45]
	s_waitcnt vmcnt(8)
	s_waitcnt lgkmcnt(0)
	s_barrier
	s_setprio 1
	s_waitcnt lgkmcnt(0)
	v_mfma_f32_16x16x128_f8f6f4 v[158:161], v[2:9], v[196:203], v[158:161]
	v_mfma_f32_16x16x128_f8f6f4 v[154:157], v[10:17], v[196:203], v[154:157]
	v_mfma_f32_16x16x128_f8f6f4 v[146:149], v[2:9], v[204:211], v[146:149]
	v_mfma_f32_16x16x128_f8f6f4 v[138:141], v[10:17], v[204:211], v[138:141]
	v_mfma_f32_16x16x128_f8f6f4 v[130:133], v[2:9], v[212:219], v[130:133]
	v_mfma_f32_16x16x128_f8f6f4 v[122:125], v[10:17], v[212:219], v[122:125]
	v_mfma_f32_16x16x128_f8f6f4 v[114:117], v[2:9], v[220:227], v[114:117]
	v_mfma_f32_16x16x128_f8f6f4 v[106:109], v[10:17], v[220:227], v[106:109]
	s_setprio 0
	s_setprio 1
	v_mfma_f32_16x16x128_f8f6f4 v[150:153], v[18:25], v[196:203], v[150:153]
	v_mfma_f32_16x16x128_f8f6f4 v[142:145], v[26:33], v[196:203], v[142:145]
	v_mfma_f32_16x16x128_f8f6f4 v[134:137], v[18:25], v[204:211], v[134:137]
	v_mfma_f32_16x16x128_f8f6f4 v[126:129], v[26:33], v[204:211], v[126:129]
	v_mfma_f32_16x16x128_f8f6f4 v[118:121], v[18:25], v[212:219], v[118:121]
	v_mfma_f32_16x16x128_f8f6f4 v[110:113], v[26:33], v[212:219], v[110:113]
	v_mfma_f32_16x16x128_f8f6f4 v[102:105], v[18:25], v[220:227], v[102:105]
	v_mfma_f32_16x16x128_f8f6f4 v[98:101], v[26:33], v[220:227], v[98:101]
	s_setprio 0
	s_barrier
	s_add_i32 s44, s76, s3
	s_mov_b32 m0, s44
	ds_read_b128 v[196:199], v194 offset:49152
	ds_read_b128 v[200:203], v194 offset:50176
	ds_read_b128 v[204:207], v194 offset:51200
	ds_read_b128 v[208:211], v194 offset:52224
	ds_read_b128 v[212:215], v194 offset:53248
	ds_read_b128 v[216:219], v194 offset:54272
	ds_read_b128 v[220:223], v194 offset:55296
	ds_read_b128 v[224:227], v194 offset:56320
	s_add_u32 s98, s98, 0x80
	s_addc_u32 s99, s99, 0
	global_load_lds_dwordx4 v168, s[98:99]
	s_add_i32 m0, s44, 0x2000
	s_add_u32 s42, s42, 0x58080
	s_addc_u32 s43, s43, 0
	s_add_i32 s44, s82, s3
	global_load_lds_dwordx4 v164, s[98:99]
	s_mov_b32 m0, s44
	s_nop 0
	global_load_lds_dwordx4 v168, s[42:43]
	s_add_i32 m0, s44, 0x2000
	s_nop 0
	global_load_lds_dwordx4 v164, s[42:43]
	s_mov_b32 m0, s57
	s_nop 0
	s_add_u32 s100, s100, 0x80
	s_addc_u32 s101, s101, 0
	global_load_lds_dwordx4 v172, s[100:101]
	s_mov_b32 m0, s58
	s_nop 0
	global_load_lds_dwordx4 v166, s[100:101]
	s_waitcnt vmcnt(8)
	s_waitcnt lgkmcnt(0)
	s_barrier
	s_setprio 1
	s_waitcnt lgkmcnt(0)
	v_mfma_f32_16x16x128_f8f6f4 v[94:97], v[2:9], v[196:203], v[94:97]
	v_mfma_f32_16x16x128_f8f6f4 v[90:93], v[10:17], v[196:203], v[90:93]
	v_mfma_f32_16x16x128_f8f6f4 v[82:85], v[2:9], v[204:211], v[82:85]
	v_mfma_f32_16x16x128_f8f6f4 v[74:77], v[10:17], v[204:211], v[74:77]
	v_mfma_f32_16x16x128_f8f6f4 v[66:69], v[2:9], v[212:219], v[66:69]
	v_mfma_f32_16x16x128_f8f6f4 v[58:61], v[10:17], v[212:219], v[58:61]
	v_mfma_f32_16x16x128_f8f6f4 v[50:53], v[2:9], v[220:227], v[50:53]
	v_mfma_f32_16x16x128_f8f6f4 v[42:45], v[10:17], v[220:227], v[42:45]
	s_setprio 0
	s_setprio 1
	v_mfma_f32_16x16x128_f8f6f4 v[86:89], v[18:25], v[196:203], v[86:89]
	v_mfma_f32_16x16x128_f8f6f4 v[78:81], v[26:33], v[196:203], v[78:81]
	v_mfma_f32_16x16x128_f8f6f4 v[70:73], v[18:25], v[204:211], v[70:73]
	v_mfma_f32_16x16x128_f8f6f4 v[62:65], v[26:33], v[204:211], v[62:65]
	v_mfma_f32_16x16x128_f8f6f4 v[54:57], v[18:25], v[212:219], v[54:57]
	v_mfma_f32_16x16x128_f8f6f4 v[46:49], v[26:33], v[212:219], v[46:49]
	v_mfma_f32_16x16x128_f8f6f4 v[38:41], v[18:25], v[220:227], v[38:41]
	v_mfma_f32_16x16x128_f8f6f4 v[34:37], v[26:33], v[220:227], v[34:37]
	s_setprio 0
	s_barrier
	s_add_i32 s81, s81, 2
	s_add_u32 s40, s40, 0x100
	s_addc_u32 s41, s41, 0
	s_add_u32 s79, s79, 0x100
	s_addc_u32 s80, s80, 0
	s_cmp_gt_u32 s81, 19
	s_cbranch_scc0 .LBB0_873
	s_and_b64 vcc, exec, s[20:21]
	s_cbranch_vccz .LBB0_876
	s_barrier

.LBB0_1123:
	s_add_u32 s44, s44, 0x40080
	s_addc_u32 s45, s45, 0
	s_add_u32 s21, s46, 0x100
	s_addc_u32 s37, s47, 0
	s_mov_b32 s67, -2
	ds_read_b128 v[148:151], v153
	ds_read_b128 v[156:159], v153 offset:1024
	ds_read_b128 v[160:163], v153 offset:2048
	ds_read_b128 v[164:167], v153 offset:3072
	ds_read_b128 v[172:175], v154
	ds_read_b128 v[176:179], v154 offset:1024
	ds_read_b128 v[180:183], v154 offset:2048
	ds_read_b128 v[184:187], v154 offset:3072
	s_add_u32 s46, s44, 0xfffc0080
	s_addc_u32 s47, s45, -1
	s_cmp_eq_u32 s67, 12
	s_cselect_b32 s49, s39, s47
	s_cselect_b32 s48, s38, s46
	s_cselect_b32 s47, s41, s37
	s_cselect_b32 s46, s40, s21
	s_add_i32 m0, s43, 0xc000
	ds_read_b128 v[188:191], v155
	ds_read_b128 v[192:195], v155 offset:1024
	ds_read_b128 v[196:199], v155 offset:2048
	ds_read_b128 v[200:203], v155 offset:3072
	ds_read_b128 v[204:207], v155 offset:4096
	ds_read_b128 v[208:211], v155 offset:5120
	ds_read_b128 v[212:215], v155 offset:6144
	ds_read_b128 v[216:219], v155 offset:7168
	global_load_lds_dwordx4 v140, s[44:45]
	s_add_i32 m0, s43, 0xe000
	s_nop 0
	global_load_lds_dwordx4 v142, s[44:45]
	s_waitcnt vmcnt(8)
	s_waitcnt lgkmcnt(0)
	s_barrier
	s_setprio 1
	s_waitcnt lgkmcnt(0)
	v_mfma_f32_16x16x32_bf16 v[126:129], v[148:151], v[188:191], 0
	v_mfma_f32_16x16x32_bf16 v[122:125], v[160:163], v[188:191], 0
	v_mfma_f32_16x16x32_bf16 v[118:121], v[148:151], v[196:199], 0
	v_mfma_f32_16x16x32_bf16 v[110:113], v[160:163], v[196:199], 0
	v_mfma_f32_16x16x32_bf16 v[102:105], v[148:151], v[204:207], 0
	v_mfma_f32_16x16x32_bf16 v[94:97], v[160:163], v[204:207], 0
	v_mfma_f32_16x16x32_bf16 v[86:89], v[148:151], v[212:215], 0
	v_mfma_f32_16x16x32_bf16 v[78:81], v[160:163], v[212:215], 0
	v_mfma_f32_16x16x32_bf16 v[126:129], v[156:159], v[192:195], v[126:129]
	v_mfma_f32_16x16x32_bf16 v[122:125], v[164:167], v[192:195], v[122:125]
	v_mfma_f32_16x16x32_bf16 v[118:121], v[156:159], v[200:203], v[118:121]
	v_mfma_f32_16x16x32_bf16 v[110:113], v[164:167], v[200:203], v[110:113]
	v_mfma_f32_16x16x32_bf16 v[102:105], v[156:159], v[208:211], v[102:105]
	v_mfma_f32_16x16x32_bf16 v[94:97], v[164:167], v[208:211], v[94:97]
	v_mfma_f32_16x16x32_bf16 v[86:89], v[156:159], v[216:219], v[86:89]
	v_mfma_f32_16x16x32_bf16 v[78:81], v[164:167], v[216:219], v[78:81]
	s_setprio 0
	s_setprio 1
	v_mfma_f32_16x16x32_bf16 v[114:117], v[172:175], v[188:191], 0
	v_mfma_f32_16x16x32_bf16 v[106:109], v[180:183], v[188:191], 0
	v_mfma_f32_16x16x32_bf16 v[98:101], v[172:175], v[196:199], 0
	v_mfma_f32_16x16x32_bf16 v[90:93], v[180:183], v[196:199], 0
	v_mfma_f32_16x16x32_bf16 v[82:85], v[172:175], v[204:207], 0
	v_mfma_f32_16x16x32_bf16 v[74:77], v[180:183], v[204:207], 0
	v_mfma_f32_16x16x32_bf16 v[70:73], v[172:175], v[212:215], 0
	v_mfma_f32_16x16x32_bf16 v[66:69], v[180:183], v[212:215], 0
	v_mfma_f32_16x16x32_bf16 v[114:117], v[176:179], v[192:195], v[114:117]
	v_mfma_f32_16x16x32_bf16 v[106:109], v[184:187], v[192:195], v[106:109]
	v_mfma_f32_16x16x32_bf16 v[98:101], v[176:179], v[200:203], v[98:101]
	v_mfma_f32_16x16x32_bf16 v[90:93], v[184:187], v[200:203], v[90:93]
	v_mfma_f32_16x16x32_bf16 v[82:85], v[176:179], v[208:211], v[82:85]
	v_mfma_f32_16x16x32_bf16 v[74:77], v[184:187], v[208:211], v[74:77]
	v_mfma_f32_16x16x32_bf16 v[70:73], v[176:179], v[216:219], v[70:73]
	v_mfma_f32_16x16x32_bf16 v[66:69], v[184:187], v[216:219], v[66:69]
	s_setprio 0
	s_barrier
	s_add_i32 s76, s59, s33
	s_mov_b64 s[98:99], s[46:47]
	s_mov_b32 m0, s76
	ds_read_b128 v[188:191], v155 offset:16384
	ds_read_b128 v[192:195], v155 offset:17408
	ds_read_b128 v[196:199], v155 offset:18432
	ds_read_b128 v[200:203], v155 offset:19456
	ds_read_b128 v[204:207], v155 offset:20480
	ds_read_b128 v[208:211], v155 offset:21504
	ds_read_b128 v[212:215], v155 offset:22528
	ds_read_b128 v[216:219], v155 offset:23552
	global_load_lds_dwordx4 v136, s[98:99]
	s_add_i32 m0, s76, 0x2000
	s_add_u32 s78, s46, 0x40000
	s_addc_u32 s79, s47, 0
	s_add_i32 s76, s60, s33
	global_load_lds_dwordx4 v132, s[98:99]
	s_mov_b32 m0, s76
	s_mov_b64 s[100:101], s[48:49]
	global_load_lds_dwordx4 v136, s[78:79]
	s_add_i32 m0, s76, 0x2000
	s_nop 0
	global_load_lds_dwordx4 v132, s[78:79]
	s_mov_b32 m0, s43
	s_nop 0
	global_load_lds_dwordx4 v138, s[100:101]
	s_mov_b32 m0, s52
	s_nop 0
	global_load_lds_dwordx4 v134, s[100:101]
	s_waitcnt vmcnt(8)
	s_waitcnt lgkmcnt(0)
	s_barrier
	s_setprio 1
	s_waitcnt lgkmcnt(0)
	v_mfma_f32_16x16x32_bf16 v[62:65], v[148:151], v[188:191], 0
	v_mfma_f32_16x16x32_bf16 v[58:61], v[160:163], v[188:191], 0
	v_mfma_f32_16x16x32_bf16 v[54:57], v[148:151], v[196:199], 0
	v_mfma_f32_16x16x32_bf16 v[46:49], v[160:163], v[196:199], 0
	v_mfma_f32_16x16x32_bf16 v[38:41], v[148:151], v[204:207], 0
	v_mfma_f32_16x16x32_bf16 v[30:33], v[160:163], v[204:207], 0
	v_mfma_f32_16x16x32_bf16 v[22:25], v[148:151], v[212:215], 0
	v_mfma_f32_16x16x32_bf16 v[14:17], v[160:163], v[212:215], 0
	v_mfma_f32_16x16x32_bf16 v[62:65], v[156:159], v[192:195], v[62:65]
	v_mfma_f32_16x16x32_bf16 v[58:61], v[164:167], v[192:195], v[58:61]
	v_mfma_f32_16x16x32_bf16 v[54:57], v[156:159], v[200:203], v[54:57]
	v_mfma_f32_16x16x32_bf16 v[46:49], v[164:167], v[200:203], v[46:49]
	v_mfma_f32_16x16x32_bf16 v[38:41], v[156:159], v[208:211], v[38:41]
	v_mfma_f32_16x16x32_bf16 v[30:33], v[164:167], v[208:211], v[30:33]
	v_mfma_f32_16x16x32_bf16 v[22:25], v[156:159], v[216:219], v[22:25]
	v_mfma_f32_16x16x32_bf16 v[14:17], v[164:167], v[216:219], v[14:17]
	s_setprio 0
	s_setprio 1
	v_mfma_f32_16x16x32_bf16 v[50:53], v[172:175], v[188:191], 0
	v_mfma_f32_16x16x32_bf16 v[42:45], v[180:183], v[188:191], 0
	v_mfma_f32_16x16x32_bf16 v[34:37], v[172:175], v[196:199], 0
	v_mfma_f32_16x16x32_bf16 v[26:29], v[180:183], v[196:199], 0
	v_mfma_f32_16x16x32_bf16 v[18:21], v[172:175], v[204:207], 0
	v_mfma_f32_16x16x32_bf16 v[10:13], v[180:183], v[204:207], 0
	v_mfma_f32_16x16x32_bf16 v[6:9], v[172:175], v[212:215], 0
	v_mfma_f32_16x16x32_bf16 v[2:5], v[180:183], v[212:215], 0
	v_mfma_f32_16x16x32_bf16 v[50:53], v[176:179], v[192:195], v[50:53]
	v_mfma_f32_16x16x32_bf16 v[42:45], v[184:187], v[192:195], v[42:45]
	v_mfma_f32_16x16x32_bf16 v[34:37], v[176:179], v[200:203], v[34:37]
	v_mfma_f32_16x16x32_bf16 v[26:29], v[184:187], v[200:203], v[26:29]
	v_mfma_f32_16x16x32_bf16 v[18:21], v[176:179], v[208:211], v[18:21]
	v_mfma_f32_16x16x32_bf16 v[10:13], v[184:187], v[208:211], v[10:13]
	v_mfma_f32_16x16x32_bf16 v[6:9], v[176:179], v[216:219], v[6:9]
	v_mfma_f32_16x16x32_bf16 v[2:5], v[184:187], v[216:219], v[2:5]
	s_setprio 0
	s_barrier
	s_add_i32 s76, 0, 0x18000
	s_add_i32 s78, 0, 0x1c000
	v_add_u32_e32 v164, s76, v131
	v_add_u32_e32 v184, s78, v131
	ds_read_b128 v[148:151], v164
	ds_read_b128 v[156:159], v164 offset:1024
	ds_read_b128 v[160:163], v164 offset:2048
	ds_read_b128 v[164:167], v164 offset:3072
	ds_read_b128 v[172:175], v184
	ds_read_b128 v[176:179], v184 offset:1024
	ds_read_b128 v[180:183], v184 offset:2048
	ds_read_b128 v[184:187], v184 offset:3072
	s_add_u32 s48, s48, 0x40000
	s_addc_u32 s49, s49, 0
	s_mov_b32 m0, s53
	ds_read_b128 v[188:191], v155 offset:32768
	ds_read_b128 v[192:195], v155 offset:33792
	ds_read_b128 v[196:199], v155 offset:34816
	ds_read_b128 v[200:203], v155 offset:35840
	ds_read_b128 v[204:207], v155 offset:36864
	ds_read_b128 v[208:211], v155 offset:37888
	ds_read_b128 v[212:215], v155 offset:38912
	ds_read_b128 v[216:219], v155 offset:39936
	global_load_lds_dwordx4 v138, s[48:49]
	s_mov_b32 m0, s54
	s_nop 0
	global_load_lds_dwordx4 v134, s[48:49]
	s_waitcnt vmcnt(8)
	s_waitcnt lgkmcnt(0)
	s_barrier
	s_setprio 1
	s_waitcnt lgkmcnt(0)
	v_mfma_f32_16x16x32_bf16 v[126:129], v[148:151], v[188:191], v[126:129]
	v_mfma_f32_16x16x32_bf16 v[122:125], v[160:163], v[188:191], v[122:125]
	v_mfma_f32_16x16x32_bf16 v[118:121], v[148:151], v[196:199], v[118:121]
	v_mfma_f32_16x16x32_bf16 v[110:113], v[160:163], v[196:199], v[110:113]
	v_mfma_f32_16x16x32_bf16 v[102:105], v[148:151], v[204:207], v[102:105]
	v_mfma_f32_16x16x32_bf16 v[94:97], v[160:163], v[204:207], v[94:97]
	v_mfma_f32_16x16x32_bf16 v[86:89], v[148:151], v[212:215], v[86:89]
	v_mfma_f32_16x16x32_bf16 v[78:81], v[160:163], v[212:215], v[78:81]
	v_mfma_f32_16x16x32_bf16 v[126:129], v[156:159], v[192:195], v[126:129]
	v_mfma_f32_16x16x32_bf16 v[122:125], v[164:167], v[192:195], v[122:125]
	v_mfma_f32_16x16x32_bf16 v[118:121], v[156:159], v[200:203], v[118:121]
	v_mfma_f32_16x16x32_bf16 v[110:113], v[164:167], v[200:203], v[110:113]
	v_mfma_f32_16x16x32_bf16 v[102:105], v[156:159], v[208:211], v[102:105]
	v_mfma_f32_16x16x32_bf16 v[94:97], v[164:167], v[208:211], v[94:97]
	v_mfma_f32_16x16x32_bf16 v[86:89], v[156:159], v[216:219], v[86:89]
	v_mfma_f32_16x16x32_bf16 v[78:81], v[164:167], v[216:219], v[78:81]
	s_setprio 0
	s_setprio 1
	v_mfma_f32_16x16x32_bf16 v[114:117], v[172:175], v[188:191], v[114:117]
	v_mfma_f32_16x16x32_bf16 v[106:109], v[180:183], v[188:191], v[106:109]
	v_mfma_f32_16x16x32_bf16 v[98:101], v[172:175], v[196:199], v[98:101]
	v_mfma_f32_16x16x32_bf16 v[90:93], v[180:183], v[196:199], v[90:93]
	v_mfma_f32_16x16x32_bf16 v[82:85], v[172:175], v[204:207], v[82:85]
	v_mfma_f32_16x16x32_bf16 v[74:77], v[180:183], v[204:207], v[74:77]
	v_mfma_f32_16x16x32_bf16 v[70:73], v[172:175], v[212:215], v[70:73]
	v_mfma_f32_16x16x32_bf16 v[66:69], v[180:183], v[212:215], v[66:69]
	v_mfma_f32_16x16x32_bf16 v[114:117], v[176:179], v[192:195], v[114:117]
	v_mfma_f32_16x16x32_bf16 v[106:109], v[184:187], v[192:195], v[106:109]
	v_mfma_f32_16x16x32_bf16 v[98:101], v[176:179], v[200:203], v[98:101]
	v_mfma_f32_16x16x32_bf16 v[90:93], v[184:187], v[200:203], v[90:93]
	v_mfma_f32_16x16x32_bf16 v[82:85], v[176:179], v[208:211], v[82:85]
	v_mfma_f32_16x16x32_bf16 v[74:77], v[184:187], v[208:211], v[74:77]
	v_mfma_f32_16x16x32_bf16 v[70:73], v[176:179], v[216:219], v[70:73]
	v_mfma_f32_16x16x32_bf16 v[66:69], v[184:187], v[216:219], v[66:69]
	s_setprio 0
	s_barrier
	s_add_i32 s48, s76, s33
	s_mov_b32 m0, s48
	ds_read_b128 v[188:191], v155 offset:49152
	ds_read_b128 v[192:195], v155 offset:50176
	ds_read_b128 v[196:199], v155 offset:51200
	ds_read_b128 v[200:203], v155 offset:52224
	ds_read_b128 v[204:207], v155 offset:53248
	ds_read_b128 v[208:211], v155 offset:54272
	ds_read_b128 v[212:215], v155 offset:55296
	ds_read_b128 v[216:219], v155 offset:56320
	s_add_u32 s98, s98, 0x80
	s_addc_u32 s99, s99, 0
	global_load_lds_dwordx4 v136, s[98:99]
	s_add_i32 m0, s48, 0x2000
	s_add_u32 s46, s46, 0x40080
	s_addc_u32 s47, s47, 0
	s_add_i32 s48, s78, s33
	global_load_lds_dwordx4 v132, s[98:99]
	s_mov_b32 m0, s48
	s_nop 0
	global_load_lds_dwordx4 v136, s[46:47]
	s_add_i32 m0, s48, 0x2000
	s_nop 0
	global_load_lds_dwordx4 v132, s[46:47]
	s_mov_b32 m0, s56
	s_nop 0
	s_add_u32 s100, s100, 0x80
	s_addc_u32 s101, s101, 0
	global_load_lds_dwordx4 v138, s[100:101]
	s_mov_b32 m0, s57
	s_nop 0
	global_load_lds_dwordx4 v134, s[100:101]
	s_waitcnt vmcnt(8)
	s_waitcnt lgkmcnt(0)
	s_barrier
	s_setprio 1
	s_waitcnt lgkmcnt(0)
	v_mfma_f32_16x16x32_bf16 v[62:65], v[148:151], v[188:191], v[62:65]
	v_mfma_f32_16x16x32_bf16 v[58:61], v[160:163], v[188:191], v[58:61]
	v_mfma_f32_16x16x32_bf16 v[54:57], v[148:151], v[196:199], v[54:57]
	v_mfma_f32_16x16x32_bf16 v[46:49], v[160:163], v[196:199], v[46:49]
	v_mfma_f32_16x16x32_bf16 v[38:41], v[148:151], v[204:207], v[38:41]
	v_mfma_f32_16x16x32_bf16 v[30:33], v[160:163], v[204:207], v[30:33]
	v_mfma_f32_16x16x32_bf16 v[22:25], v[148:151], v[212:215], v[22:25]
	v_mfma_f32_16x16x32_bf16 v[14:17], v[160:163], v[212:215], v[14:17]
	v_mfma_f32_16x16x32_bf16 v[62:65], v[156:159], v[192:195], v[62:65]
	v_mfma_f32_16x16x32_bf16 v[58:61], v[164:167], v[192:195], v[58:61]
	v_mfma_f32_16x16x32_bf16 v[54:57], v[156:159], v[200:203], v[54:57]
	v_mfma_f32_16x16x32_bf16 v[46:49], v[164:167], v[200:203], v[46:49]
	v_mfma_f32_16x16x32_bf16 v[38:41], v[156:159], v[208:211], v[38:41]
	v_mfma_f32_16x16x32_bf16 v[30:33], v[164:167], v[208:211], v[30:33]
	v_mfma_f32_16x16x32_bf16 v[22:25], v[156:159], v[216:219], v[22:25]
	v_mfma_f32_16x16x32_bf16 v[14:17], v[164:167], v[216:219], v[14:17]
	s_setprio 0
	s_setprio 1
	v_mfma_f32_16x16x32_bf16 v[50:53], v[172:175], v[188:191], v[50:53]
	v_mfma_f32_16x16x32_bf16 v[42:45], v[180:183], v[188:191], v[42:45]
	v_mfma_f32_16x16x32_bf16 v[34:37], v[172:175], v[196:199], v[34:37]
	v_mfma_f32_16x16x32_bf16 v[26:29], v[180:183], v[196:199], v[26:29]
	v_mfma_f32_16x16x32_bf16 v[18:21], v[172:175], v[204:207], v[18:21]
	v_mfma_f32_16x16x32_bf16 v[10:13], v[180:183], v[204:207], v[10:13]
	v_mfma_f32_16x16x32_bf16 v[6:9], v[172:175], v[212:215], v[6:9]
	v_mfma_f32_16x16x32_bf16 v[2:5], v[180:183], v[212:215], v[2:5]
	v_mfma_f32_16x16x32_bf16 v[50:53], v[176:179], v[192:195], v[50:53]
	v_mfma_f32_16x16x32_bf16 v[42:45], v[184:187], v[192:195], v[42:45]
	v_mfma_f32_16x16x32_bf16 v[34:37], v[176:179], v[200:203], v[34:37]
	v_mfma_f32_16x16x32_bf16 v[26:29], v[184:187], v[200:203], v[26:29]
	v_mfma_f32_16x16x32_bf16 v[18:21], v[176:179], v[208:211], v[18:21]
	v_mfma_f32_16x16x32_bf16 v[10:13], v[184:187], v[208:211], v[10:13]
	v_mfma_f32_16x16x32_bf16 v[6:9], v[176:179], v[216:219], v[6:9]
	v_mfma_f32_16x16x32_bf16 v[2:5], v[184:187], v[216:219], v[2:5]
	s_setprio 0
	s_barrier
	s_add_i32 s67, s67, 2
	s_add_u32 s44, s44, 0x100
	s_addc_u32 s45, s45, 0
	s_add_u32 s21, s21, 0x100
	s_addc_u32 s37, s37, 0
	s_cmp_gt_u32 s67, 13
.LBB0_1124:
	ds_read_b128 v[148:151], v153
	ds_read_b128 v[156:159], v153 offset:1024
	ds_read_b128 v[160:163], v153 offset:2048
	ds_read_b128 v[164:167], v153 offset:3072
	ds_read_b128 v[172:175], v154
	ds_read_b128 v[176:179], v154 offset:1024
	ds_read_b128 v[180:183], v154 offset:2048
	ds_read_b128 v[184:187], v154 offset:3072
	s_add_u32 s46, s44, 0xfffc0080
	s_addc_u32 s47, s45, -1
	s_cmp_eq_u32 s67, 12
	s_cselect_b32 s49, s39, s47
	s_cselect_b32 s48, s38, s46
	s_cselect_b32 s47, s41, s37
	s_cselect_b32 s46, s40, s21
	s_add_i32 m0, s43, 0xc000
	ds_read_b128 v[188:191], v155
	ds_read_b128 v[192:195], v155 offset:1024
	ds_read_b128 v[196:199], v155 offset:2048
	ds_read_b128 v[200:203], v155 offset:3072
	ds_read_b128 v[204:207], v155 offset:4096
	ds_read_b128 v[208:211], v155 offset:5120
	ds_read_b128 v[212:215], v155 offset:6144
	ds_read_b128 v[216:219], v155 offset:7168
	global_load_lds_dwordx4 v140, s[44:45]
	s_add_i32 m0, s43, 0xe000
	s_nop 0
	global_load_lds_dwordx4 v142, s[44:45]
	s_waitcnt vmcnt(8)
	s_waitcnt lgkmcnt(0)
	s_barrier
	s_setprio 1
	s_waitcnt lgkmcnt(0)
	v_mfma_f32_16x16x32_bf16 v[126:129], v[148:151], v[188:191], v[126:129]
	v_mfma_f32_16x16x32_bf16 v[122:125], v[160:163], v[188:191], v[122:125]
	v_mfma_f32_16x16x32_bf16 v[118:121], v[148:151], v[196:199], v[118:121]
	v_mfma_f32_16x16x32_bf16 v[110:113], v[160:163], v[196:199], v[110:113]
	v_mfma_f32_16x16x32_bf16 v[102:105], v[148:151], v[204:207], v[102:105]
	v_mfma_f32_16x16x32_bf16 v[94:97], v[160:163], v[204:207], v[94:97]
	v_mfma_f32_16x16x32_bf16 v[86:89], v[148:151], v[212:215], v[86:89]
	v_mfma_f32_16x16x32_bf16 v[78:81], v[160:163], v[212:215], v[78:81]
	v_mfma_f32_16x16x32_bf16 v[126:129], v[156:159], v[192:195], v[126:129]
	v_mfma_f32_16x16x32_bf16 v[122:125], v[164:167], v[192:195], v[122:125]
	v_mfma_f32_16x16x32_bf16 v[118:121], v[156:159], v[200:203], v[118:121]
	v_mfma_f32_16x16x32_bf16 v[110:113], v[164:167], v[200:203], v[110:113]
	v_mfma_f32_16x16x32_bf16 v[102:105], v[156:159], v[208:211], v[102:105]
	v_mfma_f32_16x16x32_bf16 v[94:97], v[164:167], v[208:211], v[94:97]
	v_mfma_f32_16x16x32_bf16 v[86:89], v[156:159], v[216:219], v[86:89]
	v_mfma_f32_16x16x32_bf16 v[78:81], v[164:167], v[216:219], v[78:81]
	s_setprio 0
	s_setprio 1
	v_mfma_f32_16x16x32_bf16 v[114:117], v[172:175], v[188:191], v[114:117]
	v_mfma_f32_16x16x32_bf16 v[106:109], v[180:183], v[188:191], v[106:109]
	v_mfma_f32_16x16x32_bf16 v[98:101], v[172:175], v[196:199], v[98:101]
	v_mfma_f32_16x16x32_bf16 v[90:93], v[180:183], v[196:199], v[90:93]
	v_mfma_f32_16x16x32_bf16 v[82:85], v[172:175], v[204:207], v[82:85]
	v_mfma_f32_16x16x32_bf16 v[74:77], v[180:183], v[204:207], v[74:77]
	v_mfma_f32_16x16x32_bf16 v[70:73], v[172:175], v[212:215], v[70:73]
	v_mfma_f32_16x16x32_bf16 v[66:69], v[180:183], v[212:215], v[66:69]
	v_mfma_f32_16x16x32_bf16 v[114:117], v[176:179], v[192:195], v[114:117]
	v_mfma_f32_16x16x32_bf16 v[106:109], v[184:187], v[192:195], v[106:109]
	v_mfma_f32_16x16x32_bf16 v[98:101], v[176:179], v[200:203], v[98:101]
	v_mfma_f32_16x16x32_bf16 v[90:93], v[184:187], v[200:203], v[90:93]
	v_mfma_f32_16x16x32_bf16 v[82:85], v[176:179], v[208:211], v[82:85]
	v_mfma_f32_16x16x32_bf16 v[74:77], v[184:187], v[208:211], v[74:77]
	v_mfma_f32_16x16x32_bf16 v[70:73], v[176:179], v[216:219], v[70:73]
	v_mfma_f32_16x16x32_bf16 v[66:69], v[184:187], v[216:219], v[66:69]
	s_setprio 0
	s_barrier
	s_add_i32 s76, s59, s33
	s_mov_b64 s[98:99], s[46:47]
	s_mov_b32 m0, s76
	ds_read_b128 v[188:191], v155 offset:16384
	ds_read_b128 v[192:195], v155 offset:17408
	ds_read_b128 v[196:199], v155 offset:18432
	ds_read_b128 v[200:203], v155 offset:19456
	ds_read_b128 v[204:207], v155 offset:20480
	ds_read_b128 v[208:211], v155 offset:21504
	ds_read_b128 v[212:215], v155 offset:22528
	ds_read_b128 v[216:219], v155 offset:23552
	global_load_lds_dwordx4 v136, s[98:99]
	s_add_i32 m0, s76, 0x2000
	s_add_u32 s78, s46, 0x40000
	s_addc_u32 s79, s47, 0
	s_add_i32 s76, s60, s33
	global_load_lds_dwordx4 v132, s[98:99]
	s_mov_b32 m0, s76
	s_mov_b64 s[100:101], s[48:49]
	global_load_lds_dwordx4 v136, s[78:79]
	s_add_i32 m0, s76, 0x2000
	s_nop 0
	global_load_lds_dwordx4 v132, s[78:79]
	s_mov_b32 m0, s43
	s_nop 0
	global_load_lds_dwordx4 v138, s[100:101]
	s_mov_b32 m0, s52
	s_nop 0
	global_load_lds_dwordx4 v134, s[100:101]
	s_waitcnt vmcnt(8)
	s_waitcnt lgkmcnt(0)
	s_barrier
	s_setprio 1
	s_waitcnt lgkmcnt(0)
	v_mfma_f32_16x16x32_bf16 v[62:65], v[148:151], v[188:191], v[62:65]
	v_mfma_f32_16x16x32_bf16 v[58:61], v[160:163], v[188:191], v[58:61]
	v_mfma_f32_16x16x32_bf16 v[54:57], v[148:151], v[196:199], v[54:57]
	v_mfma_f32_16x16x32_bf16 v[46:49], v[160:163], v[196:199], v[46:49]
	v_mfma_f32_16x16x32_bf16 v[38:41], v[148:151], v[204:207], v[38:41]
	v_mfma_f32_16x16x32_bf16 v[30:33], v[160:163], v[204:207], v[30:33]
	v_mfma_f32_16x16x32_bf16 v[22:25], v[148:151], v[212:215], v[22:25]
	v_mfma_f32_16x16x32_bf16 v[14:17], v[160:163], v[212:215], v[14:17]
	v_mfma_f32_16x16x32_bf16 v[62:65], v[156:159], v[192:195], v[62:65]
	v_mfma_f32_16x16x32_bf16 v[58:61], v[164:167], v[192:195], v[58:61]
	v_mfma_f32_16x16x32_bf16 v[54:57], v[156:159], v[200:203], v[54:57]
	v_mfma_f32_16x16x32_bf16 v[46:49], v[164:167], v[200:203], v[46:49]
	v_mfma_f32_16x16x32_bf16 v[38:41], v[156:159], v[208:211], v[38:41]
	v_mfma_f32_16x16x32_bf16 v[30:33], v[164:167], v[208:211], v[30:33]
	v_mfma_f32_16x16x32_bf16 v[22:25], v[156:159], v[216:219], v[22:25]
	v_mfma_f32_16x16x32_bf16 v[14:17], v[164:167], v[216:219], v[14:17]
	s_setprio 0
	s_setprio 1
	v_mfma_f32_16x16x32_bf16 v[50:53], v[172:175], v[188:191], v[50:53]
	v_mfma_f32_16x16x32_bf16 v[42:45], v[180:183], v[188:191], v[42:45]
	v_mfma_f32_16x16x32_bf16 v[34:37], v[172:175], v[196:199], v[34:37]
	v_mfma_f32_16x16x32_bf16 v[26:29], v[180:183], v[196:199], v[26:29]
	v_mfma_f32_16x16x32_bf16 v[18:21], v[172:175], v[204:207], v[18:21]
	v_mfma_f32_16x16x32_bf16 v[10:13], v[180:183], v[204:207], v[10:13]
	v_mfma_f32_16x16x32_bf16 v[6:9], v[172:175], v[212:215], v[6:9]
	v_mfma_f32_16x16x32_bf16 v[2:5], v[180:183], v[212:215], v[2:5]
	v_mfma_f32_16x16x32_bf16 v[50:53], v[176:179], v[192:195], v[50:53]
	v_mfma_f32_16x16x32_bf16 v[42:45], v[184:187], v[192:195], v[42:45]
	v_mfma_f32_16x16x32_bf16 v[34:37], v[176:179], v[200:203], v[34:37]
	v_mfma_f32_16x16x32_bf16 v[26:29], v[184:187], v[200:203], v[26:29]
	v_mfma_f32_16x16x32_bf16 v[18:21], v[176:179], v[208:211], v[18:21]
	v_mfma_f32_16x16x32_bf16 v[10:13], v[184:187], v[208:211], v[10:13]
	v_mfma_f32_16x16x32_bf16 v[6:9], v[176:179], v[216:219], v[6:9]
	v_mfma_f32_16x16x32_bf16 v[2:5], v[184:187], v[216:219], v[2:5]
	s_setprio 0
	s_barrier
	s_add_i32 s76, 0, 0x18000
	s_add_i32 s78, 0, 0x1c000
	v_add_u32_e32 v164, s76, v131
	v_add_u32_e32 v184, s78, v131
	ds_read_b128 v[148:151], v164
	ds_read_b128 v[156:159], v164 offset:1024
	ds_read_b128 v[160:163], v164 offset:2048
	ds_read_b128 v[164:167], v164 offset:3072
	ds_read_b128 v[172:175], v184
	ds_read_b128 v[176:179], v184 offset:1024
	ds_read_b128 v[180:183], v184 offset:2048
	ds_read_b128 v[184:187], v184 offset:3072
	s_add_u32 s48, s48, 0x40000
	s_addc_u32 s49, s49, 0
	s_mov_b32 m0, s53
	ds_read_b128 v[188:191], v155 offset:32768
	ds_read_b128 v[192:195], v155 offset:33792
	ds_read_b128 v[196:199], v155 offset:34816
	ds_read_b128 v[200:203], v155 offset:35840
	ds_read_b128 v[204:207], v155 offset:36864
	ds_read_b128 v[208:211], v155 offset:37888
	ds_read_b128 v[212:215], v155 offset:38912
	ds_read_b128 v[216:219], v155 offset:39936
	global_load_lds_dwordx4 v138, s[48:49]
	s_mov_b32 m0, s54
	s_nop 0
	global_load_lds_dwordx4 v134, s[48:49]
	s_waitcnt vmcnt(8)
	s_waitcnt lgkmcnt(0)
	s_barrier
	s_setprio 1
	s_waitcnt lgkmcnt(0)
	v_mfma_f32_16x16x32_bf16 v[126:129], v[148:151], v[188:191], v[126:129]
	v_mfma_f32_16x16x32_bf16 v[122:125], v[160:163], v[188:191], v[122:125]
	v_mfma_f32_16x16x32_bf16 v[118:121], v[148:151], v[196:199], v[118:121]
	v_mfma_f32_16x16x32_bf16 v[110:113], v[160:163], v[196:199], v[110:113]
	v_mfma_f32_16x16x32_bf16 v[102:105], v[148:151], v[204:207], v[102:105]
	v_mfma_f32_16x16x32_bf16 v[94:97], v[160:163], v[204:207], v[94:97]
	v_mfma_f32_16x16x32_bf16 v[86:89], v[148:151], v[212:215], v[86:89]
	v_mfma_f32_16x16x32_bf16 v[78:81], v[160:163], v[212:215], v[78:81]
	v_mfma_f32_16x16x32_bf16 v[126:129], v[156:159], v[192:195], v[126:129]
	v_mfma_f32_16x16x32_bf16 v[122:125], v[164:167], v[192:195], v[122:125]
	v_mfma_f32_16x16x32_bf16 v[118:121], v[156:159], v[200:203], v[118:121]
	v_mfma_f32_16x16x32_bf16 v[110:113], v[164:167], v[200:203], v[110:113]
	v_mfma_f32_16x16x32_bf16 v[102:105], v[156:159], v[208:211], v[102:105]
	v_mfma_f32_16x16x32_bf16 v[94:97], v[164:167], v[208:211], v[94:97]
	v_mfma_f32_16x16x32_bf16 v[86:89], v[156:159], v[216:219], v[86:89]
	v_mfma_f32_16x16x32_bf16 v[78:81], v[164:167], v[216:219], v[78:81]
	s_setprio 0
	s_setprio 1
	v_mfma_f32_16x16x32_bf16 v[114:117], v[172:175], v[188:191], v[114:117]
	v_mfma_f32_16x16x32_bf16 v[106:109], v[180:183], v[188:191], v[106:109]
	v_mfma_f32_16x16x32_bf16 v[98:101], v[172:175], v[196:199], v[98:101]
	v_mfma_f32_16x16x32_bf16 v[90:93], v[180:183], v[196:199], v[90:93]
	v_mfma_f32_16x16x32_bf16 v[82:85], v[172:175], v[204:207], v[82:85]
	v_mfma_f32_16x16x32_bf16 v[74:77], v[180:183], v[204:207], v[74:77]
	v_mfma_f32_16x16x32_bf16 v[70:73], v[172:175], v[212:215], v[70:73]
	v_mfma_f32_16x16x32_bf16 v[66:69], v[180:183], v[212:215], v[66:69]
	v_mfma_f32_16x16x32_bf16 v[114:117], v[176:179], v[192:195], v[114:117]
	v_mfma_f32_16x16x32_bf16 v[106:109], v[184:187], v[192:195], v[106:109]
	v_mfma_f32_16x16x32_bf16 v[98:101], v[176:179], v[200:203], v[98:101]
	v_mfma_f32_16x16x32_bf16 v[90:93], v[184:187], v[200:203], v[90:93]
	v_mfma_f32_16x16x32_bf16 v[82:85], v[176:179], v[208:211], v[82:85]
	v_mfma_f32_16x16x32_bf16 v[74:77], v[184:187], v[208:211], v[74:77]
	v_mfma_f32_16x16x32_bf16 v[70:73], v[176:179], v[216:219], v[70:73]
	v_mfma_f32_16x16x32_bf16 v[66:69], v[184:187], v[216:219], v[66:69]
	s_setprio 0
	s_barrier
	s_add_i32 s48, s76, s33
	s_mov_b32 m0, s48
	ds_read_b128 v[188:191], v155 offset:49152
	ds_read_b128 v[192:195], v155 offset:50176
	ds_read_b128 v[196:199], v155 offset:51200
	ds_read_b128 v[200:203], v155 offset:52224
	ds_read_b128 v[204:207], v155 offset:53248
	ds_read_b128 v[208:211], v155 offset:54272
	ds_read_b128 v[212:215], v155 offset:55296
	ds_read_b128 v[216:219], v155 offset:56320
	s_add_u32 s98, s98, 0x80
	s_addc_u32 s99, s99, 0
	global_load_lds_dwordx4 v136, s[98:99]
	s_add_i32 m0, s48, 0x2000
	s_add_u32 s46, s46, 0x40080
	s_addc_u32 s47, s47, 0
	s_add_i32 s48, s78, s33
	global_load_lds_dwordx4 v132, s[98:99]
	s_mov_b32 m0, s48
	s_nop 0
	global_load_lds_dwordx4 v136, s[46:47]
	s_add_i32 m0, s48, 0x2000
	s_nop 0
	global_load_lds_dwordx4 v132, s[46:47]
	s_mov_b32 m0, s56
	s_nop 0
	s_add_u32 s100, s100, 0x80
	s_addc_u32 s101, s101, 0
	global_load_lds_dwordx4 v138, s[100:101]
	s_mov_b32 m0, s57
	s_nop 0
	global_load_lds_dwordx4 v134, s[100:101]
	s_waitcnt vmcnt(8)
	s_waitcnt lgkmcnt(0)
	s_barrier
	s_setprio 1
	s_waitcnt lgkmcnt(0)
	v_mfma_f32_16x16x32_bf16 v[62:65], v[148:151], v[188:191], v[62:65]
	v_mfma_f32_16x16x32_bf16 v[58:61], v[160:163], v[188:191], v[58:61]
	v_mfma_f32_16x16x32_bf16 v[54:57], v[148:151], v[196:199], v[54:57]
	v_mfma_f32_16x16x32_bf16 v[46:49], v[160:163], v[196:199], v[46:49]
	v_mfma_f32_16x16x32_bf16 v[38:41], v[148:151], v[204:207], v[38:41]
	v_mfma_f32_16x16x32_bf16 v[30:33], v[160:163], v[204:207], v[30:33]
	v_mfma_f32_16x16x32_bf16 v[22:25], v[148:151], v[212:215], v[22:25]
	v_mfma_f32_16x16x32_bf16 v[14:17], v[160:163], v[212:215], v[14:17]
	v_mfma_f32_16x16x32_bf16 v[62:65], v[156:159], v[192:195], v[62:65]
	v_mfma_f32_16x16x32_bf16 v[58:61], v[164:167], v[192:195], v[58:61]
	v_mfma_f32_16x16x32_bf16 v[54:57], v[156:159], v[200:203], v[54:57]
	v_mfma_f32_16x16x32_bf16 v[46:49], v[164:167], v[200:203], v[46:49]
	v_mfma_f32_16x16x32_bf16 v[38:41], v[156:159], v[208:211], v[38:41]
	v_mfma_f32_16x16x32_bf16 v[30:33], v[164:167], v[208:211], v[30:33]
	v_mfma_f32_16x16x32_bf16 v[22:25], v[156:159], v[216:219], v[22:25]
	v_mfma_f32_16x16x32_bf16 v[14:17], v[164:167], v[216:219], v[14:17]
	s_setprio 0
	s_setprio 1
	v_mfma_f32_16x16x32_bf16 v[50:53], v[172:175], v[188:191], v[50:53]
	v_mfma_f32_16x16x32_bf16 v[42:45], v[180:183], v[188:191], v[42:45]
	v_mfma_f32_16x16x32_bf16 v[34:37], v[172:175], v[196:199], v[34:37]
	v_mfma_f32_16x16x32_bf16 v[26:29], v[180:183], v[196:199], v[26:29]
	v_mfma_f32_16x16x32_bf16 v[18:21], v[172:175], v[204:207], v[18:21]
	v_mfma_f32_16x16x32_bf16 v[10:13], v[180:183], v[204:207], v[10:13]
	v_mfma_f32_16x16x32_bf16 v[6:9], v[172:175], v[212:215], v[6:9]
	v_mfma_f32_16x16x32_bf16 v[2:5], v[180:183], v[212:215], v[2:5]
	v_mfma_f32_16x16x32_bf16 v[50:53], v[176:179], v[192:195], v[50:53]
	v_mfma_f32_16x16x32_bf16 v[42:45], v[184:187], v[192:195], v[42:45]
	v_mfma_f32_16x16x32_bf16 v[34:37], v[176:179], v[200:203], v[34:37]
	v_mfma_f32_16x16x32_bf16 v[26:29], v[184:187], v[200:203], v[26:29]
	v_mfma_f32_16x16x32_bf16 v[18:21], v[176:179], v[208:211], v[18:21]
	v_mfma_f32_16x16x32_bf16 v[10:13], v[184:187], v[208:211], v[10:13]
	v_mfma_f32_16x16x32_bf16 v[6:9], v[176:179], v[216:219], v[6:9]
	v_mfma_f32_16x16x32_bf16 v[2:5], v[184:187], v[216:219], v[2:5]
	s_setprio 0
	s_barrier
	s_add_i32 s67, s67, 2
	s_add_u32 s44, s44, 0x100
	s_addc_u32 s45, s45, 0
	s_add_u32 s21, s21, 0x100
	s_addc_u32 s37, s37, 0
	s_cmp_gt_u32 s67, 13
	s_cbranch_scc0 .LBB0_1124
	s_and_b64 vcc, exec, s[18:19]
	s_cbranch_vccz .LBB0_1127
	s_barrier

.LBB0_1630:
	s_add_u32 s18, s18, 0x50080
	s_addc_u32 s19, s19, 0
	s_add_u32 s55, s20, 0x100
	s_addc_u32 s56, s21, 0
	s_mov_b32 s57, -2
	ds_read_b128 v[118:121], v168
	ds_read_b128 v[126:129], v168 offset:1024
	ds_read_b128 v[130:133], v168 offset:2048
	ds_read_b128 v[134:137], v168 offset:3072
	ds_read_b128 v[162:165], v169
	ds_read_b128 v[172:175], v169 offset:1024
	ds_read_b128 v[176:179], v169 offset:2048
	ds_read_b128 v[180:183], v169 offset:3072
	s_add_u32 s20, s18, 0xfffb0080
	s_addc_u32 s21, s19, -1
	s_cmp_eq_u32 s57, 16
	s_cselect_b32 s37, s13, s21
	s_cselect_b32 s36, s12, s20
	s_cselect_b32 s21, s17, s56
	s_cselect_b32 s20, s16, s55
	s_add_i32 m0, s35, 0xc000
	ds_read_b128 v[184:187], v171
	ds_read_b128 v[188:191], v171 offset:1024
	ds_read_b128 v[192:195], v171 offset:2048
	ds_read_b128 v[196:199], v171 offset:3072
	ds_read_b128 v[200:203], v171 offset:4096
	ds_read_b128 v[204:207], v171 offset:5120
	ds_read_b128 v[208:211], v171 offset:6144
	ds_read_b128 v[212:215], v171 offset:7168
	global_load_lds_dwordx4 v154, s[18:19]
	s_add_i32 m0, s35, 0xe000
	s_nop 0
	global_load_lds_dwordx4 v156, s[18:19]
	s_waitcnt vmcnt(8)
	s_waitcnt lgkmcnt(0)
	s_barrier
	s_setprio 1
	s_waitcnt lgkmcnt(0)
	v_mfma_f32_16x16x32_bf16 v[142:145], v[118:121], v[184:187], 0
	v_mfma_f32_16x16x32_bf16 v[138:141], v[130:133], v[184:187], 0
	v_mfma_f32_16x16x32_bf16 v[114:117], v[118:121], v[192:195], 0
	v_mfma_f32_16x16x32_bf16 v[106:109], v[130:133], v[192:195], 0
	v_mfma_f32_16x16x32_bf16 v[98:101], v[118:121], v[200:203], 0
	v_mfma_f32_16x16x32_bf16 v[90:93], v[130:133], v[200:203], 0
	v_mfma_f32_16x16x32_bf16 v[82:85], v[118:121], v[208:211], 0
	v_mfma_f32_16x16x32_bf16 v[74:77], v[130:133], v[208:211], 0
	v_mfma_f32_16x16x32_bf16 v[142:145], v[126:129], v[188:191], v[142:145]
	v_mfma_f32_16x16x32_bf16 v[138:141], v[134:137], v[188:191], v[138:141]
	v_mfma_f32_16x16x32_bf16 v[114:117], v[126:129], v[196:199], v[114:117]
	v_mfma_f32_16x16x32_bf16 v[106:109], v[134:137], v[196:199], v[106:109]
	v_mfma_f32_16x16x32_bf16 v[98:101], v[126:129], v[204:207], v[98:101]
	v_mfma_f32_16x16x32_bf16 v[90:93], v[134:137], v[204:207], v[90:93]
	v_mfma_f32_16x16x32_bf16 v[82:85], v[126:129], v[212:215], v[82:85]
	v_mfma_f32_16x16x32_bf16 v[74:77], v[134:137], v[212:215], v[74:77]
	s_setprio 0
	s_setprio 1
	v_mfma_f32_16x16x32_bf16 v[122:125], v[162:165], v[184:187], 0
	v_mfma_f32_16x16x32_bf16 v[110:113], v[176:179], v[184:187], 0
	v_mfma_f32_16x16x32_bf16 v[102:105], v[162:165], v[192:195], 0
	v_mfma_f32_16x16x32_bf16 v[94:97], v[176:179], v[192:195], 0
	v_mfma_f32_16x16x32_bf16 v[86:89], v[162:165], v[200:203], 0
	v_mfma_f32_16x16x32_bf16 v[78:81], v[176:179], v[200:203], 0
	v_mfma_f32_16x16x32_bf16 v[70:73], v[162:165], v[208:211], 0
	v_mfma_f32_16x16x32_bf16 v[66:69], v[176:179], v[208:211], 0
	v_mfma_f32_16x16x32_bf16 v[122:125], v[172:175], v[188:191], v[122:125]
	v_mfma_f32_16x16x32_bf16 v[110:113], v[180:183], v[188:191], v[110:113]
	v_mfma_f32_16x16x32_bf16 v[102:105], v[172:175], v[196:199], v[102:105]
	v_mfma_f32_16x16x32_bf16 v[94:97], v[180:183], v[196:199], v[94:97]
	v_mfma_f32_16x16x32_bf16 v[86:89], v[172:175], v[204:207], v[86:89]
	v_mfma_f32_16x16x32_bf16 v[78:81], v[180:183], v[204:207], v[78:81]
	v_mfma_f32_16x16x32_bf16 v[70:73], v[172:175], v[212:215], v[70:73]
	v_mfma_f32_16x16x32_bf16 v[66:69], v[180:183], v[212:215], v[66:69]
	s_setprio 0
	s_barrier
	s_add_i32 s58, s47, s34
	s_mov_b64 s[98:99], s[20:21]
	s_mov_b32 m0, s58
	ds_read_b128 v[184:187], v171 offset:16384
	ds_read_b128 v[188:191], v171 offset:17408
	ds_read_b128 v[192:195], v171 offset:18432
	ds_read_b128 v[196:199], v171 offset:19456
	ds_read_b128 v[200:203], v171 offset:20480
	ds_read_b128 v[204:207], v171 offset:21504
	ds_read_b128 v[208:211], v171 offset:22528
	ds_read_b128 v[212:215], v171 offset:23552
	global_load_lds_dwordx4 v148, s[98:99]
	s_add_i32 m0, s58, 0x2000
	s_add_u32 s58, s20, 0x50000
	s_addc_u32 s59, s21, 0
	s_add_i32 s60, s48, s34
	global_load_lds_dwordx4 v152, s[98:99]
	s_mov_b32 m0, s60
	s_mov_b64 s[100:101], s[36:37]
	global_load_lds_dwordx4 v148, s[58:59]
	s_add_i32 m0, s60, 0x2000
	s_nop 0
	global_load_lds_dwordx4 v152, s[58:59]
	s_mov_b32 m0, s35
	s_nop 0
	global_load_lds_dwordx4 v146, s[100:101]
	s_mov_b32 m0, s38
	s_nop 0
	global_load_lds_dwordx4 v150, s[100:101]
	s_waitcnt vmcnt(8)
	s_waitcnt lgkmcnt(0)
	s_barrier
	s_setprio 1
	s_waitcnt lgkmcnt(0)
	v_mfma_f32_16x16x32_bf16 v[62:65], v[118:121], v[184:187], 0
	v_mfma_f32_16x16x32_bf16 v[58:61], v[130:133], v[184:187], 0
	v_mfma_f32_16x16x32_bf16 v[50:53], v[118:121], v[192:195], 0
	v_mfma_f32_16x16x32_bf16 v[42:45], v[130:133], v[192:195], 0
	v_mfma_f32_16x16x32_bf16 v[34:37], v[118:121], v[200:203], 0
	v_mfma_f32_16x16x32_bf16 v[26:29], v[130:133], v[200:203], 0
	v_mfma_f32_16x16x32_bf16 v[18:21], v[118:121], v[208:211], 0
	v_mfma_f32_16x16x32_bf16 v[10:13], v[130:133], v[208:211], 0
	v_mfma_f32_16x16x32_bf16 v[62:65], v[126:129], v[188:191], v[62:65]
	v_mfma_f32_16x16x32_bf16 v[58:61], v[134:137], v[188:191], v[58:61]
	v_mfma_f32_16x16x32_bf16 v[50:53], v[126:129], v[196:199], v[50:53]
	v_mfma_f32_16x16x32_bf16 v[42:45], v[134:137], v[196:199], v[42:45]
	v_mfma_f32_16x16x32_bf16 v[34:37], v[126:129], v[204:207], v[34:37]
	v_mfma_f32_16x16x32_bf16 v[26:29], v[134:137], v[204:207], v[26:29]
	v_mfma_f32_16x16x32_bf16 v[18:21], v[126:129], v[212:215], v[18:21]
	v_mfma_f32_16x16x32_bf16 v[10:13], v[134:137], v[212:215], v[10:13]
	s_setprio 0
	s_setprio 1
	v_mfma_f32_16x16x32_bf16 v[54:57], v[162:165], v[184:187], 0
	v_mfma_f32_16x16x32_bf16 v[46:49], v[176:179], v[184:187], 0
	v_mfma_f32_16x16x32_bf16 v[38:41], v[162:165], v[192:195], 0
	v_mfma_f32_16x16x32_bf16 v[30:33], v[176:179], v[192:195], 0
	v_mfma_f32_16x16x32_bf16 v[22:25], v[162:165], v[200:203], 0
	v_mfma_f32_16x16x32_bf16 v[14:17], v[176:179], v[200:203], 0
	v_mfma_f32_16x16x32_bf16 v[6:9], v[162:165], v[208:211], 0
	v_mfma_f32_16x16x32_bf16 v[2:5], v[176:179], v[208:211], 0
	v_mfma_f32_16x16x32_bf16 v[54:57], v[172:175], v[188:191], v[54:57]
	v_mfma_f32_16x16x32_bf16 v[46:49], v[180:183], v[188:191], v[46:49]
	v_mfma_f32_16x16x32_bf16 v[38:41], v[172:175], v[196:199], v[38:41]
	v_mfma_f32_16x16x32_bf16 v[30:33], v[180:183], v[196:199], v[30:33]
	v_mfma_f32_16x16x32_bf16 v[22:25], v[172:175], v[204:207], v[22:25]
	v_mfma_f32_16x16x32_bf16 v[14:17], v[180:183], v[204:207], v[14:17]
	v_mfma_f32_16x16x32_bf16 v[6:9], v[172:175], v[212:215], v[6:9]
	v_mfma_f32_16x16x32_bf16 v[2:5], v[180:183], v[212:215], v[2:5]
	s_setprio 0
	s_barrier
	s_add_i32 s58, 0, 0x18000
	s_add_i32 s59, 0, 0x1c000
	v_add_u32_e32 v134, s58, v166
	v_add_u32_e32 v170, s59, v166
	ds_read_b128 v[118:121], v134
	ds_read_b128 v[126:129], v134 offset:1024
	ds_read_b128 v[130:133], v134 offset:2048
	ds_read_b128 v[134:137], v134 offset:3072
	ds_read_b128 v[162:165], v170
	ds_read_b128 v[172:175], v170 offset:1024
	ds_read_b128 v[176:179], v170 offset:2048
	ds_read_b128 v[180:183], v170 offset:3072
	s_add_u32 s36, s36, 0x50000
	s_addc_u32 s37, s37, 0
	s_mov_b32 m0, s39
	ds_read_b128 v[184:187], v171 offset:32768
	ds_read_b128 v[188:191], v171 offset:33792
	ds_read_b128 v[192:195], v171 offset:34816
	ds_read_b128 v[196:199], v171 offset:35840
	ds_read_b128 v[200:203], v171 offset:36864
	ds_read_b128 v[204:207], v171 offset:37888
	ds_read_b128 v[208:211], v171 offset:38912
	ds_read_b128 v[212:215], v171 offset:39936
	global_load_lds_dwordx4 v146, s[36:37]
	s_mov_b32 m0, s40
	s_nop 0
	global_load_lds_dwordx4 v150, s[36:37]
	s_waitcnt vmcnt(8)
	s_waitcnt lgkmcnt(0)
	s_barrier
	s_setprio 1
	s_waitcnt lgkmcnt(0)
	v_mfma_f32_16x16x32_bf16 v[142:145], v[118:121], v[184:187], v[142:145]
	v_mfma_f32_16x16x32_bf16 v[138:141], v[130:133], v[184:187], v[138:141]
	v_mfma_f32_16x16x32_bf16 v[114:117], v[118:121], v[192:195], v[114:117]
	v_mfma_f32_16x16x32_bf16 v[106:109], v[130:133], v[192:195], v[106:109]
	v_mfma_f32_16x16x32_bf16 v[98:101], v[118:121], v[200:203], v[98:101]
	v_mfma_f32_16x16x32_bf16 v[90:93], v[130:133], v[200:203], v[90:93]
	v_mfma_f32_16x16x32_bf16 v[82:85], v[118:121], v[208:211], v[82:85]
	v_mfma_f32_16x16x32_bf16 v[74:77], v[130:133], v[208:211], v[74:77]
	v_mfma_f32_16x16x32_bf16 v[142:145], v[126:129], v[188:191], v[142:145]
	v_mfma_f32_16x16x32_bf16 v[138:141], v[134:137], v[188:191], v[138:141]
	v_mfma_f32_16x16x32_bf16 v[114:117], v[126:129], v[196:199], v[114:117]
	v_mfma_f32_16x16x32_bf16 v[106:109], v[134:137], v[196:199], v[106:109]
	v_mfma_f32_16x16x32_bf16 v[98:101], v[126:129], v[204:207], v[98:101]
	v_mfma_f32_16x16x32_bf16 v[90:93], v[134:137], v[204:207], v[90:93]
	v_mfma_f32_16x16x32_bf16 v[82:85], v[126:129], v[212:215], v[82:85]
	v_mfma_f32_16x16x32_bf16 v[74:77], v[134:137], v[212:215], v[74:77]
	s_setprio 0
	s_setprio 1
	v_mfma_f32_16x16x32_bf16 v[122:125], v[162:165], v[184:187], v[122:125]
	v_mfma_f32_16x16x32_bf16 v[110:113], v[176:179], v[184:187], v[110:113]
	v_mfma_f32_16x16x32_bf16 v[102:105], v[162:165], v[192:195], v[102:105]
	v_mfma_f32_16x16x32_bf16 v[94:97], v[176:179], v[192:195], v[94:97]
	v_mfma_f32_16x16x32_bf16 v[86:89], v[162:165], v[200:203], v[86:89]
	v_mfma_f32_16x16x32_bf16 v[78:81], v[176:179], v[200:203], v[78:81]
	v_mfma_f32_16x16x32_bf16 v[70:73], v[162:165], v[208:211], v[70:73]
	v_mfma_f32_16x16x32_bf16 v[66:69], v[176:179], v[208:211], v[66:69]
	v_mfma_f32_16x16x32_bf16 v[122:125], v[172:175], v[188:191], v[122:125]
	v_mfma_f32_16x16x32_bf16 v[110:113], v[180:183], v[188:191], v[110:113]
	v_mfma_f32_16x16x32_bf16 v[102:105], v[172:175], v[196:199], v[102:105]
	v_mfma_f32_16x16x32_bf16 v[94:97], v[180:183], v[196:199], v[94:97]
	v_mfma_f32_16x16x32_bf16 v[86:89], v[172:175], v[204:207], v[86:89]
	v_mfma_f32_16x16x32_bf16 v[78:81], v[180:183], v[204:207], v[78:81]
	v_mfma_f32_16x16x32_bf16 v[70:73], v[172:175], v[212:215], v[70:73]
	v_mfma_f32_16x16x32_bf16 v[66:69], v[180:183], v[212:215], v[66:69]
	s_setprio 0
	s_barrier
	s_add_i32 s36, s58, s34
	s_mov_b32 m0, s36
	ds_read_b128 v[184:187], v171 offset:49152
	ds_read_b128 v[188:191], v171 offset:50176
	ds_read_b128 v[192:195], v171 offset:51200
	ds_read_b128 v[196:199], v171 offset:52224
	ds_read_b128 v[200:203], v171 offset:53248
	ds_read_b128 v[204:207], v171 offset:54272
	ds_read_b128 v[208:211], v171 offset:55296
	ds_read_b128 v[212:215], v171 offset:56320
	s_add_u32 s98, s98, 0x80
	s_addc_u32 s99, s99, 0
	global_load_lds_dwordx4 v148, s[98:99]
	s_add_i32 m0, s36, 0x2000
	s_add_u32 s20, s20, 0x50080
	s_addc_u32 s21, s21, 0
	s_add_i32 s36, s59, s34
	global_load_lds_dwordx4 v152, s[98:99]
	s_mov_b32 m0, s36
	s_nop 0
	global_load_lds_dwordx4 v148, s[20:21]
	s_add_i32 m0, s36, 0x2000
	s_nop 0
	global_load_lds_dwordx4 v152, s[20:21]
	s_mov_b32 m0, s44
	s_nop 0
	s_add_u32 s100, s100, 0x80
	s_addc_u32 s101, s101, 0
	global_load_lds_dwordx4 v146, s[100:101]
	s_mov_b32 m0, s45
	s_nop 0
	global_load_lds_dwordx4 v150, s[100:101]
	s_waitcnt vmcnt(8)
	s_waitcnt lgkmcnt(0)
	s_barrier
	s_setprio 1
	s_waitcnt lgkmcnt(0)
	v_mfma_f32_16x16x32_bf16 v[62:65], v[118:121], v[184:187], v[62:65]
	v_mfma_f32_16x16x32_bf16 v[58:61], v[130:133], v[184:187], v[58:61]
	v_mfma_f32_16x16x32_bf16 v[50:53], v[118:121], v[192:195], v[50:53]
	v_mfma_f32_16x16x32_bf16 v[42:45], v[130:133], v[192:195], v[42:45]
	v_mfma_f32_16x16x32_bf16 v[34:37], v[118:121], v[200:203], v[34:37]
	v_mfma_f32_16x16x32_bf16 v[26:29], v[130:133], v[200:203], v[26:29]
	v_mfma_f32_16x16x32_bf16 v[18:21], v[118:121], v[208:211], v[18:21]
	v_mfma_f32_16x16x32_bf16 v[10:13], v[130:133], v[208:211], v[10:13]
	v_mfma_f32_16x16x32_bf16 v[62:65], v[126:129], v[188:191], v[62:65]
	v_mfma_f32_16x16x32_bf16 v[58:61], v[134:137], v[188:191], v[58:61]
	v_mfma_f32_16x16x32_bf16 v[50:53], v[126:129], v[196:199], v[50:53]
	v_mfma_f32_16x16x32_bf16 v[42:45], v[134:137], v[196:199], v[42:45]
	v_mfma_f32_16x16x32_bf16 v[34:37], v[126:129], v[204:207], v[34:37]
	v_mfma_f32_16x16x32_bf16 v[26:29], v[134:137], v[204:207], v[26:29]
	v_mfma_f32_16x16x32_bf16 v[18:21], v[126:129], v[212:215], v[18:21]
	v_mfma_f32_16x16x32_bf16 v[10:13], v[134:137], v[212:215], v[10:13]
	s_setprio 0
	s_setprio 1
	v_mfma_f32_16x16x32_bf16 v[54:57], v[162:165], v[184:187], v[54:57]
	v_mfma_f32_16x16x32_bf16 v[46:49], v[176:179], v[184:187], v[46:49]
	v_mfma_f32_16x16x32_bf16 v[38:41], v[162:165], v[192:195], v[38:41]
	v_mfma_f32_16x16x32_bf16 v[30:33], v[176:179], v[192:195], v[30:33]
	v_mfma_f32_16x16x32_bf16 v[22:25], v[162:165], v[200:203], v[22:25]
	v_mfma_f32_16x16x32_bf16 v[14:17], v[176:179], v[200:203], v[14:17]
	v_mfma_f32_16x16x32_bf16 v[6:9], v[162:165], v[208:211], v[6:9]
	v_mfma_f32_16x16x32_bf16 v[2:5], v[176:179], v[208:211], v[2:5]
	v_mfma_f32_16x16x32_bf16 v[54:57], v[172:175], v[188:191], v[54:57]
	v_mfma_f32_16x16x32_bf16 v[46:49], v[180:183], v[188:191], v[46:49]
	v_mfma_f32_16x16x32_bf16 v[38:41], v[172:175], v[196:199], v[38:41]
	v_mfma_f32_16x16x32_bf16 v[30:33], v[180:183], v[196:199], v[30:33]
	v_mfma_f32_16x16x32_bf16 v[22:25], v[172:175], v[204:207], v[22:25]
	v_mfma_f32_16x16x32_bf16 v[14:17], v[180:183], v[204:207], v[14:17]
	v_mfma_f32_16x16x32_bf16 v[6:9], v[172:175], v[212:215], v[6:9]
	v_mfma_f32_16x16x32_bf16 v[2:5], v[180:183], v[212:215], v[2:5]
	s_setprio 0
	s_barrier
	s_add_i32 s57, s57, 2
	s_add_u32 s18, s18, 0x100
	s_addc_u32 s19, s19, 0
	s_add_u32 s55, s55, 0x100
	s_addc_u32 s56, s56, 0
	s_cmp_gt_u32 s57, 17
.LBB0_1631:
	ds_read_b128 v[118:121], v168
	ds_read_b128 v[126:129], v168 offset:1024
	ds_read_b128 v[130:133], v168 offset:2048
	ds_read_b128 v[134:137], v168 offset:3072
	ds_read_b128 v[162:165], v169
	ds_read_b128 v[172:175], v169 offset:1024
	ds_read_b128 v[176:179], v169 offset:2048
	ds_read_b128 v[180:183], v169 offset:3072
	s_add_u32 s20, s18, 0xfffb0080
	s_addc_u32 s21, s19, -1
	s_cmp_eq_u32 s57, 16
	s_cselect_b32 s37, s13, s21
	s_cselect_b32 s36, s12, s20
	s_cselect_b32 s21, s17, s56
	s_cselect_b32 s20, s16, s55
	s_add_i32 m0, s35, 0xc000
	ds_read_b128 v[184:187], v171
	ds_read_b128 v[188:191], v171 offset:1024
	ds_read_b128 v[192:195], v171 offset:2048
	ds_read_b128 v[196:199], v171 offset:3072
	ds_read_b128 v[200:203], v171 offset:4096
	ds_read_b128 v[204:207], v171 offset:5120
	ds_read_b128 v[208:211], v171 offset:6144
	ds_read_b128 v[212:215], v171 offset:7168
	global_load_lds_dwordx4 v154, s[18:19]
	s_add_i32 m0, s35, 0xe000
	s_nop 0
	global_load_lds_dwordx4 v156, s[18:19]
	s_waitcnt vmcnt(8)
	s_waitcnt lgkmcnt(0)
	s_barrier
	s_setprio 1
	s_waitcnt lgkmcnt(0)
	v_mfma_f32_16x16x32_bf16 v[142:145], v[118:121], v[184:187], v[142:145]
	v_mfma_f32_16x16x32_bf16 v[138:141], v[130:133], v[184:187], v[138:141]
	v_mfma_f32_16x16x32_bf16 v[114:117], v[118:121], v[192:195], v[114:117]
	v_mfma_f32_16x16x32_bf16 v[106:109], v[130:133], v[192:195], v[106:109]
	v_mfma_f32_16x16x32_bf16 v[98:101], v[118:121], v[200:203], v[98:101]
	v_mfma_f32_16x16x32_bf16 v[90:93], v[130:133], v[200:203], v[90:93]
	v_mfma_f32_16x16x32_bf16 v[82:85], v[118:121], v[208:211], v[82:85]
	v_mfma_f32_16x16x32_bf16 v[74:77], v[130:133], v[208:211], v[74:77]
	v_mfma_f32_16x16x32_bf16 v[142:145], v[126:129], v[188:191], v[142:145]
	v_mfma_f32_16x16x32_bf16 v[138:141], v[134:137], v[188:191], v[138:141]
	v_mfma_f32_16x16x32_bf16 v[114:117], v[126:129], v[196:199], v[114:117]
	v_mfma_f32_16x16x32_bf16 v[106:109], v[134:137], v[196:199], v[106:109]
	v_mfma_f32_16x16x32_bf16 v[98:101], v[126:129], v[204:207], v[98:101]
	v_mfma_f32_16x16x32_bf16 v[90:93], v[134:137], v[204:207], v[90:93]
	v_mfma_f32_16x16x32_bf16 v[82:85], v[126:129], v[212:215], v[82:85]
	v_mfma_f32_16x16x32_bf16 v[74:77], v[134:137], v[212:215], v[74:77]
	s_setprio 0
	s_setprio 1
	v_mfma_f32_16x16x32_bf16 v[122:125], v[162:165], v[184:187], v[122:125]
	v_mfma_f32_16x16x32_bf16 v[110:113], v[176:179], v[184:187], v[110:113]
	v_mfma_f32_16x16x32_bf16 v[102:105], v[162:165], v[192:195], v[102:105]
	v_mfma_f32_16x16x32_bf16 v[94:97], v[176:179], v[192:195], v[94:97]
	v_mfma_f32_16x16x32_bf16 v[86:89], v[162:165], v[200:203], v[86:89]
	v_mfma_f32_16x16x32_bf16 v[78:81], v[176:179], v[200:203], v[78:81]
	v_mfma_f32_16x16x32_bf16 v[70:73], v[162:165], v[208:211], v[70:73]
	v_mfma_f32_16x16x32_bf16 v[66:69], v[176:179], v[208:211], v[66:69]
	v_mfma_f32_16x16x32_bf16 v[122:125], v[172:175], v[188:191], v[122:125]
	v_mfma_f32_16x16x32_bf16 v[110:113], v[180:183], v[188:191], v[110:113]
	v_mfma_f32_16x16x32_bf16 v[102:105], v[172:175], v[196:199], v[102:105]
	v_mfma_f32_16x16x32_bf16 v[94:97], v[180:183], v[196:199], v[94:97]
	v_mfma_f32_16x16x32_bf16 v[86:89], v[172:175], v[204:207], v[86:89]
	v_mfma_f32_16x16x32_bf16 v[78:81], v[180:183], v[204:207], v[78:81]
	v_mfma_f32_16x16x32_bf16 v[70:73], v[172:175], v[212:215], v[70:73]
	v_mfma_f32_16x16x32_bf16 v[66:69], v[180:183], v[212:215], v[66:69]
	s_setprio 0
	s_barrier
	s_add_i32 s58, s47, s34
	s_mov_b64 s[98:99], s[20:21]
	s_mov_b32 m0, s58
	ds_read_b128 v[184:187], v171 offset:16384
	ds_read_b128 v[188:191], v171 offset:17408
	ds_read_b128 v[192:195], v171 offset:18432
	ds_read_b128 v[196:199], v171 offset:19456
	ds_read_b128 v[200:203], v171 offset:20480
	ds_read_b128 v[204:207], v171 offset:21504
	ds_read_b128 v[208:211], v171 offset:22528
	ds_read_b128 v[212:215], v171 offset:23552
	global_load_lds_dwordx4 v148, s[98:99]
	s_add_i32 m0, s58, 0x2000
	s_add_u32 s58, s20, 0x50000
	s_addc_u32 s59, s21, 0
	s_add_i32 s60, s48, s34
	global_load_lds_dwordx4 v152, s[98:99]
	s_mov_b32 m0, s60
	s_mov_b64 s[100:101], s[36:37]
	global_load_lds_dwordx4 v148, s[58:59]
	s_add_i32 m0, s60, 0x2000
	s_nop 0
	global_load_lds_dwordx4 v152, s[58:59]
	s_mov_b32 m0, s35
	s_nop 0
	global_load_lds_dwordx4 v146, s[100:101]
	s_mov_b32 m0, s38
	s_nop 0
	global_load_lds_dwordx4 v150, s[100:101]
	s_waitcnt vmcnt(8)
	s_waitcnt lgkmcnt(0)
	s_barrier
	s_setprio 1
	s_waitcnt lgkmcnt(0)
	v_mfma_f32_16x16x32_bf16 v[62:65], v[118:121], v[184:187], v[62:65]
	v_mfma_f32_16x16x32_bf16 v[58:61], v[130:133], v[184:187], v[58:61]
	v_mfma_f32_16x16x32_bf16 v[50:53], v[118:121], v[192:195], v[50:53]
	v_mfma_f32_16x16x32_bf16 v[42:45], v[130:133], v[192:195], v[42:45]
	v_mfma_f32_16x16x32_bf16 v[34:37], v[118:121], v[200:203], v[34:37]
	v_mfma_f32_16x16x32_bf16 v[26:29], v[130:133], v[200:203], v[26:29]
	v_mfma_f32_16x16x32_bf16 v[18:21], v[118:121], v[208:211], v[18:21]
	v_mfma_f32_16x16x32_bf16 v[10:13], v[130:133], v[208:211], v[10:13]
	v_mfma_f32_16x16x32_bf16 v[62:65], v[126:129], v[188:191], v[62:65]
	v_mfma_f32_16x16x32_bf16 v[58:61], v[134:137], v[188:191], v[58:61]
	v_mfma_f32_16x16x32_bf16 v[50:53], v[126:129], v[196:199], v[50:53]
	v_mfma_f32_16x16x32_bf16 v[42:45], v[134:137], v[196:199], v[42:45]
	v_mfma_f32_16x16x32_bf16 v[34:37], v[126:129], v[204:207], v[34:37]
	v_mfma_f32_16x16x32_bf16 v[26:29], v[134:137], v[204:207], v[26:29]
	v_mfma_f32_16x16x32_bf16 v[18:21], v[126:129], v[212:215], v[18:21]
	v_mfma_f32_16x16x32_bf16 v[10:13], v[134:137], v[212:215], v[10:13]
	s_setprio 0
	s_setprio 1
	v_mfma_f32_16x16x32_bf16 v[54:57], v[162:165], v[184:187], v[54:57]
	v_mfma_f32_16x16x32_bf16 v[46:49], v[176:179], v[184:187], v[46:49]
	v_mfma_f32_16x16x32_bf16 v[38:41], v[162:165], v[192:195], v[38:41]
	v_mfma_f32_16x16x32_bf16 v[30:33], v[176:179], v[192:195], v[30:33]
	v_mfma_f32_16x16x32_bf16 v[22:25], v[162:165], v[200:203], v[22:25]
	v_mfma_f32_16x16x32_bf16 v[14:17], v[176:179], v[200:203], v[14:17]
	v_mfma_f32_16x16x32_bf16 v[6:9], v[162:165], v[208:211], v[6:9]
	v_mfma_f32_16x16x32_bf16 v[2:5], v[176:179], v[208:211], v[2:5]
	v_mfma_f32_16x16x32_bf16 v[54:57], v[172:175], v[188:191], v[54:57]
	v_mfma_f32_16x16x32_bf16 v[46:49], v[180:183], v[188:191], v[46:49]
	v_mfma_f32_16x16x32_bf16 v[38:41], v[172:175], v[196:199], v[38:41]
	v_mfma_f32_16x16x32_bf16 v[30:33], v[180:183], v[196:199], v[30:33]
	v_mfma_f32_16x16x32_bf16 v[22:25], v[172:175], v[204:207], v[22:25]
	v_mfma_f32_16x16x32_bf16 v[14:17], v[180:183], v[204:207], v[14:17]
	v_mfma_f32_16x16x32_bf16 v[6:9], v[172:175], v[212:215], v[6:9]
	v_mfma_f32_16x16x32_bf16 v[2:5], v[180:183], v[212:215], v[2:5]
	s_setprio 0
	s_barrier
	s_add_i32 s58, 0, 0x18000
	s_add_i32 s59, 0, 0x1c000
	v_add_u32_e32 v134, s58, v166
	v_add_u32_e32 v170, s59, v166
	ds_read_b128 v[118:121], v134
	ds_read_b128 v[126:129], v134 offset:1024
	ds_read_b128 v[130:133], v134 offset:2048
	ds_read_b128 v[134:137], v134 offset:3072
	ds_read_b128 v[162:165], v170
	ds_read_b128 v[172:175], v170 offset:1024
	ds_read_b128 v[176:179], v170 offset:2048
	ds_read_b128 v[180:183], v170 offset:3072
	s_add_u32 s36, s36, 0x50000
	s_addc_u32 s37, s37, 0
	s_mov_b32 m0, s39
	ds_read_b128 v[184:187], v171 offset:32768
	ds_read_b128 v[188:191], v171 offset:33792
	ds_read_b128 v[192:195], v171 offset:34816
	ds_read_b128 v[196:199], v171 offset:35840
	ds_read_b128 v[200:203], v171 offset:36864
	ds_read_b128 v[204:207], v171 offset:37888
	ds_read_b128 v[208:211], v171 offset:38912
	ds_read_b128 v[212:215], v171 offset:39936
	global_load_lds_dwordx4 v146, s[36:37]
	s_mov_b32 m0, s40
	s_nop 0
	global_load_lds_dwordx4 v150, s[36:37]
	s_waitcnt vmcnt(8)
	s_waitcnt lgkmcnt(0)
	s_barrier
	s_setprio 1
	s_waitcnt lgkmcnt(0)
	v_mfma_f32_16x16x32_bf16 v[142:145], v[118:121], v[184:187], v[142:145]
	v_mfma_f32_16x16x32_bf16 v[138:141], v[130:133], v[184:187], v[138:141]
	v_mfma_f32_16x16x32_bf16 v[114:117], v[118:121], v[192:195], v[114:117]
	v_mfma_f32_16x16x32_bf16 v[106:109], v[130:133], v[192:195], v[106:109]
	v_mfma_f32_16x16x32_bf16 v[98:101], v[118:121], v[200:203], v[98:101]
	v_mfma_f32_16x16x32_bf16 v[90:93], v[130:133], v[200:203], v[90:93]
	v_mfma_f32_16x16x32_bf16 v[82:85], v[118:121], v[208:211], v[82:85]
	v_mfma_f32_16x16x32_bf16 v[74:77], v[130:133], v[208:211], v[74:77]
	v_mfma_f32_16x16x32_bf16 v[142:145], v[126:129], v[188:191], v[142:145]
	v_mfma_f32_16x16x32_bf16 v[138:141], v[134:137], v[188:191], v[138:141]
	v_mfma_f32_16x16x32_bf16 v[114:117], v[126:129], v[196:199], v[114:117]
	v_mfma_f32_16x16x32_bf16 v[106:109], v[134:137], v[196:199], v[106:109]
	v_mfma_f32_16x16x32_bf16 v[98:101], v[126:129], v[204:207], v[98:101]
	v_mfma_f32_16x16x32_bf16 v[90:93], v[134:137], v[204:207], v[90:93]
	v_mfma_f32_16x16x32_bf16 v[82:85], v[126:129], v[212:215], v[82:85]
	v_mfma_f32_16x16x32_bf16 v[74:77], v[134:137], v[212:215], v[74:77]
	s_setprio 0
	s_setprio 1
	v_mfma_f32_16x16x32_bf16 v[122:125], v[162:165], v[184:187], v[122:125]
	v_mfma_f32_16x16x32_bf16 v[110:113], v[176:179], v[184:187], v[110:113]
	v_mfma_f32_16x16x32_bf16 v[102:105], v[162:165], v[192:195], v[102:105]
	v_mfma_f32_16x16x32_bf16 v[94:97], v[176:179], v[192:195], v[94:97]
	v_mfma_f32_16x16x32_bf16 v[86:89], v[162:165], v[200:203], v[86:89]
	v_mfma_f32_16x16x32_bf16 v[78:81], v[176:179], v[200:203], v[78:81]
	v_mfma_f32_16x16x32_bf16 v[70:73], v[162:165], v[208:211], v[70:73]
	v_mfma_f32_16x16x32_bf16 v[66:69], v[176:179], v[208:211], v[66:69]
	v_mfma_f32_16x16x32_bf16 v[122:125], v[172:175], v[188:191], v[122:125]
	v_mfma_f32_16x16x32_bf16 v[110:113], v[180:183], v[188:191], v[110:113]
	v_mfma_f32_16x16x32_bf16 v[102:105], v[172:175], v[196:199], v[102:105]
	v_mfma_f32_16x16x32_bf16 v[94:97], v[180:183], v[196:199], v[94:97]
	v_mfma_f32_16x16x32_bf16 v[86:89], v[172:175], v[204:207], v[86:89]
	v_mfma_f32_16x16x32_bf16 v[78:81], v[180:183], v[204:207], v[78:81]
	v_mfma_f32_16x16x32_bf16 v[70:73], v[172:175], v[212:215], v[70:73]
	v_mfma_f32_16x16x32_bf16 v[66:69], v[180:183], v[212:215], v[66:69]
	s_setprio 0
	s_barrier
	s_add_i32 s36, s58, s34
	s_mov_b32 m0, s36
	ds_read_b128 v[184:187], v171 offset:49152
	ds_read_b128 v[188:191], v171 offset:50176
	ds_read_b128 v[192:195], v171 offset:51200
	ds_read_b128 v[196:199], v171 offset:52224
	ds_read_b128 v[200:203], v171 offset:53248
	ds_read_b128 v[204:207], v171 offset:54272
	ds_read_b128 v[208:211], v171 offset:55296
	ds_read_b128 v[212:215], v171 offset:56320
	s_add_u32 s98, s98, 0x80
	s_addc_u32 s99, s99, 0
	global_load_lds_dwordx4 v148, s[98:99]
	s_add_i32 m0, s36, 0x2000
	s_add_u32 s20, s20, 0x50080
	s_addc_u32 s21, s21, 0
	s_add_i32 s36, s59, s34
	global_load_lds_dwordx4 v152, s[98:99]
	s_mov_b32 m0, s36
	s_nop 0
	global_load_lds_dwordx4 v148, s[20:21]
	s_add_i32 m0, s36, 0x2000
	s_nop 0
	global_load_lds_dwordx4 v152, s[20:21]
	s_mov_b32 m0, s44
	s_nop 0
	s_add_u32 s100, s100, 0x80
	s_addc_u32 s101, s101, 0
	global_load_lds_dwordx4 v146, s[100:101]
	s_mov_b32 m0, s45
	s_nop 0
	global_load_lds_dwordx4 v150, s[100:101]
	s_waitcnt vmcnt(8)
	s_waitcnt lgkmcnt(0)
	s_barrier
	s_setprio 1
	s_waitcnt lgkmcnt(0)
	v_mfma_f32_16x16x32_bf16 v[62:65], v[118:121], v[184:187], v[62:65]
	v_mfma_f32_16x16x32_bf16 v[58:61], v[130:133], v[184:187], v[58:61]
	v_mfma_f32_16x16x32_bf16 v[50:53], v[118:121], v[192:195], v[50:53]
	v_mfma_f32_16x16x32_bf16 v[42:45], v[130:133], v[192:195], v[42:45]
	v_mfma_f32_16x16x32_bf16 v[34:37], v[118:121], v[200:203], v[34:37]
	v_mfma_f32_16x16x32_bf16 v[26:29], v[130:133], v[200:203], v[26:29]
	v_mfma_f32_16x16x32_bf16 v[18:21], v[118:121], v[208:211], v[18:21]
	v_mfma_f32_16x16x32_bf16 v[10:13], v[130:133], v[208:211], v[10:13]
	v_mfma_f32_16x16x32_bf16 v[62:65], v[126:129], v[188:191], v[62:65]
	v_mfma_f32_16x16x32_bf16 v[58:61], v[134:137], v[188:191], v[58:61]
	v_mfma_f32_16x16x32_bf16 v[50:53], v[126:129], v[196:199], v[50:53]
	v_mfma_f32_16x16x32_bf16 v[42:45], v[134:137], v[196:199], v[42:45]
	v_mfma_f32_16x16x32_bf16 v[34:37], v[126:129], v[204:207], v[34:37]
	v_mfma_f32_16x16x32_bf16 v[26:29], v[134:137], v[204:207], v[26:29]
	v_mfma_f32_16x16x32_bf16 v[18:21], v[126:129], v[212:215], v[18:21]
	v_mfma_f32_16x16x32_bf16 v[10:13], v[134:137], v[212:215], v[10:13]
	s_setprio 0
	s_setprio 1
	v_mfma_f32_16x16x32_bf16 v[54:57], v[162:165], v[184:187], v[54:57]
	v_mfma_f32_16x16x32_bf16 v[46:49], v[176:179], v[184:187], v[46:49]
	v_mfma_f32_16x16x32_bf16 v[38:41], v[162:165], v[192:195], v[38:41]
	v_mfma_f32_16x16x32_bf16 v[30:33], v[176:179], v[192:195], v[30:33]
	v_mfma_f32_16x16x32_bf16 v[22:25], v[162:165], v[200:203], v[22:25]
	v_mfma_f32_16x16x32_bf16 v[14:17], v[176:179], v[200:203], v[14:17]
	v_mfma_f32_16x16x32_bf16 v[6:9], v[162:165], v[208:211], v[6:9]
	v_mfma_f32_16x16x32_bf16 v[2:5], v[176:179], v[208:211], v[2:5]
	v_mfma_f32_16x16x32_bf16 v[54:57], v[172:175], v[188:191], v[54:57]
	v_mfma_f32_16x16x32_bf16 v[46:49], v[180:183], v[188:191], v[46:49]
	v_mfma_f32_16x16x32_bf16 v[38:41], v[172:175], v[196:199], v[38:41]
	v_mfma_f32_16x16x32_bf16 v[30:33], v[180:183], v[196:199], v[30:33]
	v_mfma_f32_16x16x32_bf16 v[22:25], v[172:175], v[204:207], v[22:25]
	v_mfma_f32_16x16x32_bf16 v[14:17], v[180:183], v[204:207], v[14:17]
	v_mfma_f32_16x16x32_bf16 v[6:9], v[172:175], v[212:215], v[6:9]
	v_mfma_f32_16x16x32_bf16 v[2:5], v[180:183], v[212:215], v[2:5]
	s_setprio 0
	s_barrier
	s_add_i32 s57, s57, 2
	s_add_u32 s18, s18, 0x100
	s_addc_u32 s19, s19, 0
	s_add_u32 s55, s55, 0x100
	s_addc_u32 s56, s56, 0
	s_cmp_gt_u32 s57, 17
	s_cbranch_scc0 .LBB0_1631
	s_and_b64 vcc, exec, s[10:11]
	s_cbranch_vccz .LBB0_1634
	s_barrier

.LBB0_1910:
	v_add_u32_e32 v6, s62, v171
	v_add_u32_e32 v2, v6, v192
	v_ashrrev_i32_e32 v3, 31, v2
	v_add_u32_e32 v6, v6, v193
	v_lshl_add_u64 v[4:5], v[2:3], 2, s[10:11]
	v_add_u32_e32 v2, 0x80, v2
	v_ashrrev_i32_e32 v7, 31, v6
	v_ashrrev_i32_e32 v3, 31, v2
	v_lshl_add_u64 v[8:9], v[6:7], 2, s[10:11]
	v_add_u32_e32 v6, 0x80, v6
	v_lshl_add_u64 v[2:3], v[2:3], 2, s[10:11]
	v_ashrrev_i32_e32 v7, 31, v6
	v_lshl_add_u64 v[6:7], v[6:7], 2, s[10:11]
	global_load_dword v236, v[4:5], off
	s_nop 0
	global_load_dword v237, v[2:3], off
	s_nop 0
	global_load_dword v238, v[8:9], off
	global_load_dword v239, v[6:7], off
	v_mov_b32_e32 v175, v169
	v_mov_b32_e32 v179, v169
	s_add_u32 s37, s42, 0x100
	s_mov_b32 s79, -2
	s_mov_b64 s[46:47], 0
	s_addc_u32 s80, s43, 0
	v_lshl_add_u64 v[180:181], s[18:19], 0, v[174:175]
	v_lshl_add_u64 v[182:183], s[18:19], 0, v[178:179]
	ds_read_b128 v[18:21], v197
	ds_read_b128 v[22:25], v197 offset:1024
	ds_read_b128 v[26:29], v197 offset:2048
	ds_read_b128 v[30:33], v197 offset:3072
	ds_read_b128 v[2:5], v198
	ds_read_b128 v[6:9], v198 offset:1024
	ds_read_b128 v[10:13], v198 offset:2048
	ds_read_b128 v[14:17], v198 offset:3072
	s_add_u32 s42, s46, 0x100
	s_addc_u32 s43, s47, 0
	s_add_u32 s48, s37, s46
	s_addc_u32 s49, s80, s47
	s_cmpk_eq_i32 s46, 0x300
	s_cselect_b64 vcc, -1, 0
	s_and_b64 s[44:45], vcc, exec
	s_cselect_b32 s81, 0, s42
	s_cselect_b32 s76, 0, s43
	s_cselect_b32 s44, s38, s48
	s_cselect_b32 s45, s39, s49
	s_add_u32 s48, s8, s81
	s_addc_u32 s49, s9, s76
	v_lshl_add_u64 v[228:229], v[180:181], 0, s[46:47]
	s_add_i32 m0, s41, 0xc000
	ds_read_b128 v[184:187], v199
	ds_read_b128 v[188:191], v199 offset:1024
	ds_read_b128 v[204:207], v199 offset:2048
	ds_read_b128 v[208:211], v199 offset:3072
	ds_read_b128 v[212:215], v199 offset:4096
	ds_read_b128 v[216:219], v199 offset:5120
	ds_read_b128 v[220:223], v199 offset:6144
	ds_read_b128 v[224:227], v199 offset:7168
	global_load_lds_dwordx4 v[228:229], off
	v_lshl_add_u64 v[228:229], v[182:183], 0, s[46:47]
	s_add_i32 m0, s41, 0xe000
	s_nop 0
	global_load_lds_dwordx4 v[228:229], off
	s_waitcnt vmcnt(8)
	s_waitcnt lgkmcnt(0)
	s_barrier
	s_setprio 1
	s_waitcnt lgkmcnt(0)
	v_mfma_f32_16x16x128_f8f6f4 v[158:161], v[18:25], v[184:191], 0
	v_mfma_f32_16x16x128_f8f6f4 v[150:153], v[26:33], v[184:191], 0
	v_mfma_f32_16x16x128_f8f6f4 v[142:145], v[18:25], v[204:211], 0
	v_mfma_f32_16x16x128_f8f6f4 v[134:137], v[26:33], v[204:211], 0
	v_mfma_f32_16x16x128_f8f6f4 v[126:129], v[18:25], v[212:219], 0
	v_mfma_f32_16x16x128_f8f6f4 v[118:121], v[26:33], v[212:219], 0
	v_mfma_f32_16x16x128_f8f6f4 v[110:113], v[18:25], v[220:227], 0
	v_mfma_f32_16x16x128_f8f6f4 v[102:105], v[26:33], v[220:227], 0
	s_setprio 0
	s_setprio 1
	v_mfma_f32_16x16x128_f8f6f4 v[154:157], v[2:9], v[184:191], 0
	v_mfma_f32_16x16x128_f8f6f4 v[146:149], v[10:17], v[184:191], 0
	v_mfma_f32_16x16x128_f8f6f4 v[138:141], v[2:9], v[204:211], 0
	v_mfma_f32_16x16x128_f8f6f4 v[130:133], v[10:17], v[204:211], 0
	v_mfma_f32_16x16x128_f8f6f4 v[122:125], v[2:9], v[212:219], 0
	v_mfma_f32_16x16x128_f8f6f4 v[114:117], v[10:17], v[212:219], 0
	v_mfma_f32_16x16x128_f8f6f4 v[106:109], v[2:9], v[220:227], 0
	v_mfma_f32_16x16x128_f8f6f4 v[98:101], v[10:17], v[220:227], 0
	s_setprio 0
	s_barrier
	s_add_i32 s46, s5, s52
	s_mov_b64 s[98:99], s[44:45]
	s_mov_b32 m0, s46
	ds_read_b128 v[204:207], v199 offset:16384
	ds_read_b128 v[208:211], v199 offset:17408
	ds_read_b128 v[212:215], v199 offset:18432
	ds_read_b128 v[216:219], v199 offset:19456
	ds_read_b128 v[220:223], v199 offset:20480
	ds_read_b128 v[224:227], v199 offset:21504
	ds_read_b128 v[228:231], v199 offset:22528
	ds_read_b128 v[232:235], v199 offset:23552
	global_load_lds_dwordx4 v164, s[98:99]
	s_add_i32 m0, s46, 0x2000
	s_add_u32 s46, s44, 0x20000
	s_addc_u32 s47, s45, 0
	s_add_i32 s76, s66, s52
	global_load_lds_dwordx4 v166, s[98:99]
	s_mov_b32 m0, s76
	v_cndmask_b32_e32 v168, v202, v179, vcc
	global_load_lds_dwordx4 v164, s[46:47]
	v_lshl_add_u64 v[188:189], s[46:47], 0, v[166:167]
	s_add_i32 m0, s76, 0x2000
	v_lshl_add_u64 v[190:191], s[48:49], 0, v[168:169]
	global_load_lds_dwordx4 v166, s[46:47]
	s_mov_b32 m0, s41
	v_cndmask_b32_e32 v188, v176, v201, vcc
	global_load_lds_dwordx4 v168, s[48:49]
	s_mov_b32 m0, s53
	v_mov_b32_e32 v189, v169
	global_load_lds_dwordx4 v188, s[48:49]
	s_waitcnt vmcnt(8)
	s_waitcnt lgkmcnt(0)
	v_lshl_add_u64 v[188:189], s[48:49], 0, v[188:189]
	s_barrier
	s_setprio 1
	s_waitcnt lgkmcnt(0)
	v_mfma_f32_16x16x128_f8f6f4 v[94:97], v[18:25], v[204:211], 0
	v_mfma_f32_16x16x128_f8f6f4 v[86:89], v[26:33], v[204:211], 0
	v_mfma_f32_16x16x128_f8f6f4 v[78:81], v[18:25], v[212:219], 0
	v_mfma_f32_16x16x128_f8f6f4 v[70:73], v[26:33], v[212:219], 0
	v_mfma_f32_16x16x128_f8f6f4 v[58:61], v[18:25], v[220:227], 0
	v_mfma_f32_16x16x128_f8f6f4 v[46:49], v[26:33], v[220:227], 0
	v_mfma_f32_16x16x128_f8f6f4 v[38:41], v[18:25], v[228:235], 0
	v_mfma_f32_16x16x128_f8f6f4 v[34:37], v[26:33], v[228:235], 0
	s_setprio 0
	s_setprio 1
	v_mfma_f32_16x16x128_f8f6f4 v[90:93], v[2:9], v[204:211], 0
	v_mfma_f32_16x16x128_f8f6f4 v[82:85], v[10:17], v[204:211], 0
	v_mfma_f32_16x16x128_f8f6f4 v[74:77], v[2:9], v[212:219], 0
	v_mfma_f32_16x16x128_f8f6f4 v[66:69], v[10:17], v[212:219], 0
	v_mfma_f32_16x16x128_f8f6f4 v[50:53], v[2:9], v[220:227], 0
	v_mfma_f32_16x16x128_f8f6f4 v[42:45], v[10:17], v[220:227], 0
	v_mfma_f32_16x16x128_f8f6f4 v[62:65], v[2:9], v[228:235], 0
	v_mfma_f32_16x16x128_f8f6f4 v[54:57], v[10:17], v[228:235], 0
	s_setprio 0
	s_barrier
	s_add_i32 s46, 0, 0x18000
	s_add_i32 s47, 0, 0x1c000
	v_add_u32_e32 v14, s46, v177
	v_add_u32_e32 v30, s47, v177
	ds_read_b128 v[2:5], v14
	ds_read_b128 v[6:9], v14 offset:1024
	ds_read_b128 v[10:13], v14 offset:2048
	ds_read_b128 v[14:17], v14 offset:3072
	ds_read_b128 v[18:21], v30
	ds_read_b128 v[22:25], v30 offset:1024
	ds_read_b128 v[26:29], v30 offset:2048
	ds_read_b128 v[30:33], v30 offset:3072
	s_mov_b32 m0, s59
	v_cndmask_b32_e32 v168, v174, v175, vcc
	ds_read_b128 v[204:207], v199 offset:32768
	ds_read_b128 v[208:211], v199 offset:33792
	ds_read_b128 v[212:215], v199 offset:34816
	ds_read_b128 v[216:219], v199 offset:35840
	ds_read_b128 v[220:223], v199 offset:36864
	ds_read_b128 v[224:227], v199 offset:37888
	ds_read_b128 v[228:231], v199 offset:38912
	ds_read_b128 v[232:235], v199 offset:39936
	v_cndmask_b32_e32 v170, v178, v200, vcc
	global_load_lds_dwordx4 v168, s[48:49]
	s_mov_b32 m0, s60
	s_nop 0
	global_load_lds_dwordx4 v170, s[48:49]
	s_waitcnt vmcnt(8)
	s_waitcnt lgkmcnt(0)
	s_barrier
	s_setprio 1
	s_waitcnt lgkmcnt(0)
	v_mfma_f32_16x16x128_f8f6f4 v[158:161], v[2:9], v[204:211], v[158:161]
	v_mfma_f32_16x16x128_f8f6f4 v[150:153], v[10:17], v[204:211], v[150:153]
	v_mfma_f32_16x16x128_f8f6f4 v[142:145], v[2:9], v[212:219], v[142:145]
	v_mfma_f32_16x16x128_f8f6f4 v[134:137], v[10:17], v[212:219], v[134:137]
	v_mfma_f32_16x16x128_f8f6f4 v[126:129], v[2:9], v[220:227], v[126:129]
	v_mfma_f32_16x16x128_f8f6f4 v[118:121], v[10:17], v[220:227], v[118:121]
	v_mfma_f32_16x16x128_f8f6f4 v[110:113], v[2:9], v[228:235], v[110:113]
	v_mfma_f32_16x16x128_f8f6f4 v[102:105], v[10:17], v[228:235], v[102:105]
	s_setprio 0
	s_setprio 1
	v_mfma_f32_16x16x128_f8f6f4 v[154:157], v[18:25], v[204:211], v[154:157]
	v_mfma_f32_16x16x128_f8f6f4 v[146:149], v[26:33], v[204:211], v[146:149]
	v_mfma_f32_16x16x128_f8f6f4 v[138:141], v[18:25], v[212:219], v[138:141]
	v_mfma_f32_16x16x128_f8f6f4 v[130:133], v[26:33], v[212:219], v[130:133]
	v_mfma_f32_16x16x128_f8f6f4 v[122:125], v[18:25], v[220:227], v[122:125]
	v_mfma_f32_16x16x128_f8f6f4 v[114:117], v[26:33], v[220:227], v[114:117]
	v_mfma_f32_16x16x128_f8f6f4 v[106:109], v[18:25], v[228:235], v[106:109]
	v_mfma_f32_16x16x128_f8f6f4 v[98:101], v[26:33], v[228:235], v[98:101]
	s_setprio 0
	s_barrier
	s_add_i32 s46, s46, s52
	s_mov_b32 m0, s46
	ds_read_b128 v[204:207], v199 offset:49152
	ds_read_b128 v[208:211], v199 offset:50176
	ds_read_b128 v[212:215], v199 offset:51200
	ds_read_b128 v[216:219], v199 offset:52224
	ds_read_b128 v[220:223], v199 offset:53248
	ds_read_b128 v[224:227], v199 offset:54272
	ds_read_b128 v[228:231], v199 offset:55296
	ds_read_b128 v[232:235], v199 offset:56320
	s_add_u32 s98, s98, 0x80
	s_addc_u32 s99, s99, 0
	global_load_lds_dwordx4 v164, s[98:99]
	s_add_i32 m0, s46, 0x2000
	s_add_u32 s44, s44, 0x20080
	s_addc_u32 s45, s45, 0
	s_add_i32 s46, s47, s52
	global_load_lds_dwordx4 v166, s[98:99]
	s_mov_b32 m0, s46
	s_nop 0
	global_load_lds_dwordx4 v164, s[44:45]
	s_add_i32 m0, s46, 0x2000
	s_nop 0
	global_load_lds_dwordx4 v166, s[44:45]
	v_lshl_add_u64 v[184:185], v[190:191], 0, s[16:17]
	s_mov_b32 m0, s63
	s_nop 0
	global_load_lds_dwordx4 v[184:185], off
	v_lshl_add_u64 v[184:185], v[188:189], 0, s[16:17]
	s_mov_b32 m0, s64
	s_nop 0
	global_load_lds_dwordx4 v[184:185], off
	s_waitcnt vmcnt(8)
	s_waitcnt lgkmcnt(0)
	s_barrier
	s_setprio 1
	s_waitcnt lgkmcnt(0)
	v_mfma_f32_16x16x128_f8f6f4 v[94:97], v[2:9], v[204:211], v[94:97]
	v_mfma_f32_16x16x128_f8f6f4 v[86:89], v[10:17], v[204:211], v[86:89]
	v_mfma_f32_16x16x128_f8f6f4 v[78:81], v[2:9], v[212:219], v[78:81]
	v_mfma_f32_16x16x128_f8f6f4 v[70:73], v[10:17], v[212:219], v[70:73]
	v_mfma_f32_16x16x128_f8f6f4 v[58:61], v[2:9], v[220:227], v[58:61]
	v_mfma_f32_16x16x128_f8f6f4 v[46:49], v[10:17], v[220:227], v[46:49]
	v_mfma_f32_16x16x128_f8f6f4 v[38:41], v[2:9], v[228:235], v[38:41]
	v_mfma_f32_16x16x128_f8f6f4 v[34:37], v[10:17], v[228:235], v[34:37]
	s_setprio 0
	s_setprio 1
	v_mfma_f32_16x16x128_f8f6f4 v[90:93], v[18:25], v[204:211], v[90:93]
	v_mfma_f32_16x16x128_f8f6f4 v[82:85], v[26:33], v[204:211], v[82:85]
	v_mfma_f32_16x16x128_f8f6f4 v[74:77], v[18:25], v[212:219], v[74:77]
	v_mfma_f32_16x16x128_f8f6f4 v[66:69], v[26:33], v[212:219], v[66:69]
	v_mfma_f32_16x16x128_f8f6f4 v[50:53], v[18:25], v[220:227], v[50:53]
	v_mfma_f32_16x16x128_f8f6f4 v[42:45], v[26:33], v[220:227], v[42:45]
	v_mfma_f32_16x16x128_f8f6f4 v[62:65], v[18:25], v[228:235], v[62:65]
	v_mfma_f32_16x16x128_f8f6f4 v[54:57], v[26:33], v[228:235], v[54:57]
	s_setprio 0
	s_barrier
	s_add_i32 s79, s79, 2
	s_cmp_gt_u32 s79, 5
	s_mov_b64 s[46:47], s[42:43]
.LBB0_1911:
	ds_read_b128 v[18:21], v197
	ds_read_b128 v[22:25], v197 offset:1024
	ds_read_b128 v[26:29], v197 offset:2048
	ds_read_b128 v[30:33], v197 offset:3072
	ds_read_b128 v[2:5], v198
	ds_read_b128 v[6:9], v198 offset:1024
	ds_read_b128 v[10:13], v198 offset:2048
	ds_read_b128 v[14:17], v198 offset:3072
	s_add_u32 s42, s46, 0x100
	s_addc_u32 s43, s47, 0
	s_add_u32 s48, s37, s46
	s_addc_u32 s49, s80, s47
	s_cmpk_eq_i32 s46, 0x300
	s_cselect_b64 vcc, -1, 0
	s_and_b64 s[44:45], vcc, exec
	s_cselect_b32 s81, 0, s42
	s_cselect_b32 s76, 0, s43
	s_cselect_b32 s44, s38, s48
	s_cselect_b32 s45, s39, s49
	s_add_u32 s48, s8, s81
	s_addc_u32 s49, s9, s76
	v_lshl_add_u64 v[228:229], v[180:181], 0, s[46:47]
	s_add_i32 m0, s41, 0xc000
	ds_read_b128 v[184:187], v199
	ds_read_b128 v[188:191], v199 offset:1024
	ds_read_b128 v[204:207], v199 offset:2048
	ds_read_b128 v[208:211], v199 offset:3072
	ds_read_b128 v[212:215], v199 offset:4096
	ds_read_b128 v[216:219], v199 offset:5120
	ds_read_b128 v[220:223], v199 offset:6144
	ds_read_b128 v[224:227], v199 offset:7168
	global_load_lds_dwordx4 v[228:229], off
	v_lshl_add_u64 v[228:229], v[182:183], 0, s[46:47]
	s_add_i32 m0, s41, 0xe000
	s_nop 0
	global_load_lds_dwordx4 v[228:229], off
	s_waitcnt vmcnt(8)
	s_waitcnt lgkmcnt(0)
	s_barrier
	s_setprio 1
	s_waitcnt lgkmcnt(0)
	v_mfma_f32_16x16x128_f8f6f4 v[158:161], v[18:25], v[184:191], v[158:161]
	v_mfma_f32_16x16x128_f8f6f4 v[150:153], v[26:33], v[184:191], v[150:153]
	v_mfma_f32_16x16x128_f8f6f4 v[142:145], v[18:25], v[204:211], v[142:145]
	v_mfma_f32_16x16x128_f8f6f4 v[134:137], v[26:33], v[204:211], v[134:137]
	v_mfma_f32_16x16x128_f8f6f4 v[126:129], v[18:25], v[212:219], v[126:129]
	v_mfma_f32_16x16x128_f8f6f4 v[118:121], v[26:33], v[212:219], v[118:121]
	v_mfma_f32_16x16x128_f8f6f4 v[110:113], v[18:25], v[220:227], v[110:113]
	v_mfma_f32_16x16x128_f8f6f4 v[102:105], v[26:33], v[220:227], v[102:105]
	s_setprio 0
	s_setprio 1
	v_mfma_f32_16x16x128_f8f6f4 v[154:157], v[2:9], v[184:191], v[154:157]
	v_mfma_f32_16x16x128_f8f6f4 v[146:149], v[10:17], v[184:191], v[146:149]
	v_mfma_f32_16x16x128_f8f6f4 v[138:141], v[2:9], v[204:211], v[138:141]
	v_mfma_f32_16x16x128_f8f6f4 v[130:133], v[10:17], v[204:211], v[130:133]
	v_mfma_f32_16x16x128_f8f6f4 v[122:125], v[2:9], v[212:219], v[122:125]
	v_mfma_f32_16x16x128_f8f6f4 v[114:117], v[10:17], v[212:219], v[114:117]
	v_mfma_f32_16x16x128_f8f6f4 v[106:109], v[2:9], v[220:227], v[106:109]
	v_mfma_f32_16x16x128_f8f6f4 v[98:101], v[10:17], v[220:227], v[98:101]
	s_setprio 0
	s_barrier
	s_add_i32 s46, s5, s52
	s_mov_b64 s[98:99], s[44:45]
	s_mov_b32 m0, s46
	ds_read_b128 v[204:207], v199 offset:16384
	ds_read_b128 v[208:211], v199 offset:17408
	ds_read_b128 v[212:215], v199 offset:18432
	ds_read_b128 v[216:219], v199 offset:19456
	ds_read_b128 v[220:223], v199 offset:20480
	ds_read_b128 v[224:227], v199 offset:21504
	ds_read_b128 v[228:231], v199 offset:22528
	ds_read_b128 v[232:235], v199 offset:23552
	global_load_lds_dwordx4 v164, s[98:99]
	s_add_i32 m0, s46, 0x2000
	s_add_u32 s46, s44, 0x20000
	s_addc_u32 s47, s45, 0
	s_add_i32 s76, s66, s52
	global_load_lds_dwordx4 v166, s[98:99]
	s_mov_b32 m0, s76
	v_cndmask_b32_e32 v168, v202, v179, vcc
	global_load_lds_dwordx4 v164, s[46:47]
	v_lshl_add_u64 v[188:189], s[46:47], 0, v[166:167]
	s_add_i32 m0, s76, 0x2000
	v_lshl_add_u64 v[190:191], s[48:49], 0, v[168:169]
	global_load_lds_dwordx4 v166, s[46:47]
	s_mov_b32 m0, s41
	v_cndmask_b32_e32 v188, v176, v201, vcc
	global_load_lds_dwordx4 v168, s[48:49]
	s_mov_b32 m0, s53
	v_mov_b32_e32 v189, v169
	global_load_lds_dwordx4 v188, s[48:49]
	s_waitcnt vmcnt(8)
	s_waitcnt lgkmcnt(0)
	v_lshl_or_b32 v179, v236, 10, v194
	v_lshl_or_b32 v175, v237, 10, v194
	v_lshl_or_b32 v201, v238, 10, v194
	v_lshl_or_b32 v200, v239, 10, v194
	v_lshl_add_u64 v[188:189], s[48:49], 0, v[188:189]
	s_barrier
	s_setprio 1
	s_waitcnt lgkmcnt(0)
	v_mfma_f32_16x16x128_f8f6f4 v[94:97], v[18:25], v[204:211], v[94:97]
	v_mfma_f32_16x16x128_f8f6f4 v[86:89], v[26:33], v[204:211], v[86:89]
	v_mfma_f32_16x16x128_f8f6f4 v[78:81], v[18:25], v[212:219], v[78:81]
	v_mfma_f32_16x16x128_f8f6f4 v[70:73], v[26:33], v[212:219], v[70:73]
	v_mfma_f32_16x16x128_f8f6f4 v[58:61], v[18:25], v[220:227], v[58:61]
	v_mfma_f32_16x16x128_f8f6f4 v[46:49], v[26:33], v[220:227], v[46:49]
	v_mfma_f32_16x16x128_f8f6f4 v[38:41], v[18:25], v[228:235], v[38:41]
	v_mfma_f32_16x16x128_f8f6f4 v[34:37], v[26:33], v[228:235], v[34:37]
	s_setprio 0
	s_setprio 1
	v_mfma_f32_16x16x128_f8f6f4 v[90:93], v[2:9], v[204:211], v[90:93]
	v_mfma_f32_16x16x128_f8f6f4 v[82:85], v[10:17], v[204:211], v[82:85]
	v_mfma_f32_16x16x128_f8f6f4 v[74:77], v[2:9], v[212:219], v[74:77]
	v_mfma_f32_16x16x128_f8f6f4 v[66:69], v[10:17], v[212:219], v[66:69]
	v_mfma_f32_16x16x128_f8f6f4 v[50:53], v[2:9], v[220:227], v[50:53]
	v_mfma_f32_16x16x128_f8f6f4 v[42:45], v[10:17], v[220:227], v[42:45]
	v_mfma_f32_16x16x128_f8f6f4 v[62:65], v[2:9], v[228:235], v[62:65]
	v_mfma_f32_16x16x128_f8f6f4 v[54:57], v[10:17], v[228:235], v[54:57]
	s_setprio 0
	s_barrier
	s_add_i32 s46, 0, 0x18000
	s_add_i32 s47, 0, 0x1c000
	v_add_u32_e32 v14, s46, v177
	v_add_u32_e32 v30, s47, v177
	ds_read_b128 v[2:5], v14
	ds_read_b128 v[6:9], v14 offset:1024
	ds_read_b128 v[10:13], v14 offset:2048
	ds_read_b128 v[14:17], v14 offset:3072
	ds_read_b128 v[18:21], v30
	ds_read_b128 v[22:25], v30 offset:1024
	ds_read_b128 v[26:29], v30 offset:2048
	ds_read_b128 v[30:33], v30 offset:3072
	s_mov_b32 m0, s59
	v_cndmask_b32_e32 v168, v174, v175, vcc
	ds_read_b128 v[204:207], v199 offset:32768
	ds_read_b128 v[208:211], v199 offset:33792
	ds_read_b128 v[212:215], v199 offset:34816
	ds_read_b128 v[216:219], v199 offset:35840
	ds_read_b128 v[220:223], v199 offset:36864
	ds_read_b128 v[224:227], v199 offset:37888
	ds_read_b128 v[228:231], v199 offset:38912
	ds_read_b128 v[232:235], v199 offset:39936
	v_cndmask_b32_e32 v170, v178, v200, vcc
	global_load_lds_dwordx4 v168, s[48:49]
	s_mov_b32 m0, s60
	s_nop 0
	global_load_lds_dwordx4 v170, s[48:49]
	s_waitcnt vmcnt(8)
	s_waitcnt lgkmcnt(0)
	s_barrier
	s_setprio 1
	s_waitcnt lgkmcnt(0)
	v_mfma_f32_16x16x128_f8f6f4 v[158:161], v[2:9], v[204:211], v[158:161]
	v_mfma_f32_16x16x128_f8f6f4 v[150:153], v[10:17], v[204:211], v[150:153]
	v_mfma_f32_16x16x128_f8f6f4 v[142:145], v[2:9], v[212:219], v[142:145]
	v_mfma_f32_16x16x128_f8f6f4 v[134:137], v[10:17], v[212:219], v[134:137]
	v_mfma_f32_16x16x128_f8f6f4 v[126:129], v[2:9], v[220:227], v[126:129]
	v_mfma_f32_16x16x128_f8f6f4 v[118:121], v[10:17], v[220:227], v[118:121]
	v_mfma_f32_16x16x128_f8f6f4 v[110:113], v[2:9], v[228:235], v[110:113]
	v_mfma_f32_16x16x128_f8f6f4 v[102:105], v[10:17], v[228:235], v[102:105]
	s_setprio 0
	s_setprio 1
	v_mfma_f32_16x16x128_f8f6f4 v[154:157], v[18:25], v[204:211], v[154:157]
	v_mfma_f32_16x16x128_f8f6f4 v[146:149], v[26:33], v[204:211], v[146:149]
	v_mfma_f32_16x16x128_f8f6f4 v[138:141], v[18:25], v[212:219], v[138:141]
	v_mfma_f32_16x16x128_f8f6f4 v[130:133], v[26:33], v[212:219], v[130:133]
	v_mfma_f32_16x16x128_f8f6f4 v[122:125], v[18:25], v[220:227], v[122:125]
	v_mfma_f32_16x16x128_f8f6f4 v[114:117], v[26:33], v[220:227], v[114:117]
	v_mfma_f32_16x16x128_f8f6f4 v[106:109], v[18:25], v[228:235], v[106:109]
	v_mfma_f32_16x16x128_f8f6f4 v[98:101], v[26:33], v[228:235], v[98:101]
	s_setprio 0
	s_barrier
	s_add_i32 s46, s46, s52
	s_mov_b32 m0, s46
	ds_read_b128 v[204:207], v199 offset:49152
	ds_read_b128 v[208:211], v199 offset:50176
	ds_read_b128 v[212:215], v199 offset:51200
	ds_read_b128 v[216:219], v199 offset:52224
	ds_read_b128 v[220:223], v199 offset:53248
	ds_read_b128 v[224:227], v199 offset:54272
	ds_read_b128 v[228:231], v199 offset:55296
	ds_read_b128 v[232:235], v199 offset:56320
	s_add_u32 s98, s98, 0x80
	s_addc_u32 s99, s99, 0
	global_load_lds_dwordx4 v164, s[98:99]
	s_add_i32 m0, s46, 0x2000
	s_add_u32 s44, s44, 0x20080
	s_addc_u32 s45, s45, 0
	s_add_i32 s46, s47, s52
	global_load_lds_dwordx4 v166, s[98:99]
	s_mov_b32 m0, s46
	s_nop 0
	global_load_lds_dwordx4 v164, s[44:45]
	s_add_i32 m0, s46, 0x2000
	s_nop 0
	global_load_lds_dwordx4 v166, s[44:45]
	v_lshl_add_u64 v[184:185], v[190:191], 0, s[16:17]
	s_mov_b32 m0, s63
	s_nop 0
	global_load_lds_dwordx4 v[184:185], off
	v_lshl_add_u64 v[184:185], v[188:189], 0, s[16:17]
	s_mov_b32 m0, s64
	s_nop 0
	global_load_lds_dwordx4 v[184:185], off
	s_waitcnt vmcnt(8)
	s_waitcnt lgkmcnt(0)
	s_barrier
	s_setprio 1
	s_waitcnt lgkmcnt(0)
	v_mfma_f32_16x16x128_f8f6f4 v[94:97], v[2:9], v[204:211], v[94:97]
	v_mfma_f32_16x16x128_f8f6f4 v[86:89], v[10:17], v[204:211], v[86:89]
	v_mfma_f32_16x16x128_f8f6f4 v[78:81], v[2:9], v[212:219], v[78:81]
	v_mfma_f32_16x16x128_f8f6f4 v[70:73], v[10:17], v[212:219], v[70:73]
	v_mfma_f32_16x16x128_f8f6f4 v[58:61], v[2:9], v[220:227], v[58:61]
	v_mfma_f32_16x16x128_f8f6f4 v[46:49], v[10:17], v[220:227], v[46:49]
	v_mfma_f32_16x16x128_f8f6f4 v[38:41], v[2:9], v[228:235], v[38:41]
	v_mfma_f32_16x16x128_f8f6f4 v[34:37], v[10:17], v[228:235], v[34:37]
	s_setprio 0
	s_setprio 1
	v_mfma_f32_16x16x128_f8f6f4 v[90:93], v[18:25], v[204:211], v[90:93]
	v_mfma_f32_16x16x128_f8f6f4 v[82:85], v[26:33], v[204:211], v[82:85]
	v_mfma_f32_16x16x128_f8f6f4 v[74:77], v[18:25], v[212:219], v[74:77]
	v_mfma_f32_16x16x128_f8f6f4 v[66:69], v[26:33], v[212:219], v[66:69]
	v_mfma_f32_16x16x128_f8f6f4 v[50:53], v[18:25], v[220:227], v[50:53]
	v_mfma_f32_16x16x128_f8f6f4 v[42:45], v[26:33], v[220:227], v[42:45]
	v_mfma_f32_16x16x128_f8f6f4 v[62:65], v[18:25], v[228:235], v[62:65]
	v_mfma_f32_16x16x128_f8f6f4 v[54:57], v[26:33], v[228:235], v[54:57]
	s_setprio 0
	s_barrier
	s_add_i32 s79, s79, 2
	s_cmp_gt_u32 s79, 5
	s_mov_b64 s[46:47], s[42:43]
	s_cbranch_scc0 .LBB0_1911
	s_and_b64 vcc, exec, s[20:21]
	s_cbranch_vccz .LBB0_1914
	s_barrier

.LBB0_2047:
	s_add_u32 s20, s20, 0x70080
	s_addc_u32 s21, s21, 0
	s_add_u32 s52, s22, 0x100
	s_addc_u32 s53, s23, 0
	s_mov_b32 s59, -2
	ds_read_b128 v[18:21], v189
	ds_read_b128 v[22:25], v189 offset:1024
	ds_read_b128 v[26:29], v189 offset:2048
	ds_read_b128 v[30:33], v189 offset:3072
	ds_read_b128 v[2:5], v190
	ds_read_b128 v[6:9], v190 offset:1024
	ds_read_b128 v[10:13], v190 offset:2048
	ds_read_b128 v[14:17], v190 offset:3072
	s_add_u32 s22, s20, 0xfff90080
	s_addc_u32 s23, s21, -1
	s_cmp_eq_u32 s59, 24
	s_cselect_b32 s25, s17, s23
	s_cselect_b32 s24, s16, s22
	s_cselect_b32 s23, s19, s53
	s_cselect_b32 s22, s18, s52
	s_add_i32 m0, s38, 0xc000
	ds_read_b128 v[178:181], v191
	ds_read_b128 v[182:185], v191 offset:1024
	ds_read_b128 v[192:195], v191 offset:2048
	ds_read_b128 v[196:199], v191 offset:3072
	ds_read_b128 v[200:203], v191 offset:4096
	ds_read_b128 v[204:207], v191 offset:5120
	ds_read_b128 v[208:211], v191 offset:6144
	ds_read_b128 v[212:215], v191 offset:7168
	global_load_lds_dwordx4 v172, s[20:21]
	s_add_i32 m0, s38, 0xe000
	s_nop 0
	global_load_lds_dwordx4 v174, s[20:21]
	s_waitcnt vmcnt(8)
	s_waitcnt lgkmcnt(0)
	s_barrier
	s_setprio 1
	s_waitcnt lgkmcnt(0)
	v_mfma_f32_16x16x128_f8f6f4 v[158:161], v[18:25], v[178:185], 0
	v_mfma_f32_16x16x128_f8f6f4 v[154:157], v[26:33], v[178:185], 0
	v_mfma_f32_16x16x128_f8f6f4 v[150:153], v[18:25], v[192:199], 0
	v_mfma_f32_16x16x128_f8f6f4 v[146:149], v[26:33], v[192:199], 0
	v_mfma_f32_16x16x128_f8f6f4 v[142:145], v[18:25], v[200:207], 0
	v_mfma_f32_16x16x128_f8f6f4 v[138:141], v[26:33], v[200:207], 0
	v_mfma_f32_16x16x128_f8f6f4 v[134:137], v[18:25], v[208:215], 0
	v_mfma_f32_16x16x128_f8f6f4 v[130:133], v[26:33], v[208:215], 0
	s_setprio 0
	s_setprio 1
	v_mfma_f32_16x16x128_f8f6f4 v[126:129], v[2:9], v[178:185], 0
	v_mfma_f32_16x16x128_f8f6f4 v[122:125], v[10:17], v[178:185], 0
	v_mfma_f32_16x16x128_f8f6f4 v[118:121], v[2:9], v[192:199], 0
	v_mfma_f32_16x16x128_f8f6f4 v[114:117], v[10:17], v[192:199], 0
	v_mfma_f32_16x16x128_f8f6f4 v[110:113], v[2:9], v[200:207], 0
	v_mfma_f32_16x16x128_f8f6f4 v[106:109], v[10:17], v[200:207], 0
	v_mfma_f32_16x16x128_f8f6f4 v[102:105], v[2:9], v[208:215], 0
	v_mfma_f32_16x16x128_f8f6f4 v[98:101], v[10:17], v[208:215], 0
	s_setprio 0
	s_barrier
	s_add_i32 s60, s46, s35
	s_mov_b64 s[98:99], s[22:23]
	s_mov_b32 m0, s60
	ds_read_b128 v[192:195], v191 offset:16384
	ds_read_b128 v[196:199], v191 offset:17408
	ds_read_b128 v[200:203], v191 offset:18432
	ds_read_b128 v[204:207], v191 offset:19456
	ds_read_b128 v[208:211], v191 offset:20480
	ds_read_b128 v[212:215], v191 offset:21504
	ds_read_b128 v[216:219], v191 offset:22528
	ds_read_b128 v[220:223], v191 offset:23552
	global_load_lds_dwordx4 v166, s[98:99]
	s_add_i32 m0, s60, 0x2000
	s_add_u32 s60, s22, 0x70000
	s_addc_u32 s61, s23, 0
	s_add_i32 s62, s47, s35
	global_load_lds_dwordx4 v162, s[98:99]
	s_mov_b32 m0, s62
	s_mov_b64 s[100:101], s[24:25]
	global_load_lds_dwordx4 v166, s[60:61]
	s_add_i32 m0, s62, 0x2000
	s_nop 0
	global_load_lds_dwordx4 v162, s[60:61]
	s_mov_b32 m0, s38
	s_nop 0
	global_load_lds_dwordx4 v168, s[100:101]
	s_mov_b32 m0, s39
	s_nop 0
	global_load_lds_dwordx4 v164, s[100:101]
	s_waitcnt vmcnt(8)
	s_waitcnt lgkmcnt(0)
	s_barrier
	s_setprio 1
	s_waitcnt lgkmcnt(0)
	v_mfma_f32_16x16x128_f8f6f4 v[94:97], v[18:25], v[192:199], 0
	v_mfma_f32_16x16x128_f8f6f4 v[90:93], v[26:33], v[192:199], 0
	v_mfma_f32_16x16x128_f8f6f4 v[86:89], v[18:25], v[200:207], 0
	v_mfma_f32_16x16x128_f8f6f4 v[82:85], v[26:33], v[200:207], 0
	v_mfma_f32_16x16x128_f8f6f4 v[78:81], v[18:25], v[208:215], 0
	v_mfma_f32_16x16x128_f8f6f4 v[74:77], v[26:33], v[208:215], 0
	v_mfma_f32_16x16x128_f8f6f4 v[70:73], v[18:25], v[216:223], 0
	v_mfma_f32_16x16x128_f8f6f4 v[66:69], v[26:33], v[216:223], 0
	s_setprio 0
	s_setprio 1
	v_mfma_f32_16x16x128_f8f6f4 v[62:65], v[2:9], v[192:199], 0
	v_mfma_f32_16x16x128_f8f6f4 v[58:61], v[10:17], v[192:199], 0
	v_mfma_f32_16x16x128_f8f6f4 v[54:57], v[2:9], v[200:207], 0
	v_mfma_f32_16x16x128_f8f6f4 v[50:53], v[10:17], v[200:207], 0
	v_mfma_f32_16x16x128_f8f6f4 v[46:49], v[2:9], v[208:215], 0
	v_mfma_f32_16x16x128_f8f6f4 v[42:45], v[10:17], v[208:215], 0
	v_mfma_f32_16x16x128_f8f6f4 v[38:41], v[2:9], v[216:223], 0
	v_mfma_f32_16x16x128_f8f6f4 v[34:37], v[10:17], v[216:223], 0
	s_setprio 0
	s_barrier
	s_add_i32 s60, 0, 0x18000
	s_add_i32 s61, 0, 0x1c000
	v_add_u32_e32 v14, s60, v186
	v_add_u32_e32 v30, s61, v186
	ds_read_b128 v[2:5], v14
	ds_read_b128 v[6:9], v14 offset:1024
	ds_read_b128 v[10:13], v14 offset:2048
	ds_read_b128 v[14:17], v14 offset:3072
	ds_read_b128 v[18:21], v30
	ds_read_b128 v[22:25], v30 offset:1024
	ds_read_b128 v[26:29], v30 offset:2048
	ds_read_b128 v[30:33], v30 offset:3072
	s_add_u32 s24, s24, 0x70000
	s_addc_u32 s25, s25, 0
	s_mov_b32 m0, s40
	ds_read_b128 v[192:195], v191 offset:32768
	ds_read_b128 v[196:199], v191 offset:33792
	ds_read_b128 v[200:203], v191 offset:34816
	ds_read_b128 v[204:207], v191 offset:35840
	ds_read_b128 v[208:211], v191 offset:36864
	ds_read_b128 v[212:215], v191 offset:37888
	ds_read_b128 v[216:219], v191 offset:38912
	ds_read_b128 v[220:223], v191 offset:39936
	global_load_lds_dwordx4 v168, s[24:25]
	s_mov_b32 m0, s41
	s_nop 0
	global_load_lds_dwordx4 v164, s[24:25]
	s_waitcnt vmcnt(8)
	s_waitcnt lgkmcnt(0)
	s_barrier
	s_setprio 1
	s_waitcnt lgkmcnt(0)
	v_mfma_f32_16x16x128_f8f6f4 v[158:161], v[2:9], v[192:199], v[158:161]
	v_mfma_f32_16x16x128_f8f6f4 v[154:157], v[10:17], v[192:199], v[154:157]
	v_mfma_f32_16x16x128_f8f6f4 v[150:153], v[2:9], v[200:207], v[150:153]
	v_mfma_f32_16x16x128_f8f6f4 v[146:149], v[10:17], v[200:207], v[146:149]
	v_mfma_f32_16x16x128_f8f6f4 v[142:145], v[2:9], v[208:215], v[142:145]
	v_mfma_f32_16x16x128_f8f6f4 v[138:141], v[10:17], v[208:215], v[138:141]
	v_mfma_f32_16x16x128_f8f6f4 v[134:137], v[2:9], v[216:223], v[134:137]
	v_mfma_f32_16x16x128_f8f6f4 v[130:133], v[10:17], v[216:223], v[130:133]
	s_setprio 0
	s_setprio 1
	v_mfma_f32_16x16x128_f8f6f4 v[126:129], v[18:25], v[192:199], v[126:129]
	v_mfma_f32_16x16x128_f8f6f4 v[122:125], v[26:33], v[192:199], v[122:125]
	v_mfma_f32_16x16x128_f8f6f4 v[118:121], v[18:25], v[200:207], v[118:121]
	v_mfma_f32_16x16x128_f8f6f4 v[114:117], v[26:33], v[200:207], v[114:117]
	v_mfma_f32_16x16x128_f8f6f4 v[110:113], v[18:25], v[208:215], v[110:113]
	v_mfma_f32_16x16x128_f8f6f4 v[106:109], v[26:33], v[208:215], v[106:109]
	v_mfma_f32_16x16x128_f8f6f4 v[102:105], v[18:25], v[216:223], v[102:105]
	v_mfma_f32_16x16x128_f8f6f4 v[98:101], v[26:33], v[216:223], v[98:101]
	s_setprio 0
	s_barrier
	s_add_i32 s24, s60, s35
	s_mov_b32 m0, s24
	ds_read_b128 v[192:195], v191 offset:49152
	ds_read_b128 v[196:199], v191 offset:50176
	ds_read_b128 v[200:203], v191 offset:51200
	ds_read_b128 v[204:207], v191 offset:52224
	ds_read_b128 v[208:211], v191 offset:53248
	ds_read_b128 v[212:215], v191 offset:54272
	ds_read_b128 v[216:219], v191 offset:55296
	ds_read_b128 v[220:223], v191 offset:56320
	s_add_u32 s98, s98, 0x80
	s_addc_u32 s99, s99, 0
	global_load_lds_dwordx4 v166, s[98:99]
	s_add_i32 m0, s24, 0x2000
	s_add_u32 s22, s22, 0x70080
	s_addc_u32 s23, s23, 0
	s_add_i32 s24, s61, s35
	global_load_lds_dwordx4 v162, s[98:99]
	s_mov_b32 m0, s24
	s_nop 0
	global_load_lds_dwordx4 v166, s[22:23]
	s_add_i32 m0, s24, 0x2000
	s_nop 0
	global_load_lds_dwordx4 v162, s[22:23]
	s_mov_b32 m0, s43
	s_nop 0
	s_add_u32 s100, s100, 0x80
	s_addc_u32 s101, s101, 0
	global_load_lds_dwordx4 v168, s[100:101]
	s_mov_b32 m0, s44
	s_nop 0
	global_load_lds_dwordx4 v164, s[100:101]
	s_waitcnt vmcnt(8)
	s_waitcnt lgkmcnt(0)
	s_barrier
	s_setprio 1
	s_waitcnt lgkmcnt(0)
	v_mfma_f32_16x16x128_f8f6f4 v[94:97], v[2:9], v[192:199], v[94:97]
	v_mfma_f32_16x16x128_f8f6f4 v[90:93], v[10:17], v[192:199], v[90:93]
	v_mfma_f32_16x16x128_f8f6f4 v[86:89], v[2:9], v[200:207], v[86:89]
	v_mfma_f32_16x16x128_f8f6f4 v[82:85], v[10:17], v[200:207], v[82:85]
	v_mfma_f32_16x16x128_f8f6f4 v[78:81], v[2:9], v[208:215], v[78:81]
	v_mfma_f32_16x16x128_f8f6f4 v[74:77], v[10:17], v[208:215], v[74:77]
	v_mfma_f32_16x16x128_f8f6f4 v[70:73], v[2:9], v[216:223], v[70:73]
	v_mfma_f32_16x16x128_f8f6f4 v[66:69], v[10:17], v[216:223], v[66:69]
	s_setprio 0
	s_setprio 1
	v_mfma_f32_16x16x128_f8f6f4 v[62:65], v[18:25], v[192:199], v[62:65]
	v_mfma_f32_16x16x128_f8f6f4 v[58:61], v[26:33], v[192:199], v[58:61]
	v_mfma_f32_16x16x128_f8f6f4 v[54:57], v[18:25], v[200:207], v[54:57]
	v_mfma_f32_16x16x128_f8f6f4 v[50:53], v[26:33], v[200:207], v[50:53]
	v_mfma_f32_16x16x128_f8f6f4 v[46:49], v[18:25], v[208:215], v[46:49]
	v_mfma_f32_16x16x128_f8f6f4 v[42:45], v[26:33], v[208:215], v[42:45]
	v_mfma_f32_16x16x128_f8f6f4 v[38:41], v[18:25], v[216:223], v[38:41]
	v_mfma_f32_16x16x128_f8f6f4 v[34:37], v[26:33], v[216:223], v[34:37]
	s_setprio 0
	s_barrier
	s_add_i32 s59, s59, 2
	s_add_u32 s20, s20, 0x100
	s_addc_u32 s21, s21, 0
	s_add_u32 s52, s52, 0x100
	s_addc_u32 s53, s53, 0
	s_cmp_gt_u32 s59, 25
.LBB0_2048:
	ds_read_b128 v[18:21], v189
	ds_read_b128 v[22:25], v189 offset:1024
	ds_read_b128 v[26:29], v189 offset:2048
	ds_read_b128 v[30:33], v189 offset:3072
	ds_read_b128 v[2:5], v190
	ds_read_b128 v[6:9], v190 offset:1024
	ds_read_b128 v[10:13], v190 offset:2048
	ds_read_b128 v[14:17], v190 offset:3072
	s_add_u32 s22, s20, 0xfff90080
	s_addc_u32 s23, s21, -1
	s_cmp_eq_u32 s59, 24
	s_cselect_b32 s25, s17, s23
	s_cselect_b32 s24, s16, s22
	s_cselect_b32 s23, s19, s53
	s_cselect_b32 s22, s18, s52
	s_add_i32 m0, s38, 0xc000
	ds_read_b128 v[178:181], v191
	ds_read_b128 v[182:185], v191 offset:1024
	ds_read_b128 v[192:195], v191 offset:2048
	ds_read_b128 v[196:199], v191 offset:3072
	ds_read_b128 v[200:203], v191 offset:4096
	ds_read_b128 v[204:207], v191 offset:5120
	ds_read_b128 v[208:211], v191 offset:6144
	ds_read_b128 v[212:215], v191 offset:7168
	global_load_lds_dwordx4 v172, s[20:21]
	s_add_i32 m0, s38, 0xe000
	s_nop 0
	global_load_lds_dwordx4 v174, s[20:21]
	s_waitcnt vmcnt(8)
	s_waitcnt lgkmcnt(0)
	s_barrier
	s_setprio 1
	s_waitcnt lgkmcnt(0)
	v_mfma_f32_16x16x128_f8f6f4 v[158:161], v[18:25], v[178:185], v[158:161]
	v_mfma_f32_16x16x128_f8f6f4 v[154:157], v[26:33], v[178:185], v[154:157]
	v_mfma_f32_16x16x128_f8f6f4 v[150:153], v[18:25], v[192:199], v[150:153]
	v_mfma_f32_16x16x128_f8f6f4 v[146:149], v[26:33], v[192:199], v[146:149]
	v_mfma_f32_16x16x128_f8f6f4 v[142:145], v[18:25], v[200:207], v[142:145]
	v_mfma_f32_16x16x128_f8f6f4 v[138:141], v[26:33], v[200:207], v[138:141]
	v_mfma_f32_16x16x128_f8f6f4 v[134:137], v[18:25], v[208:215], v[134:137]
	v_mfma_f32_16x16x128_f8f6f4 v[130:133], v[26:33], v[208:215], v[130:133]
	s_setprio 0
	s_setprio 1
	v_mfma_f32_16x16x128_f8f6f4 v[126:129], v[2:9], v[178:185], v[126:129]
	v_mfma_f32_16x16x128_f8f6f4 v[122:125], v[10:17], v[178:185], v[122:125]
	v_mfma_f32_16x16x128_f8f6f4 v[118:121], v[2:9], v[192:199], v[118:121]
	v_mfma_f32_16x16x128_f8f6f4 v[114:117], v[10:17], v[192:199], v[114:117]
	v_mfma_f32_16x16x128_f8f6f4 v[110:113], v[2:9], v[200:207], v[110:113]
	v_mfma_f32_16x16x128_f8f6f4 v[106:109], v[10:17], v[200:207], v[106:109]
	v_mfma_f32_16x16x128_f8f6f4 v[102:105], v[2:9], v[208:215], v[102:105]
	v_mfma_f32_16x16x128_f8f6f4 v[98:101], v[10:17], v[208:215], v[98:101]
	s_setprio 0
	s_barrier
	s_add_i32 s60, s46, s35
	s_mov_b64 s[98:99], s[22:23]
	s_mov_b32 m0, s60
	ds_read_b128 v[192:195], v191 offset:16384
	ds_read_b128 v[196:199], v191 offset:17408
	ds_read_b128 v[200:203], v191 offset:18432
	ds_read_b128 v[204:207], v191 offset:19456
	ds_read_b128 v[208:211], v191 offset:20480
	ds_read_b128 v[212:215], v191 offset:21504
	ds_read_b128 v[216:219], v191 offset:22528
	ds_read_b128 v[220:223], v191 offset:23552
	global_load_lds_dwordx4 v166, s[98:99]
	s_add_i32 m0, s60, 0x2000
	s_add_u32 s60, s22, 0x70000
	s_addc_u32 s61, s23, 0
	s_add_i32 s62, s47, s35
	global_load_lds_dwordx4 v162, s[98:99]
	s_mov_b32 m0, s62
	s_mov_b64 s[100:101], s[24:25]
	global_load_lds_dwordx4 v166, s[60:61]
	s_add_i32 m0, s62, 0x2000
	s_nop 0
	global_load_lds_dwordx4 v162, s[60:61]
	s_mov_b32 m0, s38
	s_nop 0
	global_load_lds_dwordx4 v168, s[100:101]
	s_mov_b32 m0, s39
	s_nop 0
	global_load_lds_dwordx4 v164, s[100:101]
	s_waitcnt vmcnt(8)
	s_waitcnt lgkmcnt(0)
	s_barrier
	s_setprio 1
	s_waitcnt lgkmcnt(0)
	v_mfma_f32_16x16x128_f8f6f4 v[94:97], v[18:25], v[192:199], v[94:97]
	v_mfma_f32_16x16x128_f8f6f4 v[90:93], v[26:33], v[192:199], v[90:93]
	v_mfma_f32_16x16x128_f8f6f4 v[86:89], v[18:25], v[200:207], v[86:89]
	v_mfma_f32_16x16x128_f8f6f4 v[82:85], v[26:33], v[200:207], v[82:85]
	v_mfma_f32_16x16x128_f8f6f4 v[78:81], v[18:25], v[208:215], v[78:81]
	v_mfma_f32_16x16x128_f8f6f4 v[74:77], v[26:33], v[208:215], v[74:77]
	v_mfma_f32_16x16x128_f8f6f4 v[70:73], v[18:25], v[216:223], v[70:73]
	v_mfma_f32_16x16x128_f8f6f4 v[66:69], v[26:33], v[216:223], v[66:69]
	s_setprio 0
	s_setprio 1
	v_mfma_f32_16x16x128_f8f6f4 v[62:65], v[2:9], v[192:199], v[62:65]
	v_mfma_f32_16x16x128_f8f6f4 v[58:61], v[10:17], v[192:199], v[58:61]
	v_mfma_f32_16x16x128_f8f6f4 v[54:57], v[2:9], v[200:207], v[54:57]
	v_mfma_f32_16x16x128_f8f6f4 v[50:53], v[10:17], v[200:207], v[50:53]
	v_mfma_f32_16x16x128_f8f6f4 v[46:49], v[2:9], v[208:215], v[46:49]
	v_mfma_f32_16x16x128_f8f6f4 v[42:45], v[10:17], v[208:215], v[42:45]
	v_mfma_f32_16x16x128_f8f6f4 v[38:41], v[2:9], v[216:223], v[38:41]
	v_mfma_f32_16x16x128_f8f6f4 v[34:37], v[10:17], v[216:223], v[34:37]
	s_setprio 0
	s_barrier
	s_add_i32 s60, 0, 0x18000
	s_add_i32 s61, 0, 0x1c000
	v_add_u32_e32 v14, s60, v186
	v_add_u32_e32 v30, s61, v186
	ds_read_b128 v[2:5], v14
	ds_read_b128 v[6:9], v14 offset:1024
	ds_read_b128 v[10:13], v14 offset:2048
	ds_read_b128 v[14:17], v14 offset:3072
	ds_read_b128 v[18:21], v30
	ds_read_b128 v[22:25], v30 offset:1024
	ds_read_b128 v[26:29], v30 offset:2048
	ds_read_b128 v[30:33], v30 offset:3072
	s_add_u32 s24, s24, 0x70000
	s_addc_u32 s25, s25, 0
	s_mov_b32 m0, s40
	ds_read_b128 v[192:195], v191 offset:32768
	ds_read_b128 v[196:199], v191 offset:33792
	ds_read_b128 v[200:203], v191 offset:34816
	ds_read_b128 v[204:207], v191 offset:35840
	ds_read_b128 v[208:211], v191 offset:36864
	ds_read_b128 v[212:215], v191 offset:37888
	ds_read_b128 v[216:219], v191 offset:38912
	ds_read_b128 v[220:223], v191 offset:39936
	global_load_lds_dwordx4 v168, s[24:25]
	s_mov_b32 m0, s41
	s_nop 0
	global_load_lds_dwordx4 v164, s[24:25]
	s_waitcnt vmcnt(8)
	s_waitcnt lgkmcnt(0)
	s_barrier
	s_setprio 1
	s_waitcnt lgkmcnt(0)
	v_mfma_f32_16x16x128_f8f6f4 v[158:161], v[2:9], v[192:199], v[158:161]
	v_mfma_f32_16x16x128_f8f6f4 v[154:157], v[10:17], v[192:199], v[154:157]
	v_mfma_f32_16x16x128_f8f6f4 v[150:153], v[2:9], v[200:207], v[150:153]
	v_mfma_f32_16x16x128_f8f6f4 v[146:149], v[10:17], v[200:207], v[146:149]
	v_mfma_f32_16x16x128_f8f6f4 v[142:145], v[2:9], v[208:215], v[142:145]
	v_mfma_f32_16x16x128_f8f6f4 v[138:141], v[10:17], v[208:215], v[138:141]
	v_mfma_f32_16x16x128_f8f6f4 v[134:137], v[2:9], v[216:223], v[134:137]
	v_mfma_f32_16x16x128_f8f6f4 v[130:133], v[10:17], v[216:223], v[130:133]
	s_setprio 0
	s_setprio 1
	v_mfma_f32_16x16x128_f8f6f4 v[126:129], v[18:25], v[192:199], v[126:129]
	v_mfma_f32_16x16x128_f8f6f4 v[122:125], v[26:33], v[192:199], v[122:125]
	v_mfma_f32_16x16x128_f8f6f4 v[118:121], v[18:25], v[200:207], v[118:121]
	v_mfma_f32_16x16x128_f8f6f4 v[114:117], v[26:33], v[200:207], v[114:117]
	v_mfma_f32_16x16x128_f8f6f4 v[110:113], v[18:25], v[208:215], v[110:113]
	v_mfma_f32_16x16x128_f8f6f4 v[106:109], v[26:33], v[208:215], v[106:109]
	v_mfma_f32_16x16x128_f8f6f4 v[102:105], v[18:25], v[216:223], v[102:105]
	v_mfma_f32_16x16x128_f8f6f4 v[98:101], v[26:33], v[216:223], v[98:101]
	s_setprio 0
	s_barrier
	s_add_i32 s24, s60, s35
	s_mov_b32 m0, s24
	ds_read_b128 v[192:195], v191 offset:49152
	ds_read_b128 v[196:199], v191 offset:50176
	ds_read_b128 v[200:203], v191 offset:51200
	ds_read_b128 v[204:207], v191 offset:52224
	ds_read_b128 v[208:211], v191 offset:53248
	ds_read_b128 v[212:215], v191 offset:54272
	ds_read_b128 v[216:219], v191 offset:55296
	ds_read_b128 v[220:223], v191 offset:56320
	s_add_u32 s98, s98, 0x80
	s_addc_u32 s99, s99, 0
	global_load_lds_dwordx4 v166, s[98:99]
	s_add_i32 m0, s24, 0x2000
	s_add_u32 s22, s22, 0x70080
	s_addc_u32 s23, s23, 0
	s_add_i32 s24, s61, s35
	global_load_lds_dwordx4 v162, s[98:99]
	s_mov_b32 m0, s24
	s_nop 0
	global_load_lds_dwordx4 v166, s[22:23]
	s_add_i32 m0, s24, 0x2000
	s_nop 0
	global_load_lds_dwordx4 v162, s[22:23]
	s_mov_b32 m0, s43
	s_nop 0
	s_add_u32 s100, s100, 0x80
	s_addc_u32 s101, s101, 0
	global_load_lds_dwordx4 v168, s[100:101]
	s_mov_b32 m0, s44
	s_nop 0
	global_load_lds_dwordx4 v164, s[100:101]
	s_waitcnt vmcnt(8)
	s_waitcnt lgkmcnt(0)
	s_barrier
	s_setprio 1
	s_waitcnt lgkmcnt(0)
	v_mfma_f32_16x16x128_f8f6f4 v[94:97], v[2:9], v[192:199], v[94:97]
	v_mfma_f32_16x16x128_f8f6f4 v[90:93], v[10:17], v[192:199], v[90:93]
	v_mfma_f32_16x16x128_f8f6f4 v[86:89], v[2:9], v[200:207], v[86:89]
	v_mfma_f32_16x16x128_f8f6f4 v[82:85], v[10:17], v[200:207], v[82:85]
	v_mfma_f32_16x16x128_f8f6f4 v[78:81], v[2:9], v[208:215], v[78:81]
	v_mfma_f32_16x16x128_f8f6f4 v[74:77], v[10:17], v[208:215], v[74:77]
	v_mfma_f32_16x16x128_f8f6f4 v[70:73], v[2:9], v[216:223], v[70:73]
	v_mfma_f32_16x16x128_f8f6f4 v[66:69], v[10:17], v[216:223], v[66:69]
	s_setprio 0
	s_setprio 1
	v_mfma_f32_16x16x128_f8f6f4 v[62:65], v[18:25], v[192:199], v[62:65]
	v_mfma_f32_16x16x128_f8f6f4 v[58:61], v[26:33], v[192:199], v[58:61]
	v_mfma_f32_16x16x128_f8f6f4 v[54:57], v[18:25], v[200:207], v[54:57]
	v_mfma_f32_16x16x128_f8f6f4 v[50:53], v[26:33], v[200:207], v[50:53]
	v_mfma_f32_16x16x128_f8f6f4 v[46:49], v[18:25], v[208:215], v[46:49]
	v_mfma_f32_16x16x128_f8f6f4 v[42:45], v[26:33], v[208:215], v[42:45]
	v_mfma_f32_16x16x128_f8f6f4 v[38:41], v[18:25], v[216:223], v[38:41]
	v_mfma_f32_16x16x128_f8f6f4 v[34:37], v[26:33], v[216:223], v[34:37]
	s_setprio 0
	s_barrier
	s_add_i32 s59, s59, 2
	s_add_u32 s20, s20, 0x100
	s_addc_u32 s21, s21, 0
	s_add_u32 s52, s52, 0x100
	s_addc_u32 s53, s53, 0
	s_cmp_gt_u32 s59, 25
	s_cbranch_scc0 .LBB0_2048
	s_and_b64 vcc, exec, s[12:13]
	s_cbranch_vccz .LBB0_2051
	s_barrier

.LBB0_2188:
	s_add_u32 s22, s22, 0x70080
	s_addc_u32 s23, s23, 0
	s_add_u32 s61, s24, 0x100
	s_addc_u32 s62, s25, 0
	s_mov_b32 s63, -2
	ds_read_b128 v[18:21], v189
	ds_read_b128 v[22:25], v189 offset:1024
	ds_read_b128 v[26:29], v189 offset:2048
	ds_read_b128 v[30:33], v189 offset:3072
	ds_read_b128 v[2:5], v190
	ds_read_b128 v[6:9], v190 offset:1024
	ds_read_b128 v[10:13], v190 offset:2048
	ds_read_b128 v[14:17], v190 offset:3072
	s_add_u32 s24, s22, 0xfff90080
	s_addc_u32 s25, s23, -1
	s_cmp_eq_u32 s63, 24
	s_cselect_b32 s27, s19, s25
	s_cselect_b32 s26, s18, s24
	s_cselect_b32 s25, s21, s62
	s_cselect_b32 s24, s20, s61
	s_add_i32 m0, s43, 0xc000
	ds_read_b128 v[178:181], v191
	ds_read_b128 v[182:185], v191 offset:1024
	ds_read_b128 v[192:195], v191 offset:2048
	ds_read_b128 v[196:199], v191 offset:3072
	ds_read_b128 v[200:203], v191 offset:4096
	ds_read_b128 v[204:207], v191 offset:5120
	ds_read_b128 v[208:211], v191 offset:6144
	ds_read_b128 v[212:215], v191 offset:7168
	global_load_lds_dwordx4 v172, s[22:23]
	s_add_i32 m0, s43, 0xe000
	s_nop 0
	global_load_lds_dwordx4 v174, s[22:23]
	s_waitcnt vmcnt(8)
	s_waitcnt lgkmcnt(0)
	s_barrier
	s_setprio 1
	s_waitcnt lgkmcnt(0)
	v_mfma_f32_16x16x128_f8f6f4 v[158:161], v[18:25], v[178:185], 0
	v_mfma_f32_16x16x128_f8f6f4 v[154:157], v[26:33], v[178:185], 0
	v_mfma_f32_16x16x128_f8f6f4 v[150:153], v[18:25], v[192:199], 0
	v_mfma_f32_16x16x128_f8f6f4 v[146:149], v[26:33], v[192:199], 0
	v_mfma_f32_16x16x128_f8f6f4 v[142:145], v[18:25], v[200:207], 0
	v_mfma_f32_16x16x128_f8f6f4 v[138:141], v[26:33], v[200:207], 0
	v_mfma_f32_16x16x128_f8f6f4 v[134:137], v[18:25], v[208:215], 0
	v_mfma_f32_16x16x128_f8f6f4 v[130:133], v[26:33], v[208:215], 0
	s_setprio 0
	s_setprio 1
	v_mfma_f32_16x16x128_f8f6f4 v[126:129], v[2:9], v[178:185], 0
	v_mfma_f32_16x16x128_f8f6f4 v[122:125], v[10:17], v[178:185], 0
	v_mfma_f32_16x16x128_f8f6f4 v[118:121], v[2:9], v[192:199], 0
	v_mfma_f32_16x16x128_f8f6f4 v[114:117], v[10:17], v[192:199], 0
	v_mfma_f32_16x16x128_f8f6f4 v[110:113], v[2:9], v[200:207], 0
	v_mfma_f32_16x16x128_f8f6f4 v[106:109], v[10:17], v[200:207], 0
	v_mfma_f32_16x16x128_f8f6f4 v[102:105], v[2:9], v[208:215], 0
	v_mfma_f32_16x16x128_f8f6f4 v[98:101], v[10:17], v[208:215], 0
	s_setprio 0
	s_barrier
	s_add_i32 s64, s7, s42
	s_mov_b64 s[98:99], s[24:25]
	s_mov_b32 m0, s64
	ds_read_b128 v[192:195], v191 offset:16384
	ds_read_b128 v[196:199], v191 offset:17408
	ds_read_b128 v[200:203], v191 offset:18432
	ds_read_b128 v[204:207], v191 offset:19456
	ds_read_b128 v[208:211], v191 offset:20480
	ds_read_b128 v[212:215], v191 offset:21504
	ds_read_b128 v[216:219], v191 offset:22528
	ds_read_b128 v[220:223], v191 offset:23552
	global_load_lds_dwordx4 v164, s[98:99]
	s_add_i32 m0, s64, 0x2000
	s_add_u32 s64, s24, 0x70000
	s_addc_u32 s65, s25, 0
	s_add_i32 s66, s51, s42
	global_load_lds_dwordx4 v168, s[98:99]
	s_mov_b32 m0, s66
	s_mov_b64 s[100:101], s[26:27]
	global_load_lds_dwordx4 v164, s[64:65]
	s_add_i32 m0, s66, 0x2000
	s_nop 0
	global_load_lds_dwordx4 v168, s[64:65]
	s_mov_b32 m0, s43
	s_nop 0
	global_load_lds_dwordx4 v162, s[100:101]
	s_mov_b32 m0, s44
	s_nop 0
	global_load_lds_dwordx4 v166, s[100:101]
	s_waitcnt vmcnt(8)
	s_waitcnt lgkmcnt(0)
	s_barrier
	s_setprio 1
	s_waitcnt lgkmcnt(0)
	v_mfma_f32_16x16x128_f8f6f4 v[94:97], v[18:25], v[192:199], 0
	v_mfma_f32_16x16x128_f8f6f4 v[90:93], v[26:33], v[192:199], 0
	v_mfma_f32_16x16x128_f8f6f4 v[86:89], v[18:25], v[200:207], 0
	v_mfma_f32_16x16x128_f8f6f4 v[82:85], v[26:33], v[200:207], 0
	v_mfma_f32_16x16x128_f8f6f4 v[78:81], v[18:25], v[208:215], 0
	v_mfma_f32_16x16x128_f8f6f4 v[74:77], v[26:33], v[208:215], 0
	v_mfma_f32_16x16x128_f8f6f4 v[70:73], v[18:25], v[216:223], 0
	v_mfma_f32_16x16x128_f8f6f4 v[66:69], v[26:33], v[216:223], 0
	s_setprio 0
	s_setprio 1
	v_mfma_f32_16x16x128_f8f6f4 v[62:65], v[2:9], v[192:199], 0
	v_mfma_f32_16x16x128_f8f6f4 v[58:61], v[10:17], v[192:199], 0
	v_mfma_f32_16x16x128_f8f6f4 v[54:57], v[2:9], v[200:207], 0
	v_mfma_f32_16x16x128_f8f6f4 v[50:53], v[10:17], v[200:207], 0
	v_mfma_f32_16x16x128_f8f6f4 v[46:49], v[2:9], v[208:215], 0
	v_mfma_f32_16x16x128_f8f6f4 v[42:45], v[10:17], v[208:215], 0
	v_mfma_f32_16x16x128_f8f6f4 v[38:41], v[2:9], v[216:223], 0
	v_mfma_f32_16x16x128_f8f6f4 v[34:37], v[10:17], v[216:223], 0
	s_setprio 0
	s_barrier
	s_add_i32 s64, 0, 0x18000
	s_add_i32 s65, 0, 0x1c000
	v_add_u32_e32 v14, s64, v186
	v_add_u32_e32 v30, s65, v186
	ds_read_b128 v[2:5], v14
	ds_read_b128 v[6:9], v14 offset:1024
	ds_read_b128 v[10:13], v14 offset:2048
	ds_read_b128 v[14:17], v14 offset:3072
	ds_read_b128 v[18:21], v30
	ds_read_b128 v[22:25], v30 offset:1024
	ds_read_b128 v[26:29], v30 offset:2048
	ds_read_b128 v[30:33], v30 offset:3072
	s_add_u32 s26, s26, 0x70000
	s_addc_u32 s27, s27, 0
	s_mov_b32 m0, s45
	ds_read_b128 v[192:195], v191 offset:32768
	ds_read_b128 v[196:199], v191 offset:33792
	ds_read_b128 v[200:203], v191 offset:34816
	ds_read_b128 v[204:207], v191 offset:35840
	ds_read_b128 v[208:211], v191 offset:36864
	ds_read_b128 v[212:215], v191 offset:37888
	ds_read_b128 v[216:219], v191 offset:38912
	ds_read_b128 v[220:223], v191 offset:39936
	global_load_lds_dwordx4 v162, s[26:27]
	s_mov_b32 m0, s46
	s_nop 0
	global_load_lds_dwordx4 v166, s[26:27]
	s_waitcnt vmcnt(8)
	s_waitcnt lgkmcnt(0)
	s_barrier
	s_setprio 1
	s_waitcnt lgkmcnt(0)
	v_mfma_f32_16x16x128_f8f6f4 v[158:161], v[2:9], v[192:199], v[158:161]
	v_mfma_f32_16x16x128_f8f6f4 v[154:157], v[10:17], v[192:199], v[154:157]
	v_mfma_f32_16x16x128_f8f6f4 v[150:153], v[2:9], v[200:207], v[150:153]
	v_mfma_f32_16x16x128_f8f6f4 v[146:149], v[10:17], v[200:207], v[146:149]
	v_mfma_f32_16x16x128_f8f6f4 v[142:145], v[2:9], v[208:215], v[142:145]
	v_mfma_f32_16x16x128_f8f6f4 v[138:141], v[10:17], v[208:215], v[138:141]
	v_mfma_f32_16x16x128_f8f6f4 v[134:137], v[2:9], v[216:223], v[134:137]
	v_mfma_f32_16x16x128_f8f6f4 v[130:133], v[10:17], v[216:223], v[130:133]
	s_setprio 0
	s_setprio 1
	v_mfma_f32_16x16x128_f8f6f4 v[126:129], v[18:25], v[192:199], v[126:129]
	v_mfma_f32_16x16x128_f8f6f4 v[122:125], v[26:33], v[192:199], v[122:125]
	v_mfma_f32_16x16x128_f8f6f4 v[118:121], v[18:25], v[200:207], v[118:121]
	v_mfma_f32_16x16x128_f8f6f4 v[114:117], v[26:33], v[200:207], v[114:117]
	v_mfma_f32_16x16x128_f8f6f4 v[110:113], v[18:25], v[208:215], v[110:113]
	v_mfma_f32_16x16x128_f8f6f4 v[106:109], v[26:33], v[208:215], v[106:109]
	v_mfma_f32_16x16x128_f8f6f4 v[102:105], v[18:25], v[216:223], v[102:105]
	v_mfma_f32_16x16x128_f8f6f4 v[98:101], v[26:33], v[216:223], v[98:101]
	s_setprio 0
	s_barrier
	s_add_i32 s26, s64, s42
	s_mov_b32 m0, s26
	ds_read_b128 v[192:195], v191 offset:49152
	ds_read_b128 v[196:199], v191 offset:50176
	ds_read_b128 v[200:203], v191 offset:51200
	ds_read_b128 v[204:207], v191 offset:52224
	ds_read_b128 v[208:211], v191 offset:53248
	ds_read_b128 v[212:215], v191 offset:54272
	ds_read_b128 v[216:219], v191 offset:55296
	ds_read_b128 v[220:223], v191 offset:56320
	s_add_u32 s98, s98, 0x80
	s_addc_u32 s99, s99, 0
	global_load_lds_dwordx4 v164, s[98:99]
	s_add_i32 m0, s26, 0x2000
	s_add_u32 s24, s24, 0x70080
	s_addc_u32 s25, s25, 0
	s_add_i32 s26, s65, s42
	global_load_lds_dwordx4 v168, s[98:99]
	s_mov_b32 m0, s26
	s_nop 0
	global_load_lds_dwordx4 v164, s[24:25]
	s_add_i32 m0, s26, 0x2000
	s_nop 0
	global_load_lds_dwordx4 v168, s[24:25]
	s_mov_b32 m0, s48
	s_nop 0
	s_add_u32 s100, s100, 0x80
	s_addc_u32 s101, s101, 0
	global_load_lds_dwordx4 v162, s[100:101]
	s_mov_b32 m0, s49
	s_nop 0
	global_load_lds_dwordx4 v166, s[100:101]
	s_waitcnt vmcnt(8)
	s_waitcnt lgkmcnt(0)
	s_barrier
	s_setprio 1
	s_waitcnt lgkmcnt(0)
	v_mfma_f32_16x16x128_f8f6f4 v[94:97], v[2:9], v[192:199], v[94:97]
	v_mfma_f32_16x16x128_f8f6f4 v[90:93], v[10:17], v[192:199], v[90:93]
	v_mfma_f32_16x16x128_f8f6f4 v[86:89], v[2:9], v[200:207], v[86:89]
	v_mfma_f32_16x16x128_f8f6f4 v[82:85], v[10:17], v[200:207], v[82:85]
	v_mfma_f32_16x16x128_f8f6f4 v[78:81], v[2:9], v[208:215], v[78:81]
	v_mfma_f32_16x16x128_f8f6f4 v[74:77], v[10:17], v[208:215], v[74:77]
	v_mfma_f32_16x16x128_f8f6f4 v[70:73], v[2:9], v[216:223], v[70:73]
	v_mfma_f32_16x16x128_f8f6f4 v[66:69], v[10:17], v[216:223], v[66:69]
	s_setprio 0
	s_setprio 1
	v_mfma_f32_16x16x128_f8f6f4 v[62:65], v[18:25], v[192:199], v[62:65]
	v_mfma_f32_16x16x128_f8f6f4 v[58:61], v[26:33], v[192:199], v[58:61]
	v_mfma_f32_16x16x128_f8f6f4 v[54:57], v[18:25], v[200:207], v[54:57]
	v_mfma_f32_16x16x128_f8f6f4 v[50:53], v[26:33], v[200:207], v[50:53]
	v_mfma_f32_16x16x128_f8f6f4 v[46:49], v[18:25], v[208:215], v[46:49]
	v_mfma_f32_16x16x128_f8f6f4 v[42:45], v[26:33], v[208:215], v[42:45]
	v_mfma_f32_16x16x128_f8f6f4 v[38:41], v[18:25], v[216:223], v[38:41]
	v_mfma_f32_16x16x128_f8f6f4 v[34:37], v[26:33], v[216:223], v[34:37]
	s_setprio 0
	s_barrier
	s_add_i32 s63, s63, 2
	s_add_u32 s22, s22, 0x100
	s_addc_u32 s23, s23, 0
	s_add_u32 s61, s61, 0x100
	s_addc_u32 s62, s62, 0
	s_cmp_gt_u32 s63, 25
.LBB0_2189:
	ds_read_b128 v[18:21], v189
	ds_read_b128 v[22:25], v189 offset:1024
	ds_read_b128 v[26:29], v189 offset:2048
	ds_read_b128 v[30:33], v189 offset:3072
	ds_read_b128 v[2:5], v190
	ds_read_b128 v[6:9], v190 offset:1024
	ds_read_b128 v[10:13], v190 offset:2048
	ds_read_b128 v[14:17], v190 offset:3072
	s_add_u32 s24, s22, 0xfff90080
	s_addc_u32 s25, s23, -1
	s_cmp_eq_u32 s63, 24
	s_cselect_b32 s27, s19, s25
	s_cselect_b32 s26, s18, s24
	s_cselect_b32 s25, s21, s62
	s_cselect_b32 s24, s20, s61
	s_add_i32 m0, s43, 0xc000
	ds_read_b128 v[178:181], v191
	ds_read_b128 v[182:185], v191 offset:1024
	ds_read_b128 v[192:195], v191 offset:2048
	ds_read_b128 v[196:199], v191 offset:3072
	ds_read_b128 v[200:203], v191 offset:4096
	ds_read_b128 v[204:207], v191 offset:5120
	ds_read_b128 v[208:211], v191 offset:6144
	ds_read_b128 v[212:215], v191 offset:7168
	global_load_lds_dwordx4 v172, s[22:23]
	s_add_i32 m0, s43, 0xe000
	s_nop 0
	global_load_lds_dwordx4 v174, s[22:23]
	s_waitcnt vmcnt(8)
	s_waitcnt lgkmcnt(0)
	s_barrier
	s_setprio 1
	s_waitcnt lgkmcnt(0)
	v_mfma_f32_16x16x128_f8f6f4 v[158:161], v[18:25], v[178:185], v[158:161]
	v_mfma_f32_16x16x128_f8f6f4 v[154:157], v[26:33], v[178:185], v[154:157]
	v_mfma_f32_16x16x128_f8f6f4 v[150:153], v[18:25], v[192:199], v[150:153]
	v_mfma_f32_16x16x128_f8f6f4 v[146:149], v[26:33], v[192:199], v[146:149]
	v_mfma_f32_16x16x128_f8f6f4 v[142:145], v[18:25], v[200:207], v[142:145]
	v_mfma_f32_16x16x128_f8f6f4 v[138:141], v[26:33], v[200:207], v[138:141]
	v_mfma_f32_16x16x128_f8f6f4 v[134:137], v[18:25], v[208:215], v[134:137]
	v_mfma_f32_16x16x128_f8f6f4 v[130:133], v[26:33], v[208:215], v[130:133]
	s_setprio 0
	s_setprio 1
	v_mfma_f32_16x16x128_f8f6f4 v[126:129], v[2:9], v[178:185], v[126:129]
	v_mfma_f32_16x16x128_f8f6f4 v[122:125], v[10:17], v[178:185], v[122:125]
	v_mfma_f32_16x16x128_f8f6f4 v[118:121], v[2:9], v[192:199], v[118:121]
	v_mfma_f32_16x16x128_f8f6f4 v[114:117], v[10:17], v[192:199], v[114:117]
	v_mfma_f32_16x16x128_f8f6f4 v[110:113], v[2:9], v[200:207], v[110:113]
	v_mfma_f32_16x16x128_f8f6f4 v[106:109], v[10:17], v[200:207], v[106:109]
	v_mfma_f32_16x16x128_f8f6f4 v[102:105], v[2:9], v[208:215], v[102:105]
	v_mfma_f32_16x16x128_f8f6f4 v[98:101], v[10:17], v[208:215], v[98:101]
	s_setprio 0
	s_barrier
	s_add_i32 s64, s7, s42
	s_mov_b64 s[98:99], s[24:25]
	s_mov_b32 m0, s64
	ds_read_b128 v[192:195], v191 offset:16384
	ds_read_b128 v[196:199], v191 offset:17408
	ds_read_b128 v[200:203], v191 offset:18432
	ds_read_b128 v[204:207], v191 offset:19456
	ds_read_b128 v[208:211], v191 offset:20480
	ds_read_b128 v[212:215], v191 offset:21504
	ds_read_b128 v[216:219], v191 offset:22528
	ds_read_b128 v[220:223], v191 offset:23552
	global_load_lds_dwordx4 v164, s[98:99]
	s_add_i32 m0, s64, 0x2000
	s_add_u32 s64, s24, 0x70000
	s_addc_u32 s65, s25, 0
	s_add_i32 s66, s51, s42
	global_load_lds_dwordx4 v168, s[98:99]
	s_mov_b32 m0, s66
	s_mov_b64 s[100:101], s[26:27]
	global_load_lds_dwordx4 v164, s[64:65]
	s_add_i32 m0, s66, 0x2000
	s_nop 0
	global_load_lds_dwordx4 v168, s[64:65]
	s_mov_b32 m0, s43
	s_nop 0
	global_load_lds_dwordx4 v162, s[100:101]
	s_mov_b32 m0, s44
	s_nop 0
	global_load_lds_dwordx4 v166, s[100:101]
	s_waitcnt vmcnt(8)
	s_waitcnt lgkmcnt(0)
	s_barrier
	s_setprio 1
	s_waitcnt lgkmcnt(0)
	v_mfma_f32_16x16x128_f8f6f4 v[94:97], v[18:25], v[192:199], v[94:97]
	v_mfma_f32_16x16x128_f8f6f4 v[90:93], v[26:33], v[192:199], v[90:93]
	v_mfma_f32_16x16x128_f8f6f4 v[86:89], v[18:25], v[200:207], v[86:89]
	v_mfma_f32_16x16x128_f8f6f4 v[82:85], v[26:33], v[200:207], v[82:85]
	v_mfma_f32_16x16x128_f8f6f4 v[78:81], v[18:25], v[208:215], v[78:81]
	v_mfma_f32_16x16x128_f8f6f4 v[74:77], v[26:33], v[208:215], v[74:77]
	v_mfma_f32_16x16x128_f8f6f4 v[70:73], v[18:25], v[216:223], v[70:73]
	v_mfma_f32_16x16x128_f8f6f4 v[66:69], v[26:33], v[216:223], v[66:69]
	s_setprio 0
	s_setprio 1
	v_mfma_f32_16x16x128_f8f6f4 v[62:65], v[2:9], v[192:199], v[62:65]
	v_mfma_f32_16x16x128_f8f6f4 v[58:61], v[10:17], v[192:199], v[58:61]
	v_mfma_f32_16x16x128_f8f6f4 v[54:57], v[2:9], v[200:207], v[54:57]
	v_mfma_f32_16x16x128_f8f6f4 v[50:53], v[10:17], v[200:207], v[50:53]
	v_mfma_f32_16x16x128_f8f6f4 v[46:49], v[2:9], v[208:215], v[46:49]
	v_mfma_f32_16x16x128_f8f6f4 v[42:45], v[10:17], v[208:215], v[42:45]
	v_mfma_f32_16x16x128_f8f6f4 v[38:41], v[2:9], v[216:223], v[38:41]
	v_mfma_f32_16x16x128_f8f6f4 v[34:37], v[10:17], v[216:223], v[34:37]
	s_setprio 0
	s_barrier
	s_add_i32 s64, 0, 0x18000
	s_add_i32 s65, 0, 0x1c000
	v_add_u32_e32 v14, s64, v186
	v_add_u32_e32 v30, s65, v186
	ds_read_b128 v[2:5], v14
	ds_read_b128 v[6:9], v14 offset:1024
	ds_read_b128 v[10:13], v14 offset:2048
	ds_read_b128 v[14:17], v14 offset:3072
	ds_read_b128 v[18:21], v30
	ds_read_b128 v[22:25], v30 offset:1024
	ds_read_b128 v[26:29], v30 offset:2048
	ds_read_b128 v[30:33], v30 offset:3072
	s_add_u32 s26, s26, 0x70000
	s_addc_u32 s27, s27, 0
	s_mov_b32 m0, s45
	ds_read_b128 v[192:195], v191 offset:32768
	ds_read_b128 v[196:199], v191 offset:33792
	ds_read_b128 v[200:203], v191 offset:34816
	ds_read_b128 v[204:207], v191 offset:35840
	ds_read_b128 v[208:211], v191 offset:36864
	ds_read_b128 v[212:215], v191 offset:37888
	ds_read_b128 v[216:219], v191 offset:38912
	ds_read_b128 v[220:223], v191 offset:39936
	global_load_lds_dwordx4 v162, s[26:27]
	s_mov_b32 m0, s46
	s_nop 0
	global_load_lds_dwordx4 v166, s[26:27]
	s_waitcnt vmcnt(8)
	s_waitcnt lgkmcnt(0)
	s_barrier
	s_setprio 1
	s_waitcnt lgkmcnt(0)
	v_mfma_f32_16x16x128_f8f6f4 v[158:161], v[2:9], v[192:199], v[158:161]
	v_mfma_f32_16x16x128_f8f6f4 v[154:157], v[10:17], v[192:199], v[154:157]
	v_mfma_f32_16x16x128_f8f6f4 v[150:153], v[2:9], v[200:207], v[150:153]
	v_mfma_f32_16x16x128_f8f6f4 v[146:149], v[10:17], v[200:207], v[146:149]
	v_mfma_f32_16x16x128_f8f6f4 v[142:145], v[2:9], v[208:215], v[142:145]
	v_mfma_f32_16x16x128_f8f6f4 v[138:141], v[10:17], v[208:215], v[138:141]
	v_mfma_f32_16x16x128_f8f6f4 v[134:137], v[2:9], v[216:223], v[134:137]
	v_mfma_f32_16x16x128_f8f6f4 v[130:133], v[10:17], v[216:223], v[130:133]
	s_setprio 0
	s_setprio 1
	v_mfma_f32_16x16x128_f8f6f4 v[126:129], v[18:25], v[192:199], v[126:129]
	v_mfma_f32_16x16x128_f8f6f4 v[122:125], v[26:33], v[192:199], v[122:125]
	v_mfma_f32_16x16x128_f8f6f4 v[118:121], v[18:25], v[200:207], v[118:121]
	v_mfma_f32_16x16x128_f8f6f4 v[114:117], v[26:33], v[200:207], v[114:117]
	v_mfma_f32_16x16x128_f8f6f4 v[110:113], v[18:25], v[208:215], v[110:113]
	v_mfma_f32_16x16x128_f8f6f4 v[106:109], v[26:33], v[208:215], v[106:109]
	v_mfma_f32_16x16x128_f8f6f4 v[102:105], v[18:25], v[216:223], v[102:105]
	v_mfma_f32_16x16x128_f8f6f4 v[98:101], v[26:33], v[216:223], v[98:101]
	s_setprio 0
	s_barrier
	s_add_i32 s26, s64, s42
	s_mov_b32 m0, s26
	ds_read_b128 v[192:195], v191 offset:49152
	ds_read_b128 v[196:199], v191 offset:50176
	ds_read_b128 v[200:203], v191 offset:51200
	ds_read_b128 v[204:207], v191 offset:52224
	ds_read_b128 v[208:211], v191 offset:53248
	ds_read_b128 v[212:215], v191 offset:54272
	ds_read_b128 v[216:219], v191 offset:55296
	ds_read_b128 v[220:223], v191 offset:56320
	s_add_u32 s98, s98, 0x80
	s_addc_u32 s99, s99, 0
	global_load_lds_dwordx4 v164, s[98:99]
	s_add_i32 m0, s26, 0x2000
	s_add_u32 s24, s24, 0x70080
	s_addc_u32 s25, s25, 0
	s_add_i32 s26, s65, s42
	global_load_lds_dwordx4 v168, s[98:99]
	s_mov_b32 m0, s26
	s_nop 0
	global_load_lds_dwordx4 v164, s[24:25]
	s_add_i32 m0, s26, 0x2000
	s_nop 0
	global_load_lds_dwordx4 v168, s[24:25]
	s_mov_b32 m0, s48
	s_nop 0
	s_add_u32 s100, s100, 0x80
	s_addc_u32 s101, s101, 0
	global_load_lds_dwordx4 v162, s[100:101]
	s_mov_b32 m0, s49
	s_nop 0
	global_load_lds_dwordx4 v166, s[100:101]
	s_waitcnt vmcnt(8)
	s_waitcnt lgkmcnt(0)
	s_barrier
	s_setprio 1
	s_waitcnt lgkmcnt(0)
	v_mfma_f32_16x16x128_f8f6f4 v[94:97], v[2:9], v[192:199], v[94:97]
	v_mfma_f32_16x16x128_f8f6f4 v[90:93], v[10:17], v[192:199], v[90:93]
	v_mfma_f32_16x16x128_f8f6f4 v[86:89], v[2:9], v[200:207], v[86:89]
	v_mfma_f32_16x16x128_f8f6f4 v[82:85], v[10:17], v[200:207], v[82:85]
	v_mfma_f32_16x16x128_f8f6f4 v[78:81], v[2:9], v[208:215], v[78:81]
	v_mfma_f32_16x16x128_f8f6f4 v[74:77], v[10:17], v[208:215], v[74:77]
	v_mfma_f32_16x16x128_f8f6f4 v[70:73], v[2:9], v[216:223], v[70:73]
	v_mfma_f32_16x16x128_f8f6f4 v[66:69], v[10:17], v[216:223], v[66:69]
	s_setprio 0
	s_setprio 1
	v_mfma_f32_16x16x128_f8f6f4 v[62:65], v[18:25], v[192:199], v[62:65]
	v_mfma_f32_16x16x128_f8f6f4 v[58:61], v[26:33], v[192:199], v[58:61]
	v_mfma_f32_16x16x128_f8f6f4 v[54:57], v[18:25], v[200:207], v[54:57]
	v_mfma_f32_16x16x128_f8f6f4 v[50:53], v[26:33], v[200:207], v[50:53]
	v_mfma_f32_16x16x128_f8f6f4 v[46:49], v[18:25], v[208:215], v[46:49]
	v_mfma_f32_16x16x128_f8f6f4 v[42:45], v[26:33], v[208:215], v[42:45]
	v_mfma_f32_16x16x128_f8f6f4 v[38:41], v[18:25], v[216:223], v[38:41]
	v_mfma_f32_16x16x128_f8f6f4 v[34:37], v[26:33], v[216:223], v[34:37]
	s_setprio 0
	s_barrier
	s_add_i32 s63, s63, 2
	s_add_u32 s22, s22, 0x100
	s_addc_u32 s23, s23, 0
	s_add_u32 s61, s61, 0x100
	s_addc_u32 s62, s62, 0
	s_cmp_gt_u32 s63, 25
	s_cbranch_scc0 .LBB0_2189
	s_and_b64 vcc, exec, s[14:15]
	s_cbranch_vccz .LBB0_2192
	s_barrier
